# v8 with the per-segment s_setprio toggles of the GEMM K-loops removed
# speedup vs baseline: 1.0010x; 1.0010x over previous
.LBB0_253:
	s_waitcnt lgkmcnt(0)
	s_barrier
	s_waitcnt lgkmcnt(0)
	v_mfma_f32_16x16x32_bf16 v[62:65], v[146:149], v[186:189], v[62:65]
	v_mfma_f32_16x16x32_bf16 v[58:61], v[154:157], v[186:189], v[58:61]
	v_mfma_f32_16x16x32_bf16 v[54:57], v[146:149], v[178:181], v[54:57]
	v_mfma_f32_16x16x32_bf16 v[46:49], v[154:157], v[178:181], v[46:49]
	v_mfma_f32_16x16x32_bf16 v[38:41], v[146:149], v[170:173], v[38:41]
	v_mfma_f32_16x16x32_bf16 v[30:33], v[154:157], v[170:173], v[30:33]
	v_mfma_f32_16x16x32_bf16 v[22:25], v[146:149], v[162:165], v[22:25]
	v_mfma_f32_16x16x32_bf16 v[14:17], v[154:157], v[162:165], v[14:17]
	v_mfma_f32_16x16x32_bf16 v[62:65], v[150:153], v[190:193], v[62:65]
	v_mfma_f32_16x16x32_bf16 v[58:61], v[158:161], v[190:193], v[58:61]
	v_mfma_f32_16x16x32_bf16 v[54:57], v[150:153], v[182:185], v[54:57]
	v_mfma_f32_16x16x32_bf16 v[46:49], v[158:161], v[182:185], v[46:49]
	v_mfma_f32_16x16x32_bf16 v[38:41], v[150:153], v[174:177], v[38:41]
	v_mfma_f32_16x16x32_bf16 v[30:33], v[158:161], v[174:177], v[30:33]
	v_mfma_f32_16x16x32_bf16 v[22:25], v[150:153], v[166:169], v[22:25]
	v_mfma_f32_16x16x32_bf16 v[14:17], v[158:161], v[166:169], v[14:17]
	v_mfma_f32_16x16x32_bf16 v[50:53], v[130:133], v[186:189], v[50:53]
	v_mfma_f32_16x16x32_bf16 v[42:45], v[138:141], v[186:189], v[42:45]
	v_mfma_f32_16x16x32_bf16 v[34:37], v[130:133], v[178:181], v[34:37]
	v_mfma_f32_16x16x32_bf16 v[26:29], v[138:141], v[178:181], v[26:29]
	v_mfma_f32_16x16x32_bf16 v[18:21], v[130:133], v[170:173], v[18:21]
	v_mfma_f32_16x16x32_bf16 v[10:13], v[138:141], v[170:173], v[10:13]
	v_mfma_f32_16x16x32_bf16 v[6:9], v[130:133], v[162:165], v[6:9]
	v_mfma_f32_16x16x32_bf16 v[2:5], v[138:141], v[162:165], v[2:5]
	v_mfma_f32_16x16x32_bf16 v[50:53], v[134:137], v[190:193], v[50:53]
	v_mfma_f32_16x16x32_bf16 v[42:45], v[142:145], v[190:193], v[42:45]
	v_mfma_f32_16x16x32_bf16 v[34:37], v[134:137], v[182:185], v[34:37]
	v_mfma_f32_16x16x32_bf16 v[26:29], v[142:145], v[182:185], v[26:29]
	v_mfma_f32_16x16x32_bf16 v[18:21], v[134:137], v[174:177], v[18:21]
	v_mfma_f32_16x16x32_bf16 v[10:13], v[142:145], v[174:177], v[10:13]
	v_mfma_f32_16x16x32_bf16 v[6:9], v[134:137], v[166:169], v[6:9]
	v_mfma_f32_16x16x32_bf16 v[2:5], v[142:145], v[166:169], v[2:5]
	s_barrier
	s_add_i32 s34, 0, 0x18000
	s_add_i32 s35, 0, 0x1c000
	v_add_u32_e32 v142, s34, v243
	v_add_u32_e32 v158, s35, v243
	ds_read_b128 v[130:133], v142
	ds_read_b128 v[134:137], v142 offset:1024
	ds_read_b128 v[138:141], v142 offset:2048
	ds_read_b128 v[142:145], v142 offset:3072
	ds_read_b128 v[146:149], v158
	ds_read_b128 v[150:153], v158 offset:1024
	ds_read_b128 v[154:157], v158 offset:2048
	ds_read_b128 v[158:161], v158 offset:3072
	s_add_u32 s30, s30, 0x80000
	s_addc_u32 s31, s31, 0
	s_mov_b32 m0, s46
	v_lshl_add_u64 v[250:251], s[30:31], 0, v[200:201]
	ds_read_b128 v[162:165], v246 offset:32768
	ds_read_b128 v[166:169], v246 offset:33792
	ds_read_b128 v[170:173], v246 offset:34816
	ds_read_b128 v[174:177], v246 offset:35840
	ds_read_b128 v[178:181], v246 offset:36864
	ds_read_b128 v[182:185], v246 offset:37888
	ds_read_b128 v[186:189], v246 offset:38912
	ds_read_b128 v[190:193], v246 offset:39936
	global_load_lds_dwordx4 v[250:251], off
	v_lshl_add_u64 v[250:251], s[30:31], 0, v[204:205]
	s_mov_b32 m0, s47
	s_nop 0
	global_load_lds_dwordx4 v[250:251], off
	s_waitcnt vmcnt(8)
	s_waitcnt lgkmcnt(0)
	s_barrier
	s_waitcnt lgkmcnt(0)
	v_mfma_f32_16x16x32_bf16 v[126:129], v[130:133], v[162:165], v[126:129]
	v_mfma_f32_16x16x32_bf16 v[122:125], v[138:141], v[162:165], v[122:125]
	v_mfma_f32_16x16x32_bf16 v[118:121], v[130:133], v[170:173], v[118:121]
	v_mfma_f32_16x16x32_bf16 v[110:113], v[138:141], v[170:173], v[110:113]
	v_mfma_f32_16x16x32_bf16 v[102:105], v[130:133], v[178:181], v[102:105]
	v_mfma_f32_16x16x32_bf16 v[94:97], v[138:141], v[178:181], v[94:97]
	v_mfma_f32_16x16x32_bf16 v[86:89], v[130:133], v[186:189], v[86:89]
	v_mfma_f32_16x16x32_bf16 v[78:81], v[138:141], v[186:189], v[78:81]
	v_mfma_f32_16x16x32_bf16 v[126:129], v[134:137], v[166:169], v[126:129]
	v_mfma_f32_16x16x32_bf16 v[122:125], v[142:145], v[166:169], v[122:125]
	v_mfma_f32_16x16x32_bf16 v[118:121], v[134:137], v[174:177], v[118:121]
	v_mfma_f32_16x16x32_bf16 v[110:113], v[142:145], v[174:177], v[110:113]
	v_mfma_f32_16x16x32_bf16 v[102:105], v[134:137], v[182:185], v[102:105]
	v_mfma_f32_16x16x32_bf16 v[94:97], v[142:145], v[182:185], v[94:97]
	v_mfma_f32_16x16x32_bf16 v[86:89], v[134:137], v[190:193], v[86:89]
	v_mfma_f32_16x16x32_bf16 v[78:81], v[142:145], v[190:193], v[78:81]
	v_mfma_f32_16x16x32_bf16 v[114:117], v[146:149], v[162:165], v[114:117]
	v_mfma_f32_16x16x32_bf16 v[106:109], v[154:157], v[162:165], v[106:109]
	v_mfma_f32_16x16x32_bf16 v[98:101], v[146:149], v[170:173], v[98:101]
	v_mfma_f32_16x16x32_bf16 v[90:93], v[154:157], v[170:173], v[90:93]
	v_mfma_f32_16x16x32_bf16 v[82:85], v[146:149], v[178:181], v[82:85]
	v_mfma_f32_16x16x32_bf16 v[74:77], v[154:157], v[178:181], v[74:77]
	v_mfma_f32_16x16x32_bf16 v[70:73], v[146:149], v[186:189], v[70:73]
	v_mfma_f32_16x16x32_bf16 v[66:69], v[154:157], v[186:189], v[66:69]
	v_mfma_f32_16x16x32_bf16 v[114:117], v[150:153], v[166:169], v[114:117]
	v_mfma_f32_16x16x32_bf16 v[106:109], v[158:161], v[166:169], v[106:109]
	v_mfma_f32_16x16x32_bf16 v[98:101], v[150:153], v[174:177], v[98:101]
	v_mfma_f32_16x16x32_bf16 v[90:93], v[158:161], v[174:177], v[90:93]
	v_mfma_f32_16x16x32_bf16 v[82:85], v[150:153], v[182:185], v[82:85]
	v_mfma_f32_16x16x32_bf16 v[74:77], v[158:161], v[182:185], v[74:77]
	v_mfma_f32_16x16x32_bf16 v[70:73], v[150:153], v[190:193], v[70:73]
	v_mfma_f32_16x16x32_bf16 v[66:69], v[158:161], v[190:193], v[66:69]
	s_barrier
	s_add_i32 s30, s34, s40
	v_lshl_add_u64 v[232:233], v[232:233], 0, s[4:5]
	s_mov_b32 m0, s30
	ds_read_b128 v[162:165], v246 offset:49152
	ds_read_b128 v[166:169], v246 offset:50176
	ds_read_b128 v[170:173], v246 offset:51200
	ds_read_b128 v[174:177], v246 offset:52224
	ds_read_b128 v[178:181], v246 offset:53248
	ds_read_b128 v[182:185], v246 offset:54272
	ds_read_b128 v[186:189], v246 offset:55296
	ds_read_b128 v[190:193], v246 offset:56320
	global_load_lds_dwordx4 v[232:233], off
	s_add_i32 m0, s30, 0x2000
	s_add_u32 s28, s28, 0x80080
	v_lshl_add_u64 v[230:231], v[230:231], 0, s[4:5]
	s_addc_u32 s29, s29, 0
	s_add_i32 s30, s35, s40
	global_load_lds_dwordx4 v[230:231], off
	v_lshl_add_u64 v[230:231], s[28:29], 0, v[202:203]
	s_mov_b32 m0, s30
	v_lshl_add_u64 v[226:227], v[226:227], 0, s[4:5]
	global_load_lds_dwordx4 v[230:231], off
	v_lshl_add_u64 v[230:231], s[28:29], 0, v[206:207]
	s_add_i32 m0, s30, 0x2000
	s_nop 0
	global_load_lds_dwordx4 v[230:231], off
	s_mov_b32 m0, s49
	s_nop 0
	global_load_lds_dwordx4 v[226:227], off
	v_lshl_add_u64 v[226:227], v[228:229], 0, s[4:5]
	s_mov_b32 m0, s50
	s_nop 0
	global_load_lds_dwordx4 v[226:227], off
	s_waitcnt vmcnt(8)
	s_waitcnt lgkmcnt(0)
	s_barrier
	s_waitcnt lgkmcnt(0)
	v_mfma_f32_16x16x32_bf16 v[62:65], v[130:133], v[162:165], v[62:65]
	v_mfma_f32_16x16x32_bf16 v[58:61], v[138:141], v[162:165], v[58:61]
	v_mfma_f32_16x16x32_bf16 v[54:57], v[130:133], v[170:173], v[54:57]
	v_mfma_f32_16x16x32_bf16 v[46:49], v[138:141], v[170:173], v[46:49]
	v_mfma_f32_16x16x32_bf16 v[38:41], v[130:133], v[178:181], v[38:41]
	v_mfma_f32_16x16x32_bf16 v[30:33], v[138:141], v[178:181], v[30:33]
	v_mfma_f32_16x16x32_bf16 v[22:25], v[130:133], v[186:189], v[22:25]
	v_mfma_f32_16x16x32_bf16 v[14:17], v[138:141], v[186:189], v[14:17]
	v_mfma_f32_16x16x32_bf16 v[62:65], v[134:137], v[166:169], v[62:65]
	v_mfma_f32_16x16x32_bf16 v[58:61], v[142:145], v[166:169], v[58:61]
	v_mfma_f32_16x16x32_bf16 v[54:57], v[134:137], v[174:177], v[54:57]
	v_mfma_f32_16x16x32_bf16 v[46:49], v[142:145], v[174:177], v[46:49]
	v_mfma_f32_16x16x32_bf16 v[38:41], v[134:137], v[182:185], v[38:41]
	v_mfma_f32_16x16x32_bf16 v[30:33], v[142:145], v[182:185], v[30:33]
	v_mfma_f32_16x16x32_bf16 v[22:25], v[134:137], v[190:193], v[22:25]
	v_mfma_f32_16x16x32_bf16 v[14:17], v[142:145], v[190:193], v[14:17]
	v_mfma_f32_16x16x32_bf16 v[50:53], v[146:149], v[162:165], v[50:53]
	v_mfma_f32_16x16x32_bf16 v[42:45], v[154:157], v[162:165], v[42:45]
	v_mfma_f32_16x16x32_bf16 v[34:37], v[146:149], v[170:173], v[34:37]
	v_mfma_f32_16x16x32_bf16 v[26:29], v[154:157], v[170:173], v[26:29]
	v_mfma_f32_16x16x32_bf16 v[18:21], v[146:149], v[178:181], v[18:21]
	v_mfma_f32_16x16x32_bf16 v[10:13], v[154:157], v[178:181], v[10:13]
	v_mfma_f32_16x16x32_bf16 v[6:9], v[146:149], v[186:189], v[6:9]
	v_mfma_f32_16x16x32_bf16 v[2:5], v[154:157], v[186:189], v[2:5]
	v_mfma_f32_16x16x32_bf16 v[50:53], v[150:153], v[166:169], v[50:53]
	v_mfma_f32_16x16x32_bf16 v[42:45], v[158:161], v[166:169], v[42:45]
	v_mfma_f32_16x16x32_bf16 v[34:37], v[150:153], v[174:177], v[34:37]
	v_mfma_f32_16x16x32_bf16 v[26:29], v[158:161], v[174:177], v[26:29]
	v_mfma_f32_16x16x32_bf16 v[18:21], v[150:153], v[182:185], v[18:21]
	v_mfma_f32_16x16x32_bf16 v[10:13], v[158:161], v[182:185], v[10:13]
	v_mfma_f32_16x16x32_bf16 v[6:9], v[150:153], v[190:193], v[6:9]
	v_mfma_f32_16x16x32_bf16 v[2:5], v[158:161], v[190:193], v[2:5]
	s_barrier
	s_add_i32 s59, s59, 2
	s_add_u32 s24, s24, 0x100
	s_addc_u32 s25, s25, 0
	s_cmp_gt_u32 s59, 29
	s_cbranch_scc1 .LBB0_262

.LBB0_258:
	s_add_u32 s28, s22, s24
	s_addc_u32 s29, s23, s25
	s_add_u32 s28, s28, 0x100
	s_addc_u32 s29, s29, 0
	s_add_u32 s36, s57, s24
	s_addc_u32 s37, s58, s25
	s_waitcnt lgkmcnt(0)
	s_cmpk_eq_i32 s24, 0xf00
	s_cselect_b32 s31, s15, s29
	s_cselect_b32 s30, s55, s28
	s_cselect_b32 s29, s11, s37
	s_cselect_b32 s28, s56, s36
	s_barrier
	s_waitcnt lgkmcnt(0)
	v_mfma_f32_16x16x32_bf16 v[126:129], v[146:149], v[186:189], v[126:129]
	v_mfma_f32_16x16x32_bf16 v[122:125], v[154:157], v[186:189], v[122:125]
	v_mfma_f32_16x16x32_bf16 v[118:121], v[146:149], v[178:181], v[118:121]
	v_mfma_f32_16x16x32_bf16 v[110:113], v[154:157], v[178:181], v[110:113]
	v_mfma_f32_16x16x32_bf16 v[102:105], v[146:149], v[170:173], v[102:105]
	v_mfma_f32_16x16x32_bf16 v[94:97], v[154:157], v[170:173], v[94:97]
	v_mfma_f32_16x16x32_bf16 v[86:89], v[146:149], v[162:165], v[86:89]
	v_mfma_f32_16x16x32_bf16 v[78:81], v[154:157], v[162:165], v[78:81]
	v_mfma_f32_16x16x32_bf16 v[126:129], v[150:153], v[190:193], v[126:129]
	v_mfma_f32_16x16x32_bf16 v[122:125], v[158:161], v[190:193], v[122:125]
	v_mfma_f32_16x16x32_bf16 v[118:121], v[150:153], v[182:185], v[118:121]
	v_mfma_f32_16x16x32_bf16 v[110:113], v[158:161], v[182:185], v[110:113]
	v_mfma_f32_16x16x32_bf16 v[102:105], v[150:153], v[174:177], v[102:105]
	v_mfma_f32_16x16x32_bf16 v[94:97], v[158:161], v[174:177], v[94:97]
	v_mfma_f32_16x16x32_bf16 v[86:89], v[150:153], v[166:169], v[86:89]
	v_mfma_f32_16x16x32_bf16 v[78:81], v[158:161], v[166:169], v[78:81]
	v_mfma_f32_16x16x32_bf16 v[114:117], v[130:133], v[186:189], v[114:117]
	v_mfma_f32_16x16x32_bf16 v[106:109], v[138:141], v[186:189], v[106:109]
	v_mfma_f32_16x16x32_bf16 v[98:101], v[130:133], v[178:181], v[98:101]
	v_mfma_f32_16x16x32_bf16 v[90:93], v[138:141], v[178:181], v[90:93]
	v_mfma_f32_16x16x32_bf16 v[82:85], v[130:133], v[170:173], v[82:85]
	v_mfma_f32_16x16x32_bf16 v[74:77], v[138:141], v[170:173], v[74:77]
	v_mfma_f32_16x16x32_bf16 v[70:73], v[130:133], v[162:165], v[70:73]
	v_mfma_f32_16x16x32_bf16 v[66:69], v[138:141], v[162:165], v[66:69]
	v_mfma_f32_16x16x32_bf16 v[114:117], v[134:137], v[190:193], v[114:117]
	v_mfma_f32_16x16x32_bf16 v[106:109], v[142:145], v[190:193], v[106:109]
	v_mfma_f32_16x16x32_bf16 v[98:101], v[134:137], v[182:185], v[98:101]
	v_mfma_f32_16x16x32_bf16 v[90:93], v[142:145], v[182:185], v[90:93]
	v_mfma_f32_16x16x32_bf16 v[82:85], v[134:137], v[174:177], v[82:85]
	v_mfma_f32_16x16x32_bf16 v[74:77], v[142:145], v[174:177], v[74:77]
	v_mfma_f32_16x16x32_bf16 v[70:73], v[134:137], v[166:169], v[70:73]
	v_mfma_f32_16x16x32_bf16 v[66:69], v[142:145], v[166:169], v[66:69]
	s_barrier
	s_mov_b32 m0, s41
	v_lshl_add_u64 v[232:233], s[28:29], 0, v[202:203]
	s_add_u32 s36, s28, 0x80000
	ds_read_b128 v[186:189], v246 offset:16384
	ds_read_b128 v[190:193], v246 offset:17408
	ds_read_b128 v[178:181], v246 offset:18432
	ds_read_b128 v[182:185], v246 offset:19456
	ds_read_b128 v[170:173], v246 offset:20480
	ds_read_b128 v[174:177], v246 offset:21504
	ds_read_b128 v[162:165], v246 offset:22528
	ds_read_b128 v[166:169], v246 offset:23552
	global_load_lds_dwordx4 v[232:233], off
	v_lshl_add_u64 v[230:231], s[28:29], 0, v[206:207]
	s_mov_b32 m0, s42
	s_addc_u32 s37, s29, 0
	global_load_lds_dwordx4 v[230:231], off
	v_lshl_add_u64 v[226:227], s[36:37], 0, v[202:203]
	s_mov_b32 m0, s43
	v_lshl_add_u64 v[228:229], s[30:31], 0, v[204:205]
	global_load_lds_dwordx4 v[226:227], off
	v_lshl_add_u64 v[226:227], s[36:37], 0, v[206:207]
	s_mov_b32 m0, s44
	s_mov_b64 s[36:37], -1
	global_load_lds_dwordx4 v[226:227], off
	v_lshl_add_u64 v[226:227], s[30:31], 0, v[200:201]
	s_mov_b32 m0, s21
	s_and_b64 vcc, exec, s[34:35]
	global_load_lds_dwordx4 v[226:227], off
	s_mov_b32 m0, s45
	s_nop 0
	global_load_lds_dwordx4 v[228:229], off
	s_cbranch_vccz .LBB0_260
	s_waitcnt vmcnt(8)
	s_mov_b64 s[36:37], 0

.LBB0_285:
	s_waitcnt lgkmcnt(0)
	s_barrier
	s_waitcnt lgkmcnt(0)
	v_mfma_f32_16x16x32_bf16 v[62:65], v[146:149], v[186:189], v[62:65]
	v_mfma_f32_16x16x32_bf16 v[58:61], v[154:157], v[186:189], v[58:61]
	v_mfma_f32_16x16x32_bf16 v[46:49], v[146:149], v[178:181], v[46:49]
	v_mfma_f32_16x16x32_bf16 v[42:45], v[154:157], v[178:181], v[42:45]
	v_mfma_f32_16x16x32_bf16 v[30:33], v[146:149], v[170:173], v[30:33]
	v_mfma_f32_16x16x32_bf16 v[26:29], v[154:157], v[170:173], v[26:29]
	v_mfma_f32_16x16x32_bf16 v[14:17], v[146:149], v[162:165], v[14:17]
	v_mfma_f32_16x16x32_bf16 v[10:13], v[154:157], v[162:165], v[10:13]
	v_mfma_f32_16x16x32_bf16 v[62:65], v[150:153], v[190:193], v[62:65]
	v_mfma_f32_16x16x32_bf16 v[58:61], v[158:161], v[190:193], v[58:61]
	v_mfma_f32_16x16x32_bf16 v[46:49], v[150:153], v[182:185], v[46:49]
	v_mfma_f32_16x16x32_bf16 v[42:45], v[158:161], v[182:185], v[42:45]
	v_mfma_f32_16x16x32_bf16 v[30:33], v[150:153], v[174:177], v[30:33]
	v_mfma_f32_16x16x32_bf16 v[26:29], v[158:161], v[174:177], v[26:29]
	v_mfma_f32_16x16x32_bf16 v[14:17], v[150:153], v[166:169], v[14:17]
	v_mfma_f32_16x16x32_bf16 v[10:13], v[158:161], v[166:169], v[10:13]
	v_mfma_f32_16x16x32_bf16 v[54:57], v[130:133], v[186:189], v[54:57]
	v_mfma_f32_16x16x32_bf16 v[50:53], v[138:141], v[186:189], v[50:53]
	v_mfma_f32_16x16x32_bf16 v[38:41], v[130:133], v[178:181], v[38:41]
	v_mfma_f32_16x16x32_bf16 v[34:37], v[138:141], v[178:181], v[34:37]
	v_mfma_f32_16x16x32_bf16 v[22:25], v[130:133], v[170:173], v[22:25]
	v_mfma_f32_16x16x32_bf16 v[18:21], v[138:141], v[170:173], v[18:21]
	v_mfma_f32_16x16x32_bf16 v[6:9], v[130:133], v[162:165], v[6:9]
	v_mfma_f32_16x16x32_bf16 v[2:5], v[138:141], v[162:165], v[2:5]
	v_mfma_f32_16x16x32_bf16 v[54:57], v[134:137], v[190:193], v[54:57]
	v_mfma_f32_16x16x32_bf16 v[50:53], v[142:145], v[190:193], v[50:53]
	v_mfma_f32_16x16x32_bf16 v[38:41], v[134:137], v[182:185], v[38:41]
	v_mfma_f32_16x16x32_bf16 v[34:37], v[142:145], v[182:185], v[34:37]
	v_mfma_f32_16x16x32_bf16 v[22:25], v[134:137], v[174:177], v[22:25]
	v_mfma_f32_16x16x32_bf16 v[18:21], v[142:145], v[174:177], v[18:21]
	v_mfma_f32_16x16x32_bf16 v[6:9], v[134:137], v[166:169], v[6:9]
	v_mfma_f32_16x16x32_bf16 v[2:5], v[142:145], v[166:169], v[2:5]
	s_barrier
	s_add_i32 s34, 0, 0x18000
	s_add_i32 s35, 0, 0x1c000
	v_add_u32_e32 v142, s34, v244
	v_add_u32_e32 v158, s35, v244
	ds_read_b128 v[130:133], v142
	ds_read_b128 v[134:137], v142 offset:1024
	ds_read_b128 v[138:141], v142 offset:2048
	ds_read_b128 v[142:145], v142 offset:3072
	ds_read_b128 v[146:149], v158
	ds_read_b128 v[150:153], v158 offset:1024
	ds_read_b128 v[154:157], v158 offset:2048
	ds_read_b128 v[158:161], v158 offset:3072
	s_add_u32 s30, s30, 0x80000
	s_addc_u32 s31, s31, 0
	s_mov_b32 m0, s46
	v_lshl_add_u64 v[250:251], s[30:31], 0, v[200:201]
	ds_read_b128 v[162:165], v247 offset:32768
	ds_read_b128 v[166:169], v247 offset:33792
	ds_read_b128 v[170:173], v247 offset:34816
	ds_read_b128 v[174:177], v247 offset:35840
	ds_read_b128 v[178:181], v247 offset:36864
	ds_read_b128 v[182:185], v247 offset:37888
	ds_read_b128 v[186:189], v247 offset:38912
	ds_read_b128 v[190:193], v247 offset:39936
	global_load_lds_dwordx4 v[250:251], off
	v_lshl_add_u64 v[250:251], s[30:31], 0, v[204:205]
	s_mov_b32 m0, s47
	s_nop 0
	global_load_lds_dwordx4 v[250:251], off
	s_waitcnt vmcnt(8)
	s_waitcnt lgkmcnt(0)
	s_barrier
	s_waitcnt lgkmcnt(0)
	v_mfma_f32_16x16x32_bf16 v[126:129], v[130:133], v[162:165], v[126:129]
	v_mfma_f32_16x16x32_bf16 v[122:125], v[138:141], v[162:165], v[122:125]
	v_mfma_f32_16x16x32_bf16 v[110:113], v[130:133], v[170:173], v[110:113]
	v_mfma_f32_16x16x32_bf16 v[106:109], v[138:141], v[170:173], v[106:109]
	v_mfma_f32_16x16x32_bf16 v[94:97], v[130:133], v[178:181], v[94:97]
	v_mfma_f32_16x16x32_bf16 v[90:93], v[138:141], v[178:181], v[90:93]
	v_mfma_f32_16x16x32_bf16 v[78:81], v[130:133], v[186:189], v[78:81]
	v_mfma_f32_16x16x32_bf16 v[74:77], v[138:141], v[186:189], v[74:77]
	v_mfma_f32_16x16x32_bf16 v[126:129], v[134:137], v[166:169], v[126:129]
	v_mfma_f32_16x16x32_bf16 v[122:125], v[142:145], v[166:169], v[122:125]
	v_mfma_f32_16x16x32_bf16 v[110:113], v[134:137], v[174:177], v[110:113]
	v_mfma_f32_16x16x32_bf16 v[106:109], v[142:145], v[174:177], v[106:109]
	v_mfma_f32_16x16x32_bf16 v[94:97], v[134:137], v[182:185], v[94:97]
	v_mfma_f32_16x16x32_bf16 v[90:93], v[142:145], v[182:185], v[90:93]
	v_mfma_f32_16x16x32_bf16 v[78:81], v[134:137], v[190:193], v[78:81]
	v_mfma_f32_16x16x32_bf16 v[74:77], v[142:145], v[190:193], v[74:77]
	v_mfma_f32_16x16x32_bf16 v[118:121], v[146:149], v[162:165], v[118:121]
	v_mfma_f32_16x16x32_bf16 v[114:117], v[154:157], v[162:165], v[114:117]
	v_mfma_f32_16x16x32_bf16 v[102:105], v[146:149], v[170:173], v[102:105]
	v_mfma_f32_16x16x32_bf16 v[98:101], v[154:157], v[170:173], v[98:101]
	v_mfma_f32_16x16x32_bf16 v[86:89], v[146:149], v[178:181], v[86:89]
	v_mfma_f32_16x16x32_bf16 v[82:85], v[154:157], v[178:181], v[82:85]
	v_mfma_f32_16x16x32_bf16 v[70:73], v[146:149], v[186:189], v[70:73]
	v_mfma_f32_16x16x32_bf16 v[66:69], v[154:157], v[186:189], v[66:69]
	v_mfma_f32_16x16x32_bf16 v[118:121], v[150:153], v[166:169], v[118:121]
	v_mfma_f32_16x16x32_bf16 v[114:117], v[158:161], v[166:169], v[114:117]
	v_mfma_f32_16x16x32_bf16 v[102:105], v[150:153], v[174:177], v[102:105]
	v_mfma_f32_16x16x32_bf16 v[98:101], v[158:161], v[174:177], v[98:101]
	v_mfma_f32_16x16x32_bf16 v[86:89], v[150:153], v[182:185], v[86:89]
	v_mfma_f32_16x16x32_bf16 v[82:85], v[158:161], v[182:185], v[82:85]
	v_mfma_f32_16x16x32_bf16 v[70:73], v[150:153], v[190:193], v[70:73]
	v_mfma_f32_16x16x32_bf16 v[66:69], v[158:161], v[190:193], v[66:69]
	s_barrier
	s_add_i32 s30, s34, s40
	v_lshl_add_u64 v[232:233], v[232:233], 0, s[4:5]
	s_mov_b32 m0, s30
	ds_read_b128 v[162:165], v247 offset:49152
	ds_read_b128 v[166:169], v247 offset:50176
	ds_read_b128 v[170:173], v247 offset:51200
	ds_read_b128 v[174:177], v247 offset:52224
	ds_read_b128 v[178:181], v247 offset:53248
	ds_read_b128 v[182:185], v247 offset:54272
	ds_read_b128 v[186:189], v247 offset:55296
	ds_read_b128 v[190:193], v247 offset:56320
	global_load_lds_dwordx4 v[232:233], off
	s_add_i32 m0, s30, 0x2000
	s_add_u32 s28, s28, 0x80080
	v_lshl_add_u64 v[230:231], v[230:231], 0, s[4:5]
	s_addc_u32 s29, s29, 0
	s_add_i32 s30, s35, s40
	global_load_lds_dwordx4 v[230:231], off
	v_lshl_add_u64 v[230:231], s[28:29], 0, v[202:203]
	s_mov_b32 m0, s30
	v_lshl_add_u64 v[226:227], v[226:227], 0, s[4:5]
	global_load_lds_dwordx4 v[230:231], off
	v_lshl_add_u64 v[230:231], s[28:29], 0, v[206:207]
	s_add_i32 m0, s30, 0x2000
	s_nop 0
	global_load_lds_dwordx4 v[230:231], off
	s_mov_b32 m0, s48
	s_nop 0
	global_load_lds_dwordx4 v[226:227], off
	v_lshl_add_u64 v[226:227], v[228:229], 0, s[4:5]
	s_mov_b32 m0, s49
	s_nop 0
	global_load_lds_dwordx4 v[226:227], off
	s_waitcnt vmcnt(8)
	s_waitcnt lgkmcnt(0)
	s_barrier
	s_waitcnt lgkmcnt(0)
	v_mfma_f32_16x16x32_bf16 v[62:65], v[130:133], v[162:165], v[62:65]
	v_mfma_f32_16x16x32_bf16 v[58:61], v[138:141], v[162:165], v[58:61]
	v_mfma_f32_16x16x32_bf16 v[46:49], v[130:133], v[170:173], v[46:49]
	v_mfma_f32_16x16x32_bf16 v[42:45], v[138:141], v[170:173], v[42:45]
	v_mfma_f32_16x16x32_bf16 v[30:33], v[130:133], v[178:181], v[30:33]
	v_mfma_f32_16x16x32_bf16 v[26:29], v[138:141], v[178:181], v[26:29]
	v_mfma_f32_16x16x32_bf16 v[14:17], v[130:133], v[186:189], v[14:17]
	v_mfma_f32_16x16x32_bf16 v[10:13], v[138:141], v[186:189], v[10:13]
	v_mfma_f32_16x16x32_bf16 v[62:65], v[134:137], v[166:169], v[62:65]
	v_mfma_f32_16x16x32_bf16 v[58:61], v[142:145], v[166:169], v[58:61]
	v_mfma_f32_16x16x32_bf16 v[46:49], v[134:137], v[174:177], v[46:49]
	v_mfma_f32_16x16x32_bf16 v[42:45], v[142:145], v[174:177], v[42:45]
	v_mfma_f32_16x16x32_bf16 v[30:33], v[134:137], v[182:185], v[30:33]
	v_mfma_f32_16x16x32_bf16 v[26:29], v[142:145], v[182:185], v[26:29]
	v_mfma_f32_16x16x32_bf16 v[14:17], v[134:137], v[190:193], v[14:17]
	v_mfma_f32_16x16x32_bf16 v[10:13], v[142:145], v[190:193], v[10:13]
	v_mfma_f32_16x16x32_bf16 v[54:57], v[146:149], v[162:165], v[54:57]
	v_mfma_f32_16x16x32_bf16 v[50:53], v[154:157], v[162:165], v[50:53]
	v_mfma_f32_16x16x32_bf16 v[38:41], v[146:149], v[170:173], v[38:41]
	v_mfma_f32_16x16x32_bf16 v[34:37], v[154:157], v[170:173], v[34:37]
	v_mfma_f32_16x16x32_bf16 v[22:25], v[146:149], v[178:181], v[22:25]
	v_mfma_f32_16x16x32_bf16 v[18:21], v[154:157], v[178:181], v[18:21]
	v_mfma_f32_16x16x32_bf16 v[6:9], v[146:149], v[186:189], v[6:9]
	v_mfma_f32_16x16x32_bf16 v[2:5], v[154:157], v[186:189], v[2:5]
	v_mfma_f32_16x16x32_bf16 v[54:57], v[150:153], v[166:169], v[54:57]
	v_mfma_f32_16x16x32_bf16 v[50:53], v[158:161], v[166:169], v[50:53]
	v_mfma_f32_16x16x32_bf16 v[38:41], v[150:153], v[174:177], v[38:41]
	v_mfma_f32_16x16x32_bf16 v[34:37], v[158:161], v[174:177], v[34:37]
	v_mfma_f32_16x16x32_bf16 v[22:25], v[150:153], v[182:185], v[22:25]
	v_mfma_f32_16x16x32_bf16 v[18:21], v[158:161], v[182:185], v[18:21]
	v_mfma_f32_16x16x32_bf16 v[6:9], v[150:153], v[190:193], v[6:9]
	v_mfma_f32_16x16x32_bf16 v[2:5], v[158:161], v[190:193], v[2:5]
	s_barrier
	s_add_i32 s59, s59, 2
	s_add_u32 s24, s24, 0x100
	s_addc_u32 s25, s25, 0
	s_cmp_gt_u32 s59, 29
	s_cbranch_scc1 .LBB0_294

.LBB0_290:
	s_add_u32 s28, s22, s24
	s_addc_u32 s29, s23, s25
	s_add_u32 s28, s28, 0x100
	s_addc_u32 s29, s29, 0
	s_add_u32 s36, s57, s24
	s_addc_u32 s37, s58, s25
	s_waitcnt lgkmcnt(0)
	s_cmpk_eq_i32 s24, 0xf00
	s_cselect_b32 s31, s15, s29
	s_cselect_b32 s30, s55, s28
	s_cselect_b32 s29, s11, s37
	s_cselect_b32 s28, s56, s36
	s_barrier
	s_waitcnt lgkmcnt(0)
	v_mfma_f32_16x16x32_bf16 v[126:129], v[146:149], v[186:189], v[126:129]
	v_mfma_f32_16x16x32_bf16 v[122:125], v[154:157], v[186:189], v[122:125]
	v_mfma_f32_16x16x32_bf16 v[110:113], v[146:149], v[178:181], v[110:113]
	v_mfma_f32_16x16x32_bf16 v[106:109], v[154:157], v[178:181], v[106:109]
	v_mfma_f32_16x16x32_bf16 v[94:97], v[146:149], v[170:173], v[94:97]
	v_mfma_f32_16x16x32_bf16 v[90:93], v[154:157], v[170:173], v[90:93]
	v_mfma_f32_16x16x32_bf16 v[78:81], v[146:149], v[162:165], v[78:81]
	v_mfma_f32_16x16x32_bf16 v[74:77], v[154:157], v[162:165], v[74:77]
	v_mfma_f32_16x16x32_bf16 v[126:129], v[150:153], v[190:193], v[126:129]
	v_mfma_f32_16x16x32_bf16 v[122:125], v[158:161], v[190:193], v[122:125]
	v_mfma_f32_16x16x32_bf16 v[110:113], v[150:153], v[182:185], v[110:113]
	v_mfma_f32_16x16x32_bf16 v[106:109], v[158:161], v[182:185], v[106:109]
	v_mfma_f32_16x16x32_bf16 v[94:97], v[150:153], v[174:177], v[94:97]
	v_mfma_f32_16x16x32_bf16 v[90:93], v[158:161], v[174:177], v[90:93]
	v_mfma_f32_16x16x32_bf16 v[78:81], v[150:153], v[166:169], v[78:81]
	v_mfma_f32_16x16x32_bf16 v[74:77], v[158:161], v[166:169], v[74:77]
	v_mfma_f32_16x16x32_bf16 v[118:121], v[130:133], v[186:189], v[118:121]
	v_mfma_f32_16x16x32_bf16 v[114:117], v[138:141], v[186:189], v[114:117]
	v_mfma_f32_16x16x32_bf16 v[102:105], v[130:133], v[178:181], v[102:105]
	v_mfma_f32_16x16x32_bf16 v[98:101], v[138:141], v[178:181], v[98:101]
	v_mfma_f32_16x16x32_bf16 v[86:89], v[130:133], v[170:173], v[86:89]
	v_mfma_f32_16x16x32_bf16 v[82:85], v[138:141], v[170:173], v[82:85]
	v_mfma_f32_16x16x32_bf16 v[70:73], v[130:133], v[162:165], v[70:73]
	v_mfma_f32_16x16x32_bf16 v[66:69], v[138:141], v[162:165], v[66:69]
	v_mfma_f32_16x16x32_bf16 v[118:121], v[134:137], v[190:193], v[118:121]
	v_mfma_f32_16x16x32_bf16 v[114:117], v[142:145], v[190:193], v[114:117]
	v_mfma_f32_16x16x32_bf16 v[102:105], v[134:137], v[182:185], v[102:105]
	v_mfma_f32_16x16x32_bf16 v[98:101], v[142:145], v[182:185], v[98:101]
	v_mfma_f32_16x16x32_bf16 v[86:89], v[134:137], v[174:177], v[86:89]
	v_mfma_f32_16x16x32_bf16 v[82:85], v[142:145], v[174:177], v[82:85]
	v_mfma_f32_16x16x32_bf16 v[70:73], v[134:137], v[166:169], v[70:73]
	v_mfma_f32_16x16x32_bf16 v[66:69], v[142:145], v[166:169], v[66:69]
	s_barrier
	s_mov_b32 m0, s41
	v_lshl_add_u64 v[232:233], s[28:29], 0, v[202:203]
	s_add_u32 s36, s28, 0x80000
	ds_read_b128 v[186:189], v247 offset:16384
	ds_read_b128 v[190:193], v247 offset:17408
	ds_read_b128 v[178:181], v247 offset:18432
	ds_read_b128 v[182:185], v247 offset:19456
	ds_read_b128 v[170:173], v247 offset:20480
	ds_read_b128 v[174:177], v247 offset:21504
	ds_read_b128 v[162:165], v247 offset:22528
	ds_read_b128 v[166:169], v247 offset:23552
	global_load_lds_dwordx4 v[232:233], off
	v_lshl_add_u64 v[230:231], s[28:29], 0, v[206:207]
	s_mov_b32 m0, s42
	s_addc_u32 s37, s29, 0
	global_load_lds_dwordx4 v[230:231], off
	v_lshl_add_u64 v[226:227], s[36:37], 0, v[202:203]
	s_mov_b32 m0, s43
	v_lshl_add_u64 v[228:229], s[30:31], 0, v[204:205]
	global_load_lds_dwordx4 v[226:227], off
	v_lshl_add_u64 v[226:227], s[36:37], 0, v[206:207]
	s_mov_b32 m0, s44
	s_mov_b64 s[36:37], -1
	global_load_lds_dwordx4 v[226:227], off
	v_lshl_add_u64 v[226:227], s[30:31], 0, v[200:201]
	s_mov_b32 m0, s21
	s_and_b64 vcc, exec, s[34:35]
	global_load_lds_dwordx4 v[226:227], off
	s_mov_b32 m0, s45
	s_nop 0
	global_load_lds_dwordx4 v[228:229], off
	s_cbranch_vccz .LBB0_292
	s_waitcnt vmcnt(8)
	s_mov_b64 s[36:37], 0

.LBB0_317:
	s_waitcnt lgkmcnt(0)
	s_barrier
	s_waitcnt lgkmcnt(0)
	v_mfma_f32_16x16x32_bf16 v[62:65], v[146:149], v[186:189], v[62:65]
	v_mfma_f32_16x16x32_bf16 v[58:61], v[154:157], v[186:189], v[58:61]
	v_mfma_f32_16x16x32_bf16 v[54:57], v[146:149], v[178:181], v[54:57]
	v_mfma_f32_16x16x32_bf16 v[46:49], v[154:157], v[178:181], v[46:49]
	v_mfma_f32_16x16x32_bf16 v[38:41], v[146:149], v[170:173], v[38:41]
	v_mfma_f32_16x16x32_bf16 v[30:33], v[154:157], v[170:173], v[30:33]
	v_mfma_f32_16x16x32_bf16 v[22:25], v[146:149], v[162:165], v[22:25]
	v_mfma_f32_16x16x32_bf16 v[14:17], v[154:157], v[162:165], v[14:17]
	v_mfma_f32_16x16x32_bf16 v[62:65], v[150:153], v[190:193], v[62:65]
	v_mfma_f32_16x16x32_bf16 v[58:61], v[158:161], v[190:193], v[58:61]
	v_mfma_f32_16x16x32_bf16 v[54:57], v[150:153], v[182:185], v[54:57]
	v_mfma_f32_16x16x32_bf16 v[46:49], v[158:161], v[182:185], v[46:49]
	v_mfma_f32_16x16x32_bf16 v[38:41], v[150:153], v[174:177], v[38:41]
	v_mfma_f32_16x16x32_bf16 v[30:33], v[158:161], v[174:177], v[30:33]
	v_mfma_f32_16x16x32_bf16 v[22:25], v[150:153], v[166:169], v[22:25]
	v_mfma_f32_16x16x32_bf16 v[14:17], v[158:161], v[166:169], v[14:17]
	v_mfma_f32_16x16x32_bf16 v[50:53], v[130:133], v[186:189], v[50:53]
	v_mfma_f32_16x16x32_bf16 v[42:45], v[138:141], v[186:189], v[42:45]
	v_mfma_f32_16x16x32_bf16 v[34:37], v[130:133], v[178:181], v[34:37]
	v_mfma_f32_16x16x32_bf16 v[26:29], v[138:141], v[178:181], v[26:29]
	v_mfma_f32_16x16x32_bf16 v[18:21], v[130:133], v[170:173], v[18:21]
	v_mfma_f32_16x16x32_bf16 v[10:13], v[138:141], v[170:173], v[10:13]
	v_mfma_f32_16x16x32_bf16 v[6:9], v[130:133], v[162:165], v[6:9]
	v_mfma_f32_16x16x32_bf16 v[2:5], v[138:141], v[162:165], v[2:5]
	v_mfma_f32_16x16x32_bf16 v[50:53], v[134:137], v[190:193], v[50:53]
	v_mfma_f32_16x16x32_bf16 v[42:45], v[142:145], v[190:193], v[42:45]
	v_mfma_f32_16x16x32_bf16 v[34:37], v[134:137], v[182:185], v[34:37]
	v_mfma_f32_16x16x32_bf16 v[26:29], v[142:145], v[182:185], v[26:29]
	v_mfma_f32_16x16x32_bf16 v[18:21], v[134:137], v[174:177], v[18:21]
	v_mfma_f32_16x16x32_bf16 v[10:13], v[142:145], v[174:177], v[10:13]
	v_mfma_f32_16x16x32_bf16 v[6:9], v[134:137], v[166:169], v[6:9]
	v_mfma_f32_16x16x32_bf16 v[2:5], v[142:145], v[166:169], v[2:5]
	s_barrier
	s_add_i32 s50, 0, 0x18000
	s_add_i32 s51, 0, 0x1c000
	v_add_u32_e32 v142, s50, v231
	v_add_u32_e32 v158, s51, v231
	ds_read_b128 v[130:133], v142
	ds_read_b128 v[134:137], v142 offset:1024
	ds_read_b128 v[138:141], v142 offset:2048
	ds_read_b128 v[142:145], v142 offset:3072
	ds_read_b128 v[146:149], v158
	ds_read_b128 v[150:153], v158 offset:1024
	ds_read_b128 v[154:157], v158 offset:2048
	ds_read_b128 v[158:161], v158 offset:3072
	s_add_u32 s48, s48, 0x80000
	s_addc_u32 s49, s49, 0
	s_mov_b32 m0, s62
	v_lshl_add_u64 v[246:247], s[48:49], 0, v[200:201]
	ds_read_b128 v[162:165], v244 offset:32768
	ds_read_b128 v[166:169], v244 offset:33792
	ds_read_b128 v[170:173], v244 offset:34816
	ds_read_b128 v[174:177], v244 offset:35840
	ds_read_b128 v[178:181], v244 offset:36864
	ds_read_b128 v[182:185], v244 offset:37888
	ds_read_b128 v[186:189], v244 offset:38912
	ds_read_b128 v[190:193], v244 offset:39936
	global_load_lds_dwordx4 v[246:247], off
	v_lshl_add_u64 v[246:247], s[48:49], 0, v[204:205]
	s_mov_b32 m0, s63
	s_nop 0
	global_load_lds_dwordx4 v[246:247], off
	s_waitcnt vmcnt(8)
	s_waitcnt lgkmcnt(0)
	s_barrier
	s_waitcnt lgkmcnt(0)
	v_mfma_f32_16x16x32_bf16 v[126:129], v[130:133], v[162:165], v[126:129]
	v_mfma_f32_16x16x32_bf16 v[122:125], v[138:141], v[162:165], v[122:125]
	v_mfma_f32_16x16x32_bf16 v[118:121], v[130:133], v[170:173], v[118:121]
	v_mfma_f32_16x16x32_bf16 v[110:113], v[138:141], v[170:173], v[110:113]
	v_mfma_f32_16x16x32_bf16 v[102:105], v[130:133], v[178:181], v[102:105]
	v_mfma_f32_16x16x32_bf16 v[94:97], v[138:141], v[178:181], v[94:97]
	v_mfma_f32_16x16x32_bf16 v[86:89], v[130:133], v[186:189], v[86:89]
	v_mfma_f32_16x16x32_bf16 v[78:81], v[138:141], v[186:189], v[78:81]
	v_mfma_f32_16x16x32_bf16 v[126:129], v[134:137], v[166:169], v[126:129]
	v_mfma_f32_16x16x32_bf16 v[122:125], v[142:145], v[166:169], v[122:125]
	v_mfma_f32_16x16x32_bf16 v[118:121], v[134:137], v[174:177], v[118:121]
	v_mfma_f32_16x16x32_bf16 v[110:113], v[142:145], v[174:177], v[110:113]
	v_mfma_f32_16x16x32_bf16 v[102:105], v[134:137], v[182:185], v[102:105]
	v_mfma_f32_16x16x32_bf16 v[94:97], v[142:145], v[182:185], v[94:97]
	v_mfma_f32_16x16x32_bf16 v[86:89], v[134:137], v[190:193], v[86:89]
	v_mfma_f32_16x16x32_bf16 v[78:81], v[142:145], v[190:193], v[78:81]
	v_mfma_f32_16x16x32_bf16 v[114:117], v[146:149], v[162:165], v[114:117]
	v_mfma_f32_16x16x32_bf16 v[106:109], v[154:157], v[162:165], v[106:109]
	v_mfma_f32_16x16x32_bf16 v[98:101], v[146:149], v[170:173], v[98:101]
	v_mfma_f32_16x16x32_bf16 v[90:93], v[154:157], v[170:173], v[90:93]
	v_mfma_f32_16x16x32_bf16 v[82:85], v[146:149], v[178:181], v[82:85]
	v_mfma_f32_16x16x32_bf16 v[74:77], v[154:157], v[178:181], v[74:77]
	v_mfma_f32_16x16x32_bf16 v[70:73], v[146:149], v[186:189], v[70:73]
	v_mfma_f32_16x16x32_bf16 v[66:69], v[154:157], v[186:189], v[66:69]
	v_mfma_f32_16x16x32_bf16 v[114:117], v[150:153], v[166:169], v[114:117]
	v_mfma_f32_16x16x32_bf16 v[106:109], v[158:161], v[166:169], v[106:109]
	v_mfma_f32_16x16x32_bf16 v[98:101], v[150:153], v[174:177], v[98:101]
	v_mfma_f32_16x16x32_bf16 v[90:93], v[158:161], v[174:177], v[90:93]
	v_mfma_f32_16x16x32_bf16 v[82:85], v[150:153], v[182:185], v[82:85]
	v_mfma_f32_16x16x32_bf16 v[74:77], v[158:161], v[182:185], v[74:77]
	v_mfma_f32_16x16x32_bf16 v[70:73], v[150:153], v[190:193], v[70:73]
	v_mfma_f32_16x16x32_bf16 v[66:69], v[158:161], v[190:193], v[66:69]
	s_barrier
	s_add_i32 s48, s50, s55
	v_lshl_add_u64 v[228:229], v[228:229], 0, s[14:15]
	s_mov_b32 m0, s48
	ds_read_b128 v[162:165], v244 offset:49152
	ds_read_b128 v[166:169], v244 offset:50176
	ds_read_b128 v[170:173], v244 offset:51200
	ds_read_b128 v[174:177], v244 offset:52224
	ds_read_b128 v[178:181], v244 offset:53248
	ds_read_b128 v[182:185], v244 offset:54272
	ds_read_b128 v[186:189], v244 offset:55296
	ds_read_b128 v[190:193], v244 offset:56320
	global_load_lds_dwordx4 v[228:229], off
	s_add_i32 m0, s48, 0x2000
	s_add_u32 s46, s46, 0x80080
	v_lshl_add_u64 v[226:227], v[226:227], 0, s[14:15]
	s_addc_u32 s47, s47, 0
	s_add_i32 s48, s51, s55
	global_load_lds_dwordx4 v[226:227], off
	v_lshl_add_u64 v[226:227], s[46:47], 0, v[202:203]
	s_mov_b32 m0, s48
	v_lshl_add_u64 v[222:223], v[222:223], 0, s[14:15]
	global_load_lds_dwordx4 v[226:227], off
	v_lshl_add_u64 v[226:227], s[46:47], 0, v[206:207]
	s_add_i32 m0, s48, 0x2000
	s_nop 0
	global_load_lds_dwordx4 v[226:227], off
	s_mov_b32 m0, s66
	s_nop 0
	global_load_lds_dwordx4 v[222:223], off
	v_lshl_add_u64 v[222:223], v[224:225], 0, s[14:15]
	s_mov_b32 m0, s67
	s_nop 0
	global_load_lds_dwordx4 v[222:223], off
	s_waitcnt vmcnt(8)
	s_waitcnt lgkmcnt(0)
	s_barrier
	s_waitcnt lgkmcnt(0)
	v_mfma_f32_16x16x32_bf16 v[62:65], v[130:133], v[162:165], v[62:65]
	v_mfma_f32_16x16x32_bf16 v[58:61], v[138:141], v[162:165], v[58:61]
	v_mfma_f32_16x16x32_bf16 v[54:57], v[130:133], v[170:173], v[54:57]
	v_mfma_f32_16x16x32_bf16 v[46:49], v[138:141], v[170:173], v[46:49]
	v_mfma_f32_16x16x32_bf16 v[38:41], v[130:133], v[178:181], v[38:41]
	v_mfma_f32_16x16x32_bf16 v[30:33], v[138:141], v[178:181], v[30:33]
	v_mfma_f32_16x16x32_bf16 v[22:25], v[130:133], v[186:189], v[22:25]
	v_mfma_f32_16x16x32_bf16 v[14:17], v[138:141], v[186:189], v[14:17]
	v_mfma_f32_16x16x32_bf16 v[62:65], v[134:137], v[166:169], v[62:65]
	v_mfma_f32_16x16x32_bf16 v[58:61], v[142:145], v[166:169], v[58:61]
	v_mfma_f32_16x16x32_bf16 v[54:57], v[134:137], v[174:177], v[54:57]
	v_mfma_f32_16x16x32_bf16 v[46:49], v[142:145], v[174:177], v[46:49]
	v_mfma_f32_16x16x32_bf16 v[38:41], v[134:137], v[182:185], v[38:41]
	v_mfma_f32_16x16x32_bf16 v[30:33], v[142:145], v[182:185], v[30:33]
	v_mfma_f32_16x16x32_bf16 v[22:25], v[134:137], v[190:193], v[22:25]
	v_mfma_f32_16x16x32_bf16 v[14:17], v[142:145], v[190:193], v[14:17]
	v_mfma_f32_16x16x32_bf16 v[50:53], v[146:149], v[162:165], v[50:53]
	v_mfma_f32_16x16x32_bf16 v[42:45], v[154:157], v[162:165], v[42:45]
	v_mfma_f32_16x16x32_bf16 v[34:37], v[146:149], v[170:173], v[34:37]
	v_mfma_f32_16x16x32_bf16 v[26:29], v[154:157], v[170:173], v[26:29]
	v_mfma_f32_16x16x32_bf16 v[18:21], v[146:149], v[178:181], v[18:21]
	v_mfma_f32_16x16x32_bf16 v[10:13], v[154:157], v[178:181], v[10:13]
	v_mfma_f32_16x16x32_bf16 v[6:9], v[146:149], v[186:189], v[6:9]
	v_mfma_f32_16x16x32_bf16 v[2:5], v[154:157], v[186:189], v[2:5]
	v_mfma_f32_16x16x32_bf16 v[50:53], v[150:153], v[166:169], v[50:53]
	v_mfma_f32_16x16x32_bf16 v[42:45], v[158:161], v[166:169], v[42:45]
	v_mfma_f32_16x16x32_bf16 v[34:37], v[150:153], v[174:177], v[34:37]
	v_mfma_f32_16x16x32_bf16 v[26:29], v[158:161], v[174:177], v[26:29]
	v_mfma_f32_16x16x32_bf16 v[18:21], v[150:153], v[182:185], v[18:21]
	v_mfma_f32_16x16x32_bf16 v[10:13], v[158:161], v[182:185], v[10:13]
	v_mfma_f32_16x16x32_bf16 v[6:9], v[150:153], v[190:193], v[6:9]
	v_mfma_f32_16x16x32_bf16 v[2:5], v[158:161], v[190:193], v[2:5]
	s_barrier
	s_add_i32 s78, s78, 2
	s_add_u32 s42, s42, 0x100
	s_addc_u32 s43, s43, 0
	s_cmp_gt_u32 s78, 29
	s_cbranch_scc1 .LBB0_326

.LBB0_322:
	s_add_u32 s46, s40, s42
	s_addc_u32 s47, s41, s43
	s_add_u32 s46, s46, 0x100
	s_addc_u32 s47, s47, 0
	s_add_u32 s52, s76, s42
	s_addc_u32 s53, s77, s43
	s_waitcnt lgkmcnt(0)
	s_cmpk_eq_i32 s42, 0xf00
	s_cselect_b32 s49, s31, s47
	s_cselect_b32 s48, s39, s46
	s_cselect_b32 s47, s29, s53
	s_cselect_b32 s46, s75, s52
	s_barrier
	s_waitcnt lgkmcnt(0)
	v_mfma_f32_16x16x32_bf16 v[126:129], v[146:149], v[186:189], v[126:129]
	v_mfma_f32_16x16x32_bf16 v[122:125], v[154:157], v[186:189], v[122:125]
	v_mfma_f32_16x16x32_bf16 v[118:121], v[146:149], v[178:181], v[118:121]
	v_mfma_f32_16x16x32_bf16 v[110:113], v[154:157], v[178:181], v[110:113]
	v_mfma_f32_16x16x32_bf16 v[102:105], v[146:149], v[170:173], v[102:105]
	v_mfma_f32_16x16x32_bf16 v[94:97], v[154:157], v[170:173], v[94:97]
	v_mfma_f32_16x16x32_bf16 v[86:89], v[146:149], v[162:165], v[86:89]
	v_mfma_f32_16x16x32_bf16 v[78:81], v[154:157], v[162:165], v[78:81]
	v_mfma_f32_16x16x32_bf16 v[126:129], v[150:153], v[190:193], v[126:129]
	v_mfma_f32_16x16x32_bf16 v[122:125], v[158:161], v[190:193], v[122:125]
	v_mfma_f32_16x16x32_bf16 v[118:121], v[150:153], v[182:185], v[118:121]
	v_mfma_f32_16x16x32_bf16 v[110:113], v[158:161], v[182:185], v[110:113]
	v_mfma_f32_16x16x32_bf16 v[102:105], v[150:153], v[174:177], v[102:105]
	v_mfma_f32_16x16x32_bf16 v[94:97], v[158:161], v[174:177], v[94:97]
	v_mfma_f32_16x16x32_bf16 v[86:89], v[150:153], v[166:169], v[86:89]
	v_mfma_f32_16x16x32_bf16 v[78:81], v[158:161], v[166:169], v[78:81]
	v_mfma_f32_16x16x32_bf16 v[114:117], v[130:133], v[186:189], v[114:117]
	v_mfma_f32_16x16x32_bf16 v[106:109], v[138:141], v[186:189], v[106:109]
	v_mfma_f32_16x16x32_bf16 v[98:101], v[130:133], v[178:181], v[98:101]
	v_mfma_f32_16x16x32_bf16 v[90:93], v[138:141], v[178:181], v[90:93]
	v_mfma_f32_16x16x32_bf16 v[82:85], v[130:133], v[170:173], v[82:85]
	v_mfma_f32_16x16x32_bf16 v[74:77], v[138:141], v[170:173], v[74:77]
	v_mfma_f32_16x16x32_bf16 v[70:73], v[130:133], v[162:165], v[70:73]
	v_mfma_f32_16x16x32_bf16 v[66:69], v[138:141], v[162:165], v[66:69]
	v_mfma_f32_16x16x32_bf16 v[114:117], v[134:137], v[190:193], v[114:117]
	v_mfma_f32_16x16x32_bf16 v[106:109], v[142:145], v[190:193], v[106:109]
	v_mfma_f32_16x16x32_bf16 v[98:101], v[134:137], v[182:185], v[98:101]
	v_mfma_f32_16x16x32_bf16 v[90:93], v[142:145], v[182:185], v[90:93]
	v_mfma_f32_16x16x32_bf16 v[82:85], v[134:137], v[174:177], v[82:85]
	v_mfma_f32_16x16x32_bf16 v[74:77], v[142:145], v[174:177], v[74:77]
	v_mfma_f32_16x16x32_bf16 v[70:73], v[134:137], v[166:169], v[70:73]
	v_mfma_f32_16x16x32_bf16 v[66:69], v[142:145], v[166:169], v[66:69]
	s_barrier
	s_mov_b32 m0, s57
	v_lshl_add_u64 v[228:229], s[46:47], 0, v[202:203]
	s_add_u32 s52, s46, 0x80000
	ds_read_b128 v[186:189], v244 offset:16384
	ds_read_b128 v[190:193], v244 offset:17408
	ds_read_b128 v[178:181], v244 offset:18432
	ds_read_b128 v[182:185], v244 offset:19456
	ds_read_b128 v[170:173], v244 offset:20480
	ds_read_b128 v[174:177], v244 offset:21504
	ds_read_b128 v[162:165], v244 offset:22528
	ds_read_b128 v[166:169], v244 offset:23552
	global_load_lds_dwordx4 v[228:229], off
	v_lshl_add_u64 v[226:227], s[46:47], 0, v[206:207]
	s_mov_b32 m0, s58
	s_addc_u32 s53, s47, 0
	global_load_lds_dwordx4 v[226:227], off
	v_lshl_add_u64 v[222:223], s[52:53], 0, v[202:203]
	s_mov_b32 m0, s59
	v_lshl_add_u64 v[224:225], s[48:49], 0, v[204:205]
	global_load_lds_dwordx4 v[222:223], off
	v_lshl_add_u64 v[222:223], s[52:53], 0, v[206:207]
	s_mov_b32 m0, s60
	s_mov_b64 s[52:53], -1
	global_load_lds_dwordx4 v[222:223], off
	v_lshl_add_u64 v[222:223], s[48:49], 0, v[200:201]
	s_mov_b32 m0, s56
	s_and_b64 vcc, exec, s[50:51]
	global_load_lds_dwordx4 v[222:223], off
	s_mov_b32 m0, s61
	s_nop 0
	global_load_lds_dwordx4 v[224:225], off
	s_cbranch_vccz .LBB0_324
	s_waitcnt vmcnt(8)
	s_mov_b64 s[52:53], 0

.LBB0_353:
	s_waitcnt lgkmcnt(0)
	s_barrier
	s_waitcnt lgkmcnt(0)
	v_mfma_scale_f32_16x16x128_f8f6f4 v[126:129], v[26:33], v[58:65], v[126:129], v239, v239 op_sel_hi:[0,0,0]
	v_mfma_scale_f32_16x16x128_f8f6f4 v[118:121], v[18:25], v[58:65], v[118:121], v239, v239 op_sel_hi:[0,0,0]
	v_mfma_scale_f32_16x16x128_f8f6f4 v[110:113], v[26:33], v[50:57], v[110:113], v239, v239 op_sel_hi:[0,0,0]
	v_mfma_scale_f32_16x16x128_f8f6f4 v[102:105], v[18:25], v[50:57], v[102:105], v239, v239 op_sel_hi:[0,0,0]
	v_mfma_scale_f32_16x16x128_f8f6f4 v[94:97], v[26:33], v[42:49], v[94:97], v239, v239 op_sel_hi:[0,0,0]
	v_mfma_scale_f32_16x16x128_f8f6f4 v[86:89], v[18:25], v[42:49], v[86:89], v239, v239 op_sel_hi:[0,0,0]
	v_mfma_scale_f32_16x16x128_f8f6f4 v[78:81], v[26:33], v[34:41], v[78:81], v239, v239 op_sel_hi:[0,0,0]
	v_mfma_scale_f32_16x16x128_f8f6f4 v[70:73], v[18:25], v[34:41], v[70:73], v239, v239 op_sel_hi:[0,0,0]
	v_mfma_scale_f32_16x16x128_f8f6f4 v[122:125], v[10:17], v[58:65], v[122:125], v239, v239 op_sel_hi:[0,0,0]
	v_mfma_scale_f32_16x16x128_f8f6f4 v[114:117], v[2:9], v[58:65], v[114:117], v239, v239 op_sel_hi:[0,0,0]
	v_mfma_scale_f32_16x16x128_f8f6f4 v[106:109], v[10:17], v[50:57], v[106:109], v239, v239 op_sel_hi:[0,0,0]
	v_mfma_scale_f32_16x16x128_f8f6f4 v[98:101], v[2:9], v[50:57], v[98:101], v239, v239 op_sel_hi:[0,0,0]
	v_mfma_scale_f32_16x16x128_f8f6f4 v[90:93], v[10:17], v[42:49], v[90:93], v239, v239 op_sel_hi:[0,0,0]
	v_mfma_scale_f32_16x16x128_f8f6f4 v[82:85], v[2:9], v[42:49], v[82:85], v239, v239 op_sel_hi:[0,0,0]
	v_mfma_scale_f32_16x16x128_f8f6f4 v[74:77], v[10:17], v[34:41], v[74:77], v239, v239 op_sel_hi:[0,0,0]
	v_mfma_scale_f32_16x16x128_f8f6f4 v[66:69], v[2:9], v[34:41], v[66:69], v239, v239 op_sel_hi:[0,0,0]
	s_barrier
	s_add_i32 s46, 0, 0x18000
	s_add_i32 s47, 0, 0x1c000
	v_add_u32_e32 v14, s46, v229
	v_add_u32_e32 v30, s47, v229
	ds_read_b128 v[2:5], v14
	ds_read_b128 v[6:9], v14 offset:1024
	ds_read_b128 v[10:13], v14 offset:2048
	ds_read_b128 v[14:17], v14 offset:3072
	ds_read_b128 v[18:21], v30
	ds_read_b128 v[22:25], v30 offset:1024
	ds_read_b128 v[26:29], v30 offset:2048
	ds_read_b128 v[30:33], v30 offset:3072
	s_add_u32 s44, s44, 0x40000
	s_addc_u32 s45, s45, 0
	s_mov_b32 m0, s60
	v_lshl_add_u64 v[240:241], s[44:45], 0, v[200:201]
	ds_read_b128 v[34:37], v233 offset:32768
	ds_read_b128 v[38:41], v233 offset:33792
	ds_read_b128 v[42:45], v233 offset:34816
	ds_read_b128 v[46:49], v233 offset:35840
	ds_read_b128 v[50:53], v233 offset:36864
	ds_read_b128 v[54:57], v233 offset:37888
	ds_read_b128 v[58:61], v233 offset:38912
	ds_read_b128 v[62:65], v233 offset:39936
	global_load_lds_dwordx4 v[240:241], off
	v_lshl_add_u64 v[240:241], s[44:45], 0, v[204:205]
	s_mov_b32 m0, s61
	s_nop 0
	global_load_lds_dwordx4 v[240:241], off
	s_waitcnt vmcnt(8)
	s_waitcnt lgkmcnt(0)
	s_barrier
	s_waitcnt lgkmcnt(0)
	v_mfma_scale_f32_16x16x128_f8f6f4 v[190:193], v[2:9], v[34:41], v[190:193], v239, v239 op_sel_hi:[0,0,0]
	v_mfma_scale_f32_16x16x128_f8f6f4 v[182:185], v[10:17], v[34:41], v[182:185], v239, v239 op_sel_hi:[0,0,0]
	v_mfma_scale_f32_16x16x128_f8f6f4 v[174:177], v[2:9], v[42:49], v[174:177], v239, v239 op_sel_hi:[0,0,0]
	v_mfma_scale_f32_16x16x128_f8f6f4 v[166:169], v[10:17], v[42:49], v[166:169], v239, v239 op_sel_hi:[0,0,0]
	v_mfma_scale_f32_16x16x128_f8f6f4 v[158:161], v[2:9], v[50:57], v[158:161], v239, v239 op_sel_hi:[0,0,0]
	v_mfma_scale_f32_16x16x128_f8f6f4 v[150:153], v[10:17], v[50:57], v[150:153], v239, v239 op_sel_hi:[0,0,0]
	v_mfma_scale_f32_16x16x128_f8f6f4 v[142:145], v[2:9], v[58:65], v[142:145], v239, v239 op_sel_hi:[0,0,0]
	v_mfma_scale_f32_16x16x128_f8f6f4 v[134:137], v[10:17], v[58:65], v[134:137], v239, v239 op_sel_hi:[0,0,0]
	v_mfma_scale_f32_16x16x128_f8f6f4 v[186:189], v[18:25], v[34:41], v[186:189], v239, v239 op_sel_hi:[0,0,0]
	v_mfma_scale_f32_16x16x128_f8f6f4 v[178:181], v[26:33], v[34:41], v[178:181], v239, v239 op_sel_hi:[0,0,0]
	v_mfma_scale_f32_16x16x128_f8f6f4 v[170:173], v[18:25], v[42:49], v[170:173], v239, v239 op_sel_hi:[0,0,0]
	v_mfma_scale_f32_16x16x128_f8f6f4 v[162:165], v[26:33], v[42:49], v[162:165], v239, v239 op_sel_hi:[0,0,0]
	v_mfma_scale_f32_16x16x128_f8f6f4 v[154:157], v[18:25], v[50:57], v[154:157], v239, v239 op_sel_hi:[0,0,0]
	v_mfma_scale_f32_16x16x128_f8f6f4 v[146:149], v[26:33], v[50:57], v[146:149], v239, v239 op_sel_hi:[0,0,0]
	v_mfma_scale_f32_16x16x128_f8f6f4 v[138:141], v[18:25], v[58:65], v[138:141], v239, v239 op_sel_hi:[0,0,0]
	v_mfma_scale_f32_16x16x128_f8f6f4 v[130:133], v[26:33], v[58:65], v[130:133], v239, v239 op_sel_hi:[0,0,0]
	s_barrier
	s_add_i32 s44, s46, s54
	v_lshl_add_u64 v[226:227], v[226:227], 0, s[6:7]
	s_mov_b32 m0, s44
	ds_read_b128 v[34:37], v233 offset:49152
	ds_read_b128 v[38:41], v233 offset:50176
	ds_read_b128 v[42:45], v233 offset:51200
	ds_read_b128 v[46:49], v233 offset:52224
	ds_read_b128 v[50:53], v233 offset:53248
	ds_read_b128 v[54:57], v233 offset:54272
	ds_read_b128 v[58:61], v233 offset:55296
	ds_read_b128 v[62:65], v233 offset:56320
	global_load_lds_dwordx4 v[226:227], off
	s_add_i32 m0, s44, 0x2000
	s_add_u32 s42, s42, 0x40080
	v_lshl_add_u64 v[224:225], v[224:225], 0, s[6:7]
	s_addc_u32 s43, s43, 0
	s_add_i32 s44, s47, s54
	global_load_lds_dwordx4 v[224:225], off
	v_lshl_add_u64 v[224:225], s[42:43], 0, v[202:203]
	s_mov_b32 m0, s44
	v_lshl_add_u64 v[220:221], v[220:221], 0, s[6:7]
	global_load_lds_dwordx4 v[224:225], off
	v_lshl_add_u64 v[224:225], s[42:43], 0, v[206:207]
	s_add_i32 m0, s44, 0x2000
	s_nop 0
	global_load_lds_dwordx4 v[224:225], off
	s_mov_b32 m0, s62
	s_nop 0
	global_load_lds_dwordx4 v[220:221], off
	v_lshl_add_u64 v[220:221], v[222:223], 0, s[6:7]
	s_mov_b32 m0, s63
	s_nop 0
	global_load_lds_dwordx4 v[220:221], off
	s_waitcnt vmcnt(8)
	s_waitcnt lgkmcnt(0)
	s_barrier
	s_waitcnt lgkmcnt(0)
	v_mfma_scale_f32_16x16x128_f8f6f4 v[126:129], v[2:9], v[34:41], v[126:129], v239, v239 op_sel_hi:[0,0,0]
	v_mfma_scale_f32_16x16x128_f8f6f4 v[118:121], v[10:17], v[34:41], v[118:121], v239, v239 op_sel_hi:[0,0,0]
	v_mfma_scale_f32_16x16x128_f8f6f4 v[110:113], v[2:9], v[42:49], v[110:113], v239, v239 op_sel_hi:[0,0,0]
	v_mfma_scale_f32_16x16x128_f8f6f4 v[102:105], v[10:17], v[42:49], v[102:105], v239, v239 op_sel_hi:[0,0,0]
	v_mfma_scale_f32_16x16x128_f8f6f4 v[94:97], v[2:9], v[50:57], v[94:97], v239, v239 op_sel_hi:[0,0,0]
	v_mfma_scale_f32_16x16x128_f8f6f4 v[86:89], v[10:17], v[50:57], v[86:89], v239, v239 op_sel_hi:[0,0,0]
	v_mfma_scale_f32_16x16x128_f8f6f4 v[78:81], v[2:9], v[58:65], v[78:81], v239, v239 op_sel_hi:[0,0,0]
	v_mfma_scale_f32_16x16x128_f8f6f4 v[70:73], v[10:17], v[58:65], v[70:73], v239, v239 op_sel_hi:[0,0,0]
	v_mfma_scale_f32_16x16x128_f8f6f4 v[122:125], v[18:25], v[34:41], v[122:125], v239, v239 op_sel_hi:[0,0,0]
	v_mfma_scale_f32_16x16x128_f8f6f4 v[114:117], v[26:33], v[34:41], v[114:117], v239, v239 op_sel_hi:[0,0,0]
	v_mfma_scale_f32_16x16x128_f8f6f4 v[106:109], v[18:25], v[42:49], v[106:109], v239, v239 op_sel_hi:[0,0,0]
	v_mfma_scale_f32_16x16x128_f8f6f4 v[98:101], v[26:33], v[42:49], v[98:101], v239, v239 op_sel_hi:[0,0,0]
	v_mfma_scale_f32_16x16x128_f8f6f4 v[90:93], v[18:25], v[50:57], v[90:93], v239, v239 op_sel_hi:[0,0,0]
	v_mfma_scale_f32_16x16x128_f8f6f4 v[82:85], v[26:33], v[50:57], v[82:85], v239, v239 op_sel_hi:[0,0,0]
	v_mfma_scale_f32_16x16x128_f8f6f4 v[74:77], v[18:25], v[58:65], v[74:77], v239, v239 op_sel_hi:[0,0,0]
	v_mfma_scale_f32_16x16x128_f8f6f4 v[66:69], v[26:33], v[58:65], v[66:69], v239, v239 op_sel_hi:[0,0,0]
	s_barrier
	s_add_i32 s71, s71, 2
	s_add_u32 s38, s38, 0x100
	s_addc_u32 s39, s39, 0
	s_cmp_gt_u32 s71, 13
	s_cbranch_scc1 .LBB0_362

.LBB0_358:
	s_add_u32 s42, s36, s38
	s_addc_u32 s43, s37, s39
	s_add_u32 s42, s42, 0x100
	s_addc_u32 s43, s43, 0
	s_add_u32 s48, s69, s38
	s_addc_u32 s49, s70, s39
	s_waitcnt lgkmcnt(0)
	s_cmpk_eq_i32 s38, 0x700
	s_cselect_b32 s45, s27, s43
	s_cselect_b32 s44, s67, s42
	s_cselect_b32 s43, s25, s49
	s_cselect_b32 s42, s68, s48
	s_barrier
	s_waitcnt lgkmcnt(0)
	v_mfma_scale_f32_16x16x128_f8f6f4 v[190:193], v[26:33], v[58:65], v[190:193], v239, v239 op_sel_hi:[0,0,0]
	v_mfma_scale_f32_16x16x128_f8f6f4 v[182:185], v[18:25], v[58:65], v[182:185], v239, v239 op_sel_hi:[0,0,0]
	v_mfma_scale_f32_16x16x128_f8f6f4 v[174:177], v[26:33], v[50:57], v[174:177], v239, v239 op_sel_hi:[0,0,0]
	v_mfma_scale_f32_16x16x128_f8f6f4 v[166:169], v[18:25], v[50:57], v[166:169], v239, v239 op_sel_hi:[0,0,0]
	v_mfma_scale_f32_16x16x128_f8f6f4 v[158:161], v[26:33], v[42:49], v[158:161], v239, v239 op_sel_hi:[0,0,0]
	v_mfma_scale_f32_16x16x128_f8f6f4 v[150:153], v[18:25], v[42:49], v[150:153], v239, v239 op_sel_hi:[0,0,0]
	v_mfma_scale_f32_16x16x128_f8f6f4 v[142:145], v[26:33], v[34:41], v[142:145], v239, v239 op_sel_hi:[0,0,0]
	v_mfma_scale_f32_16x16x128_f8f6f4 v[134:137], v[18:25], v[34:41], v[134:137], v239, v239 op_sel_hi:[0,0,0]
	v_mfma_scale_f32_16x16x128_f8f6f4 v[186:189], v[10:17], v[58:65], v[186:189], v239, v239 op_sel_hi:[0,0,0]
	v_mfma_scale_f32_16x16x128_f8f6f4 v[178:181], v[2:9], v[58:65], v[178:181], v239, v239 op_sel_hi:[0,0,0]
	v_mfma_scale_f32_16x16x128_f8f6f4 v[170:173], v[10:17], v[50:57], v[170:173], v239, v239 op_sel_hi:[0,0,0]
	v_mfma_scale_f32_16x16x128_f8f6f4 v[162:165], v[2:9], v[50:57], v[162:165], v239, v239 op_sel_hi:[0,0,0]
	v_mfma_scale_f32_16x16x128_f8f6f4 v[154:157], v[10:17], v[42:49], v[154:157], v239, v239 op_sel_hi:[0,0,0]
	v_mfma_scale_f32_16x16x128_f8f6f4 v[146:149], v[2:9], v[42:49], v[146:149], v239, v239 op_sel_hi:[0,0,0]
	v_mfma_scale_f32_16x16x128_f8f6f4 v[138:141], v[10:17], v[34:41], v[138:141], v239, v239 op_sel_hi:[0,0,0]
	v_mfma_scale_f32_16x16x128_f8f6f4 v[130:133], v[2:9], v[34:41], v[130:133], v239, v239 op_sel_hi:[0,0,0]
	s_barrier
	s_mov_b32 m0, s55
	v_lshl_add_u64 v[226:227], s[42:43], 0, v[202:203]
	s_add_u32 s48, s42, 0x40000
	ds_read_b128 v[58:61], v233 offset:16384
	ds_read_b128 v[62:65], v233 offset:17408
	ds_read_b128 v[50:53], v233 offset:18432
	ds_read_b128 v[54:57], v233 offset:19456
	ds_read_b128 v[42:45], v233 offset:20480
	ds_read_b128 v[46:49], v233 offset:21504
	ds_read_b128 v[34:37], v233 offset:22528
	ds_read_b128 v[38:41], v233 offset:23552
	global_load_lds_dwordx4 v[226:227], off
	v_lshl_add_u64 v[224:225], s[42:43], 0, v[206:207]
	s_mov_b32 m0, s56
	s_addc_u32 s49, s43, 0
	global_load_lds_dwordx4 v[224:225], off
	v_lshl_add_u64 v[220:221], s[48:49], 0, v[202:203]
	s_mov_b32 m0, s57
	v_lshl_add_u64 v[222:223], s[44:45], 0, v[204:205]
	global_load_lds_dwordx4 v[220:221], off
	v_lshl_add_u64 v[220:221], s[48:49], 0, v[206:207]
	s_mov_b32 m0, s58
	s_mov_b64 s[48:49], -1
	global_load_lds_dwordx4 v[220:221], off
	v_lshl_add_u64 v[220:221], s[44:45], 0, v[200:201]
	s_mov_b32 m0, s35
	s_and_b64 vcc, exec, s[46:47]
	global_load_lds_dwordx4 v[220:221], off
	s_mov_b32 m0, s59
	s_nop 0
	global_load_lds_dwordx4 v[222:223], off
	s_cbranch_vccz .LBB0_360
	s_waitcnt vmcnt(8)
	s_mov_b64 s[48:49], 0

.LBB0_385:
	s_waitcnt lgkmcnt(0)
	s_xor_b64 s[44:45], s[38:39], -1
	s_barrier
	s_waitcnt lgkmcnt(0)
	v_mfma_f32_16x16x32_bf16 v[62:65], v[146:149], v[186:189], v[62:65]
	v_mfma_f32_16x16x32_bf16 v[58:61], v[154:157], v[186:189], v[58:61]
	v_mfma_f32_16x16x32_bf16 v[54:57], v[146:149], v[178:181], v[54:57]
	v_mfma_f32_16x16x32_bf16 v[46:49], v[154:157], v[178:181], v[46:49]
	v_mfma_f32_16x16x32_bf16 v[38:41], v[146:149], v[170:173], v[38:41]
	v_mfma_f32_16x16x32_bf16 v[30:33], v[154:157], v[170:173], v[30:33]
	v_mfma_f32_16x16x32_bf16 v[22:25], v[146:149], v[162:165], v[22:25]
	v_mfma_f32_16x16x32_bf16 v[14:17], v[154:157], v[162:165], v[14:17]
	v_mfma_f32_16x16x32_bf16 v[62:65], v[150:153], v[190:193], v[62:65]
	v_mfma_f32_16x16x32_bf16 v[58:61], v[158:161], v[190:193], v[58:61]
	v_mfma_f32_16x16x32_bf16 v[54:57], v[150:153], v[182:185], v[54:57]
	v_mfma_f32_16x16x32_bf16 v[46:49], v[158:161], v[182:185], v[46:49]
	v_mfma_f32_16x16x32_bf16 v[38:41], v[150:153], v[174:177], v[38:41]
	v_mfma_f32_16x16x32_bf16 v[30:33], v[158:161], v[174:177], v[30:33]
	v_mfma_f32_16x16x32_bf16 v[22:25], v[150:153], v[166:169], v[22:25]
	v_mfma_f32_16x16x32_bf16 v[14:17], v[158:161], v[166:169], v[14:17]
	v_mfma_f32_16x16x32_bf16 v[50:53], v[130:133], v[186:189], v[50:53]
	v_mfma_f32_16x16x32_bf16 v[42:45], v[138:141], v[186:189], v[42:45]
	v_mfma_f32_16x16x32_bf16 v[34:37], v[130:133], v[178:181], v[34:37]
	v_mfma_f32_16x16x32_bf16 v[26:29], v[138:141], v[178:181], v[26:29]
	v_mfma_f32_16x16x32_bf16 v[18:21], v[130:133], v[170:173], v[18:21]
	v_mfma_f32_16x16x32_bf16 v[10:13], v[138:141], v[170:173], v[10:13]
	v_mfma_f32_16x16x32_bf16 v[6:9], v[130:133], v[162:165], v[6:9]
	v_mfma_f32_16x16x32_bf16 v[2:5], v[138:141], v[162:165], v[2:5]
	v_mfma_f32_16x16x32_bf16 v[50:53], v[134:137], v[190:193], v[50:53]
	v_mfma_f32_16x16x32_bf16 v[42:45], v[142:145], v[190:193], v[42:45]
	v_mfma_f32_16x16x32_bf16 v[34:37], v[134:137], v[182:185], v[34:37]
	v_mfma_f32_16x16x32_bf16 v[26:29], v[142:145], v[182:185], v[26:29]
	v_mfma_f32_16x16x32_bf16 v[18:21], v[134:137], v[174:177], v[18:21]
	v_mfma_f32_16x16x32_bf16 v[10:13], v[142:145], v[174:177], v[10:13]
	v_mfma_f32_16x16x32_bf16 v[6:9], v[134:137], v[166:169], v[6:9]
	v_mfma_f32_16x16x32_bf16 v[2:5], v[142:145], v[166:169], v[2:5]
	s_barrier
	s_add_i32 s42, 0, 0x18000
	s_add_i32 s43, 0, 0x1c000
	v_add_u32_e32 v142, s42, v1
	v_add_u32_e32 v158, s43, v1
	ds_read_b128 v[130:133], v142
	ds_read_b128 v[134:137], v142 offset:1024
	ds_read_b128 v[138:141], v142 offset:2048
	ds_read_b128 v[142:145], v142 offset:3072
	ds_read_b128 v[146:149], v158
	ds_read_b128 v[150:153], v158 offset:1024
	ds_read_b128 v[154:157], v158 offset:2048
	ds_read_b128 v[158:161], v158 offset:3072
	s_add_u32 s38, s46, 0x10000
	s_addc_u32 s39, s47, 0
	s_mov_b32 m0, s58
	v_lshl_add_u64 v[222:223], s[38:39], 0, v[200:201]
	ds_read_b128 v[162:165], v220 offset:32768
	ds_read_b128 v[166:169], v220 offset:33792
	ds_read_b128 v[170:173], v220 offset:34816
	ds_read_b128 v[174:177], v220 offset:35840
	ds_read_b128 v[178:181], v220 offset:36864
	ds_read_b128 v[182:185], v220 offset:37888
	ds_read_b128 v[186:189], v220 offset:38912
	ds_read_b128 v[190:193], v220 offset:39936
	global_load_lds_dwordx4 v[222:223], off
	v_lshl_add_u64 v[222:223], s[38:39], 0, v[204:205]
	s_mov_b32 m0, s59
	s_nop 0
	global_load_lds_dwordx4 v[222:223], off
	s_waitcnt vmcnt(8)
	s_waitcnt lgkmcnt(0)
	s_barrier
	s_waitcnt lgkmcnt(0)
	v_mfma_f32_16x16x32_bf16 v[126:129], v[130:133], v[162:165], v[126:129]
	v_mfma_f32_16x16x32_bf16 v[122:125], v[138:141], v[162:165], v[122:125]
	v_mfma_f32_16x16x32_bf16 v[118:121], v[130:133], v[170:173], v[118:121]
	v_mfma_f32_16x16x32_bf16 v[110:113], v[138:141], v[170:173], v[110:113]
	v_mfma_f32_16x16x32_bf16 v[102:105], v[130:133], v[178:181], v[102:105]
	v_mfma_f32_16x16x32_bf16 v[94:97], v[138:141], v[178:181], v[94:97]
	v_mfma_f32_16x16x32_bf16 v[86:89], v[130:133], v[186:189], v[86:89]
	v_mfma_f32_16x16x32_bf16 v[78:81], v[138:141], v[186:189], v[78:81]
	v_mfma_f32_16x16x32_bf16 v[126:129], v[134:137], v[166:169], v[126:129]
	v_mfma_f32_16x16x32_bf16 v[122:125], v[142:145], v[166:169], v[122:125]
	v_mfma_f32_16x16x32_bf16 v[118:121], v[134:137], v[174:177], v[118:121]
	v_mfma_f32_16x16x32_bf16 v[110:113], v[142:145], v[174:177], v[110:113]
	v_mfma_f32_16x16x32_bf16 v[102:105], v[134:137], v[182:185], v[102:105]
	v_mfma_f32_16x16x32_bf16 v[94:97], v[142:145], v[182:185], v[94:97]
	v_mfma_f32_16x16x32_bf16 v[86:89], v[134:137], v[190:193], v[86:89]
	v_mfma_f32_16x16x32_bf16 v[78:81], v[142:145], v[190:193], v[78:81]
	v_mfma_f32_16x16x32_bf16 v[114:117], v[146:149], v[162:165], v[114:117]
	v_mfma_f32_16x16x32_bf16 v[106:109], v[154:157], v[162:165], v[106:109]
	v_mfma_f32_16x16x32_bf16 v[98:101], v[146:149], v[170:173], v[98:101]
	v_mfma_f32_16x16x32_bf16 v[90:93], v[154:157], v[170:173], v[90:93]
	v_mfma_f32_16x16x32_bf16 v[82:85], v[146:149], v[178:181], v[82:85]
	v_mfma_f32_16x16x32_bf16 v[74:77], v[154:157], v[178:181], v[74:77]
	v_mfma_f32_16x16x32_bf16 v[70:73], v[146:149], v[186:189], v[70:73]
	v_mfma_f32_16x16x32_bf16 v[66:69], v[154:157], v[186:189], v[66:69]
	v_mfma_f32_16x16x32_bf16 v[114:117], v[150:153], v[166:169], v[114:117]
	v_mfma_f32_16x16x32_bf16 v[106:109], v[158:161], v[166:169], v[106:109]
	v_mfma_f32_16x16x32_bf16 v[98:101], v[150:153], v[174:177], v[98:101]
	v_mfma_f32_16x16x32_bf16 v[90:93], v[158:161], v[174:177], v[90:93]
	v_mfma_f32_16x16x32_bf16 v[82:85], v[150:153], v[182:185], v[82:85]
	v_mfma_f32_16x16x32_bf16 v[74:77], v[158:161], v[182:185], v[74:77]
	v_mfma_f32_16x16x32_bf16 v[70:73], v[150:153], v[190:193], v[70:73]
	v_mfma_f32_16x16x32_bf16 v[66:69], v[158:161], v[190:193], v[66:69]
	s_barrier
	s_add_i32 s38, s42, s52
	v_lshl_add_u64 v[216:217], v[216:217], 0, s[4:5]
	s_mov_b32 m0, s38
	ds_read_b128 v[162:165], v220 offset:49152
	ds_read_b128 v[166:169], v220 offset:50176
	ds_read_b128 v[170:173], v220 offset:51200
	ds_read_b128 v[174:177], v220 offset:52224
	ds_read_b128 v[178:181], v220 offset:53248
	ds_read_b128 v[182:185], v220 offset:54272
	ds_read_b128 v[186:189], v220 offset:55296
	ds_read_b128 v[190:193], v220 offset:56320
	global_load_lds_dwordx4 v[216:217], off
	s_add_i32 m0, s38, 0x2000
	s_add_u32 s38, s40, 0x10080
	v_lshl_add_u64 v[214:215], v[214:215], 0, s[4:5]
	s_addc_u32 s39, s41, 0
	s_add_i32 s40, s43, s52
	global_load_lds_dwordx4 v[214:215], off
	v_lshl_add_u64 v[214:215], s[38:39], 0, v[202:203]
	s_mov_b32 m0, s40
	v_lshl_add_u64 v[210:211], v[210:211], 0, s[4:5]
	global_load_lds_dwordx4 v[214:215], off
	v_lshl_add_u64 v[214:215], s[38:39], 0, v[206:207]
	s_add_i32 m0, s40, 0x2000
	s_nop 0
	global_load_lds_dwordx4 v[214:215], off
	s_mov_b32 m0, s60
	s_nop 0
	global_load_lds_dwordx4 v[210:211], off
	v_lshl_add_u64 v[210:211], v[212:213], 0, s[4:5]
	s_mov_b32 m0, s61
	s_nop 0
	global_load_lds_dwordx4 v[210:211], off
	s_waitcnt vmcnt(8)
	s_waitcnt lgkmcnt(0)
	s_barrier
	s_waitcnt lgkmcnt(0)
	v_mfma_f32_16x16x32_bf16 v[62:65], v[130:133], v[162:165], v[62:65]
	v_mfma_f32_16x16x32_bf16 v[58:61], v[138:141], v[162:165], v[58:61]
	v_mfma_f32_16x16x32_bf16 v[54:57], v[130:133], v[170:173], v[54:57]
	v_mfma_f32_16x16x32_bf16 v[46:49], v[138:141], v[170:173], v[46:49]
	v_mfma_f32_16x16x32_bf16 v[38:41], v[130:133], v[178:181], v[38:41]
	v_mfma_f32_16x16x32_bf16 v[30:33], v[138:141], v[178:181], v[30:33]
	v_mfma_f32_16x16x32_bf16 v[22:25], v[130:133], v[186:189], v[22:25]
	v_mfma_f32_16x16x32_bf16 v[14:17], v[138:141], v[186:189], v[14:17]
	v_mfma_f32_16x16x32_bf16 v[62:65], v[134:137], v[166:169], v[62:65]
	v_mfma_f32_16x16x32_bf16 v[58:61], v[142:145], v[166:169], v[58:61]
	v_mfma_f32_16x16x32_bf16 v[54:57], v[134:137], v[174:177], v[54:57]
	v_mfma_f32_16x16x32_bf16 v[46:49], v[142:145], v[174:177], v[46:49]
	v_mfma_f32_16x16x32_bf16 v[38:41], v[134:137], v[182:185], v[38:41]
	v_mfma_f32_16x16x32_bf16 v[30:33], v[142:145], v[182:185], v[30:33]
	v_mfma_f32_16x16x32_bf16 v[22:25], v[134:137], v[190:193], v[22:25]
	v_mfma_f32_16x16x32_bf16 v[14:17], v[142:145], v[190:193], v[14:17]
	v_mfma_f32_16x16x32_bf16 v[50:53], v[146:149], v[162:165], v[50:53]
	v_mfma_f32_16x16x32_bf16 v[42:45], v[154:157], v[162:165], v[42:45]
	v_mfma_f32_16x16x32_bf16 v[34:37], v[146:149], v[170:173], v[34:37]
	v_mfma_f32_16x16x32_bf16 v[26:29], v[154:157], v[170:173], v[26:29]
	v_mfma_f32_16x16x32_bf16 v[18:21], v[146:149], v[178:181], v[18:21]
	v_mfma_f32_16x16x32_bf16 v[10:13], v[154:157], v[178:181], v[10:13]
	v_mfma_f32_16x16x32_bf16 v[6:9], v[146:149], v[186:189], v[6:9]
	v_mfma_f32_16x16x32_bf16 v[2:5], v[154:157], v[186:189], v[2:5]
	v_mfma_f32_16x16x32_bf16 v[50:53], v[150:153], v[166:169], v[50:53]
	v_mfma_f32_16x16x32_bf16 v[42:45], v[158:161], v[166:169], v[42:45]
	v_mfma_f32_16x16x32_bf16 v[34:37], v[150:153], v[174:177], v[34:37]
	v_mfma_f32_16x16x32_bf16 v[26:29], v[158:161], v[174:177], v[26:29]
	v_mfma_f32_16x16x32_bf16 v[18:21], v[150:153], v[182:185], v[18:21]
	v_mfma_f32_16x16x32_bf16 v[10:13], v[158:161], v[182:185], v[10:13]
	v_mfma_f32_16x16x32_bf16 v[6:9], v[150:153], v[190:193], v[6:9]
	v_mfma_f32_16x16x32_bf16 v[2:5], v[158:161], v[190:193], v[2:5]
	s_barrier
	s_mov_b64 s[40:41], 0x100
	s_mov_b64 s[38:39], 0
	s_mov_b64 s[42:43], -1
	s_and_b64 vcc, exec, s[44:45]
	s_cbranch_vccnz .LBB0_394

.LBB0_390:
	s_add_u32 s71, s71, 0x100
	s_addc_u32 s72, s72, 0
	s_and_b64 s[46:47], s[42:43], exec
	s_cselect_b32 s47, s23, s72
	s_cselect_b32 s46, s69, s71
	s_add_u32 s40, s30, s40
	s_addc_u32 s41, s31, s41
	s_add_u32 s71, s40, 0x100
	s_addc_u32 s72, s41, 0
	s_waitcnt lgkmcnt(0)
	s_and_b64 s[40:41], s[42:43], exec
	s_cselect_b32 s41, s21, s72
	s_cselect_b32 s40, s70, s71
	s_barrier
	s_waitcnt lgkmcnt(0)
	v_mfma_f32_16x16x32_bf16 v[126:129], v[146:149], v[186:189], v[126:129]
	v_mfma_f32_16x16x32_bf16 v[122:125], v[154:157], v[186:189], v[122:125]
	v_mfma_f32_16x16x32_bf16 v[118:121], v[146:149], v[178:181], v[118:121]
	v_mfma_f32_16x16x32_bf16 v[110:113], v[154:157], v[178:181], v[110:113]
	v_mfma_f32_16x16x32_bf16 v[102:105], v[146:149], v[170:173], v[102:105]
	v_mfma_f32_16x16x32_bf16 v[94:97], v[154:157], v[170:173], v[94:97]
	v_mfma_f32_16x16x32_bf16 v[86:89], v[146:149], v[162:165], v[86:89]
	v_mfma_f32_16x16x32_bf16 v[78:81], v[154:157], v[162:165], v[78:81]
	v_mfma_f32_16x16x32_bf16 v[126:129], v[150:153], v[190:193], v[126:129]
	v_mfma_f32_16x16x32_bf16 v[122:125], v[158:161], v[190:193], v[122:125]
	v_mfma_f32_16x16x32_bf16 v[118:121], v[150:153], v[182:185], v[118:121]
	v_mfma_f32_16x16x32_bf16 v[110:113], v[158:161], v[182:185], v[110:113]
	v_mfma_f32_16x16x32_bf16 v[102:105], v[150:153], v[174:177], v[102:105]
	v_mfma_f32_16x16x32_bf16 v[94:97], v[158:161], v[174:177], v[94:97]
	v_mfma_f32_16x16x32_bf16 v[86:89], v[150:153], v[166:169], v[86:89]
	v_mfma_f32_16x16x32_bf16 v[78:81], v[158:161], v[166:169], v[78:81]
	v_mfma_f32_16x16x32_bf16 v[114:117], v[130:133], v[186:189], v[114:117]
	v_mfma_f32_16x16x32_bf16 v[106:109], v[138:141], v[186:189], v[106:109]
	v_mfma_f32_16x16x32_bf16 v[98:101], v[130:133], v[178:181], v[98:101]
	v_mfma_f32_16x16x32_bf16 v[90:93], v[138:141], v[178:181], v[90:93]
	v_mfma_f32_16x16x32_bf16 v[82:85], v[130:133], v[170:173], v[82:85]
	v_mfma_f32_16x16x32_bf16 v[74:77], v[138:141], v[170:173], v[74:77]
	v_mfma_f32_16x16x32_bf16 v[70:73], v[130:133], v[162:165], v[70:73]
	v_mfma_f32_16x16x32_bf16 v[66:69], v[138:141], v[162:165], v[66:69]
	v_mfma_f32_16x16x32_bf16 v[114:117], v[134:137], v[190:193], v[114:117]
	v_mfma_f32_16x16x32_bf16 v[106:109], v[142:145], v[190:193], v[106:109]
	v_mfma_f32_16x16x32_bf16 v[98:101], v[134:137], v[182:185], v[98:101]
	v_mfma_f32_16x16x32_bf16 v[90:93], v[142:145], v[182:185], v[90:93]
	v_mfma_f32_16x16x32_bf16 v[82:85], v[134:137], v[174:177], v[82:85]
	v_mfma_f32_16x16x32_bf16 v[74:77], v[142:145], v[174:177], v[74:77]
	v_mfma_f32_16x16x32_bf16 v[70:73], v[134:137], v[166:169], v[70:73]
	v_mfma_f32_16x16x32_bf16 v[66:69], v[142:145], v[166:169], v[66:69]
	s_barrier
	s_mov_b32 m0, s53
	v_lshl_add_u64 v[216:217], s[40:41], 0, v[202:203]
	s_add_u32 s42, s40, 0x10000
	ds_read_b128 v[186:189], v220 offset:16384
	ds_read_b128 v[190:193], v220 offset:17408
	ds_read_b128 v[178:181], v220 offset:18432
	ds_read_b128 v[182:185], v220 offset:19456
	ds_read_b128 v[170:173], v220 offset:20480
	ds_read_b128 v[174:177], v220 offset:21504
	ds_read_b128 v[162:165], v220 offset:22528
	ds_read_b128 v[166:169], v220 offset:23552
	global_load_lds_dwordx4 v[216:217], off
	v_lshl_add_u64 v[214:215], s[40:41], 0, v[206:207]
	s_mov_b32 m0, s54
	s_addc_u32 s43, s41, 0
	global_load_lds_dwordx4 v[214:215], off
	v_lshl_add_u64 v[210:211], s[42:43], 0, v[202:203]
	s_mov_b32 m0, s55
	v_lshl_add_u64 v[212:213], s[46:47], 0, v[204:205]
	global_load_lds_dwordx4 v[210:211], off
	v_lshl_add_u64 v[210:211], s[42:43], 0, v[206:207]
	s_mov_b32 m0, s56
	s_mov_b64 s[42:43], -1
	global_load_lds_dwordx4 v[210:211], off
	v_lshl_add_u64 v[210:211], s[46:47], 0, v[200:201]
	s_mov_b32 m0, s29
	s_and_b64 vcc, exec, s[44:45]
	global_load_lds_dwordx4 v[210:211], off
	s_mov_b32 m0, s57
	s_nop 0
	global_load_lds_dwordx4 v[212:213], off
	s_cbranch_vccz .LBB0_392
	s_waitcnt vmcnt(8)
	s_mov_b64 s[42:43], 0

.LBB0_445:
	s_waitcnt lgkmcnt(0)
	s_barrier
	s_waitcnt lgkmcnt(0)
	v_mfma_f32_16x16x32_bf16 v[30:33], v[66:69], v[106:109], v[30:33]
	v_mfma_f32_16x16x32_bf16 v[26:29], v[74:77], v[106:109], v[26:29]
	v_mfma_f32_16x16x32_bf16 v[22:25], v[66:69], v[98:101], v[22:25]
	v_mfma_f32_16x16x32_bf16 v[18:21], v[74:77], v[98:101], v[18:21]
	v_mfma_f32_16x16x32_bf16 v[14:17], v[66:69], v[90:93], v[14:17]
	v_mfma_f32_16x16x32_bf16 v[10:13], v[74:77], v[90:93], v[10:13]
	v_mfma_f32_16x16x32_bf16 v[6:9], v[66:69], v[82:85], v[6:9]
	v_mfma_f32_16x16x32_bf16 v[2:5], v[74:77], v[82:85], v[2:5]
	v_mfma_f32_16x16x32_bf16 v[30:33], v[70:73], v[110:113], v[30:33]
	v_mfma_f32_16x16x32_bf16 v[26:29], v[78:81], v[110:113], v[26:29]
	v_mfma_f32_16x16x32_bf16 v[22:25], v[70:73], v[102:105], v[22:25]
	v_mfma_f32_16x16x32_bf16 v[18:21], v[78:81], v[102:105], v[18:21]
	v_mfma_f32_16x16x32_bf16 v[14:17], v[70:73], v[94:97], v[14:17]
	v_mfma_f32_16x16x32_bf16 v[10:13], v[78:81], v[94:97], v[10:13]
	v_mfma_f32_16x16x32_bf16 v[6:9], v[70:73], v[86:89], v[6:9]
	v_mfma_f32_16x16x32_bf16 v[2:5], v[78:81], v[86:89], v[2:5]
	s_barrier
	s_add_i32 s30, 0, 0x18000
	v_add_u32_e32 v78, s30, v141
	ds_read_b128 v[66:69], v78
	ds_read_b128 v[70:73], v78 offset:1024
	ds_read_b128 v[74:77], v78 offset:2048
	ds_read_b128 v[78:81], v78 offset:3072
	s_add_u32 s28, s28, 0x28000
	s_addc_u32 s29, s29, 0
	s_mov_b32 m0, s47
	v_lshl_add_u64 v[144:145], s[28:29], 0, v[120:121]
	ds_read_b128 v[82:85], v143 offset:32768
	ds_read_b128 v[86:89], v143 offset:33792
	ds_read_b128 v[90:93], v143 offset:34816
	ds_read_b128 v[94:97], v143 offset:35840
	ds_read_b128 v[98:101], v143 offset:36864
	ds_read_b128 v[102:105], v143 offset:37888
	ds_read_b128 v[106:109], v143 offset:38912
	ds_read_b128 v[110:113], v143 offset:39936
	global_load_lds_dwordx4 v[144:145], off
	v_lshl_add_u64 v[144:145], s[28:29], 0, v[116:117]
	s_mov_b32 m0, s48
	s_nop 0
	global_load_lds_dwordx4 v[144:145], off
	s_waitcnt vmcnt(8)
	s_waitcnt lgkmcnt(0)
	s_barrier
	s_waitcnt lgkmcnt(0)
	v_mfma_f32_16x16x32_bf16 v[62:65], v[66:69], v[82:85], v[62:65]
	v_mfma_f32_16x16x32_bf16 v[58:61], v[74:77], v[82:85], v[58:61]
	v_mfma_f32_16x16x32_bf16 v[54:57], v[66:69], v[90:93], v[54:57]
	v_mfma_f32_16x16x32_bf16 v[50:53], v[74:77], v[90:93], v[50:53]
	v_mfma_f32_16x16x32_bf16 v[46:49], v[66:69], v[98:101], v[46:49]
	v_mfma_f32_16x16x32_bf16 v[42:45], v[74:77], v[98:101], v[42:45]
	v_mfma_f32_16x16x32_bf16 v[38:41], v[66:69], v[106:109], v[38:41]
	v_mfma_f32_16x16x32_bf16 v[34:37], v[74:77], v[106:109], v[34:37]
	v_mfma_f32_16x16x32_bf16 v[62:65], v[70:73], v[86:89], v[62:65]
	v_mfma_f32_16x16x32_bf16 v[58:61], v[78:81], v[86:89], v[58:61]
	v_mfma_f32_16x16x32_bf16 v[54:57], v[70:73], v[94:97], v[54:57]
	v_mfma_f32_16x16x32_bf16 v[50:53], v[78:81], v[94:97], v[50:53]
	v_mfma_f32_16x16x32_bf16 v[46:49], v[70:73], v[102:105], v[46:49]
	v_mfma_f32_16x16x32_bf16 v[42:45], v[78:81], v[102:105], v[42:45]
	v_mfma_f32_16x16x32_bf16 v[38:41], v[70:73], v[110:113], v[38:41]
	v_mfma_f32_16x16x32_bf16 v[34:37], v[78:81], v[110:113], v[34:37]
	s_barrier
	s_add_i32 s28, s30, s40
	v_lshl_add_u64 v[138:139], v[138:139], 0, s[4:5]
	s_mov_b32 m0, s28
	ds_read_b128 v[82:85], v143 offset:49152
	ds_read_b128 v[86:89], v143 offset:50176
	ds_read_b128 v[90:93], v143 offset:51200
	ds_read_b128 v[94:97], v143 offset:52224
	ds_read_b128 v[98:101], v143 offset:53248
	ds_read_b128 v[102:105], v143 offset:54272
	ds_read_b128 v[106:109], v143 offset:55296
	ds_read_b128 v[110:113], v143 offset:56320
	global_load_lds_dwordx4 v[138:139], off
	s_add_i32 m0, s28, 0x2000
	s_add_u32 s26, s26, 0x20080
	v_lshl_add_u64 v[136:137], v[136:137], 0, s[4:5]
	s_addc_u32 s27, s27, 0
	global_load_lds_dwordx4 v[136:137], off
	v_lshl_add_u64 v[136:137], s[26:27], 0, v[118:119]
	s_mov_b32 m0, s53
	v_lshl_add_u64 v[132:133], v[132:133], 0, s[4:5]
	global_load_lds_dwordx4 v[136:137], off
	v_lshl_add_u64 v[136:137], s[26:27], 0, v[114:115]
	s_mov_b32 m0, s54
	s_nop 0
	global_load_lds_dwordx4 v[136:137], off
	s_mov_b32 m0, s51
	s_nop 0
	global_load_lds_dwordx4 v[132:133], off
	v_lshl_add_u64 v[132:133], v[134:135], 0, s[4:5]
	s_mov_b32 m0, s52
	s_nop 0
	global_load_lds_dwordx4 v[132:133], off
	s_waitcnt vmcnt(8)
	s_waitcnt lgkmcnt(0)
	s_barrier
	s_waitcnt lgkmcnt(0)
	v_mfma_f32_16x16x32_bf16 v[30:33], v[66:69], v[82:85], v[30:33]
	v_mfma_f32_16x16x32_bf16 v[26:29], v[74:77], v[82:85], v[26:29]
	v_mfma_f32_16x16x32_bf16 v[22:25], v[66:69], v[90:93], v[22:25]
	v_mfma_f32_16x16x32_bf16 v[18:21], v[74:77], v[90:93], v[18:21]
	v_mfma_f32_16x16x32_bf16 v[14:17], v[66:69], v[98:101], v[14:17]
	v_mfma_f32_16x16x32_bf16 v[10:13], v[74:77], v[98:101], v[10:13]
	v_mfma_f32_16x16x32_bf16 v[6:9], v[66:69], v[106:109], v[6:9]
	v_mfma_f32_16x16x32_bf16 v[2:5], v[74:77], v[106:109], v[2:5]
	v_mfma_f32_16x16x32_bf16 v[30:33], v[70:73], v[86:89], v[30:33]
	v_mfma_f32_16x16x32_bf16 v[26:29], v[78:81], v[86:89], v[26:29]
	v_mfma_f32_16x16x32_bf16 v[22:25], v[70:73], v[94:97], v[22:25]
	v_mfma_f32_16x16x32_bf16 v[18:21], v[78:81], v[94:97], v[18:21]
	v_mfma_f32_16x16x32_bf16 v[14:17], v[70:73], v[102:105], v[14:17]
	v_mfma_f32_16x16x32_bf16 v[10:13], v[78:81], v[102:105], v[10:13]
	v_mfma_f32_16x16x32_bf16 v[6:9], v[70:73], v[110:113], v[6:9]
	v_mfma_f32_16x16x32_bf16 v[2:5], v[78:81], v[110:113], v[2:5]
	s_barrier
	s_add_i32 s65, s65, 2
	s_add_u32 s22, s22, 0x100
	s_addc_u32 s23, s23, 0
	s_cmp_gt_u32 s65, 5
	s_cbranch_scc1 .LBB0_441

.LBB0_450:
	s_add_u32 s26, s6, s22
	s_addc_u32 s27, s7, s23
	s_add_u32 s26, s26, 0x100
	s_addc_u32 s27, s27, 0
	s_add_u32 s34, s63, s22
	s_addc_u32 s35, s64, s23
	s_waitcnt lgkmcnt(0)
	s_cmpk_eq_i32 s22, 0x300
	s_cselect_b32 s29, s17, s27
	s_cselect_b32 s28, s16, s26
	s_cselect_b32 s27, s61, s35
	s_cselect_b32 s26, s62, s34
	s_barrier
	s_waitcnt lgkmcnt(0)
	v_mfma_f32_16x16x32_bf16 v[62:65], v[66:69], v[106:109], v[62:65]
	v_mfma_f32_16x16x32_bf16 v[58:61], v[74:77], v[106:109], v[58:61]
	v_mfma_f32_16x16x32_bf16 v[54:57], v[66:69], v[98:101], v[54:57]
	v_mfma_f32_16x16x32_bf16 v[50:53], v[74:77], v[98:101], v[50:53]
	v_mfma_f32_16x16x32_bf16 v[46:49], v[66:69], v[90:93], v[46:49]
	v_mfma_f32_16x16x32_bf16 v[42:45], v[74:77], v[90:93], v[42:45]
	v_mfma_f32_16x16x32_bf16 v[38:41], v[66:69], v[82:85], v[38:41]
	v_mfma_f32_16x16x32_bf16 v[34:37], v[74:77], v[82:85], v[34:37]
	v_mfma_f32_16x16x32_bf16 v[62:65], v[70:73], v[110:113], v[62:65]
	v_mfma_f32_16x16x32_bf16 v[58:61], v[78:81], v[110:113], v[58:61]
	v_mfma_f32_16x16x32_bf16 v[54:57], v[70:73], v[102:105], v[54:57]
	v_mfma_f32_16x16x32_bf16 v[50:53], v[78:81], v[102:105], v[50:53]
	v_mfma_f32_16x16x32_bf16 v[46:49], v[70:73], v[94:97], v[46:49]
	v_mfma_f32_16x16x32_bf16 v[42:45], v[78:81], v[94:97], v[42:45]
	v_mfma_f32_16x16x32_bf16 v[38:41], v[70:73], v[86:89], v[38:41]
	v_mfma_f32_16x16x32_bf16 v[34:37], v[78:81], v[86:89], v[34:37]
	s_barrier
	s_mov_b32 m0, s42
	v_lshl_add_u64 v[138:139], s[26:27], 0, v[118:119]
	s_add_u32 s34, s26, 0x20000
	ds_read_b128 v[106:109], v143 offset:16384
	ds_read_b128 v[110:113], v143 offset:17408
	ds_read_b128 v[98:101], v143 offset:18432
	ds_read_b128 v[102:105], v143 offset:19456
	ds_read_b128 v[90:93], v143 offset:20480
	ds_read_b128 v[94:97], v143 offset:21504
	ds_read_b128 v[82:85], v143 offset:22528
	ds_read_b128 v[86:89], v143 offset:23552
	global_load_lds_dwordx4 v[138:139], off
	v_lshl_add_u64 v[136:137], s[26:27], 0, v[114:115]
	s_mov_b32 m0, s43
	s_addc_u32 s35, s27, 0
	global_load_lds_dwordx4 v[136:137], off
	v_lshl_add_u64 v[132:133], s[34:35], 0, v[118:119]
	s_mov_b32 m0, s44
	v_lshl_add_u64 v[134:135], s[28:29], 0, v[116:117]
	global_load_lds_dwordx4 v[132:133], off
	v_lshl_add_u64 v[132:133], s[34:35], 0, v[114:115]
	s_mov_b32 m0, s45
	s_mov_b64 s[34:35], -1
	global_load_lds_dwordx4 v[132:133], off
	v_lshl_add_u64 v[132:133], s[28:29], 0, v[120:121]
	s_mov_b32 m0, s41
	s_and_b64 vcc, exec, s[30:31]
	global_load_lds_dwordx4 v[132:133], off
	s_mov_b32 m0, s46
	s_nop 0
	global_load_lds_dwordx4 v[134:135], off
	s_cbranch_vccz .LBB0_452
	s_waitcnt vmcnt(8)
	s_mov_b64 s[34:35], 0

.LBB0_642:
	s_waitcnt lgkmcnt(0)
	s_barrier
	s_waitcnt lgkmcnt(0)
	v_mfma_f32_16x16x32_bf16 v[62:65], v[146:149], v[186:189], v[62:65]
	v_mfma_f32_16x16x32_bf16 v[58:61], v[154:157], v[186:189], v[58:61]
	v_mfma_f32_16x16x32_bf16 v[46:49], v[146:149], v[178:181], v[46:49]
	v_mfma_f32_16x16x32_bf16 v[42:45], v[154:157], v[178:181], v[42:45]
	v_mfma_f32_16x16x32_bf16 v[30:33], v[146:149], v[170:173], v[30:33]
	v_mfma_f32_16x16x32_bf16 v[26:29], v[154:157], v[170:173], v[26:29]
	v_mfma_f32_16x16x32_bf16 v[14:17], v[146:149], v[162:165], v[14:17]
	v_mfma_f32_16x16x32_bf16 v[10:13], v[154:157], v[162:165], v[10:13]
	v_mfma_f32_16x16x32_bf16 v[62:65], v[150:153], v[190:193], v[62:65]
	v_mfma_f32_16x16x32_bf16 v[58:61], v[158:161], v[190:193], v[58:61]
	v_mfma_f32_16x16x32_bf16 v[46:49], v[150:153], v[182:185], v[46:49]
	v_mfma_f32_16x16x32_bf16 v[42:45], v[158:161], v[182:185], v[42:45]
	v_mfma_f32_16x16x32_bf16 v[30:33], v[150:153], v[174:177], v[30:33]
	v_mfma_f32_16x16x32_bf16 v[26:29], v[158:161], v[174:177], v[26:29]
	v_mfma_f32_16x16x32_bf16 v[14:17], v[150:153], v[166:169], v[14:17]
	v_mfma_f32_16x16x32_bf16 v[10:13], v[158:161], v[166:169], v[10:13]
	v_mfma_f32_16x16x32_bf16 v[54:57], v[130:133], v[186:189], v[54:57]
	v_mfma_f32_16x16x32_bf16 v[50:53], v[138:141], v[186:189], v[50:53]
	v_mfma_f32_16x16x32_bf16 v[38:41], v[130:133], v[178:181], v[38:41]
	v_mfma_f32_16x16x32_bf16 v[34:37], v[138:141], v[178:181], v[34:37]
	v_mfma_f32_16x16x32_bf16 v[22:25], v[130:133], v[170:173], v[22:25]
	v_mfma_f32_16x16x32_bf16 v[18:21], v[138:141], v[170:173], v[18:21]
	v_mfma_f32_16x16x32_bf16 v[6:9], v[130:133], v[162:165], v[6:9]
	v_mfma_f32_16x16x32_bf16 v[2:5], v[138:141], v[162:165], v[2:5]
	v_mfma_f32_16x16x32_bf16 v[54:57], v[134:137], v[190:193], v[54:57]
	v_mfma_f32_16x16x32_bf16 v[50:53], v[142:145], v[190:193], v[50:53]
	v_mfma_f32_16x16x32_bf16 v[38:41], v[134:137], v[182:185], v[38:41]
	v_mfma_f32_16x16x32_bf16 v[34:37], v[142:145], v[182:185], v[34:37]
	v_mfma_f32_16x16x32_bf16 v[22:25], v[134:137], v[174:177], v[22:25]
	v_mfma_f32_16x16x32_bf16 v[18:21], v[142:145], v[174:177], v[18:21]
	v_mfma_f32_16x16x32_bf16 v[6:9], v[134:137], v[166:169], v[6:9]
	v_mfma_f32_16x16x32_bf16 v[2:5], v[142:145], v[166:169], v[2:5]
	s_barrier
	s_add_i32 s26, 0, 0x18000
	s_add_i32 s27, 0, 0x1c000
	v_add_u32_e32 v142, s26, v224
	v_add_u32_e32 v158, s27, v224
	ds_read_b128 v[130:133], v142
	ds_read_b128 v[134:137], v142 offset:1024
	ds_read_b128 v[138:141], v142 offset:2048
	ds_read_b128 v[142:145], v142 offset:3072
	ds_read_b128 v[146:149], v158
	ds_read_b128 v[150:153], v158 offset:1024
	ds_read_b128 v[154:157], v158 offset:2048
	ds_read_b128 v[158:161], v158 offset:3072
	s_add_u32 s24, s24, 0x28000
	s_addc_u32 s25, s25, 0
	s_mov_b32 m0, s40
	v_lshl_add_u64 v[230:231], s[24:25], 0, v[204:205]
	ds_read_b128 v[162:165], v228 offset:32768
	ds_read_b128 v[166:169], v228 offset:33792
	ds_read_b128 v[170:173], v228 offset:34816
	ds_read_b128 v[174:177], v228 offset:35840
	ds_read_b128 v[178:181], v228 offset:36864
	ds_read_b128 v[182:185], v228 offset:37888
	ds_read_b128 v[186:189], v228 offset:38912
	ds_read_b128 v[190:193], v228 offset:39936
	global_load_lds_dwordx4 v[230:231], off
	v_lshl_add_u64 v[230:231], s[24:25], 0, v[200:201]
	s_mov_b32 m0, s41
	s_nop 0
	global_load_lds_dwordx4 v[230:231], off
	s_waitcnt vmcnt(8)
	s_waitcnt lgkmcnt(0)
	s_barrier
	s_waitcnt lgkmcnt(0)
	v_mfma_f32_16x16x32_bf16 v[126:129], v[130:133], v[162:165], v[126:129]
	v_mfma_f32_16x16x32_bf16 v[122:125], v[138:141], v[162:165], v[122:125]
	v_mfma_f32_16x16x32_bf16 v[110:113], v[130:133], v[170:173], v[110:113]
	v_mfma_f32_16x16x32_bf16 v[106:109], v[138:141], v[170:173], v[106:109]
	v_mfma_f32_16x16x32_bf16 v[94:97], v[130:133], v[178:181], v[94:97]
	v_mfma_f32_16x16x32_bf16 v[90:93], v[138:141], v[178:181], v[90:93]
	v_mfma_f32_16x16x32_bf16 v[78:81], v[130:133], v[186:189], v[78:81]
	v_mfma_f32_16x16x32_bf16 v[74:77], v[138:141], v[186:189], v[74:77]
	v_mfma_f32_16x16x32_bf16 v[126:129], v[134:137], v[166:169], v[126:129]
	v_mfma_f32_16x16x32_bf16 v[122:125], v[142:145], v[166:169], v[122:125]
	v_mfma_f32_16x16x32_bf16 v[110:113], v[134:137], v[174:177], v[110:113]
	v_mfma_f32_16x16x32_bf16 v[106:109], v[142:145], v[174:177], v[106:109]
	v_mfma_f32_16x16x32_bf16 v[94:97], v[134:137], v[182:185], v[94:97]
	v_mfma_f32_16x16x32_bf16 v[90:93], v[142:145], v[182:185], v[90:93]
	v_mfma_f32_16x16x32_bf16 v[78:81], v[134:137], v[190:193], v[78:81]
	v_mfma_f32_16x16x32_bf16 v[74:77], v[142:145], v[190:193], v[74:77]
	v_mfma_f32_16x16x32_bf16 v[118:121], v[146:149], v[162:165], v[118:121]
	v_mfma_f32_16x16x32_bf16 v[114:117], v[154:157], v[162:165], v[114:117]
	v_mfma_f32_16x16x32_bf16 v[102:105], v[146:149], v[170:173], v[102:105]
	v_mfma_f32_16x16x32_bf16 v[98:101], v[154:157], v[170:173], v[98:101]
	v_mfma_f32_16x16x32_bf16 v[86:89], v[146:149], v[178:181], v[86:89]
	v_mfma_f32_16x16x32_bf16 v[82:85], v[154:157], v[178:181], v[82:85]
	v_mfma_f32_16x16x32_bf16 v[70:73], v[146:149], v[186:189], v[70:73]
	v_mfma_f32_16x16x32_bf16 v[66:69], v[154:157], v[186:189], v[66:69]
	v_mfma_f32_16x16x32_bf16 v[118:121], v[150:153], v[166:169], v[118:121]
	v_mfma_f32_16x16x32_bf16 v[114:117], v[158:161], v[166:169], v[114:117]
	v_mfma_f32_16x16x32_bf16 v[102:105], v[150:153], v[174:177], v[102:105]
	v_mfma_f32_16x16x32_bf16 v[98:101], v[158:161], v[174:177], v[98:101]
	v_mfma_f32_16x16x32_bf16 v[86:89], v[150:153], v[182:185], v[86:89]
	v_mfma_f32_16x16x32_bf16 v[82:85], v[158:161], v[182:185], v[82:85]
	v_mfma_f32_16x16x32_bf16 v[70:73], v[150:153], v[190:193], v[70:73]
	v_mfma_f32_16x16x32_bf16 v[66:69], v[158:161], v[190:193], v[66:69]
	s_barrier
	s_add_i32 s24, s26, s33
	v_lshl_add_u64 v[222:223], v[222:223], 0, s[2:3]
	s_mov_b32 m0, s24
	ds_read_b128 v[162:165], v228 offset:49152
	ds_read_b128 v[166:169], v228 offset:50176
	ds_read_b128 v[170:173], v228 offset:51200
	ds_read_b128 v[174:177], v228 offset:52224
	ds_read_b128 v[178:181], v228 offset:53248
	ds_read_b128 v[182:185], v228 offset:54272
	ds_read_b128 v[186:189], v228 offset:55296
	ds_read_b128 v[190:193], v228 offset:56320
	global_load_lds_dwordx4 v[222:223], off
	s_add_i32 m0, s24, 0x2000
	s_add_u32 s22, s22, 0x28080
	v_lshl_add_u64 v[220:221], v[220:221], 0, s[2:3]
	s_addc_u32 s23, s23, 0
	s_add_i32 s24, s27, s33
	global_load_lds_dwordx4 v[220:221], off
	v_lshl_add_u64 v[220:221], s[22:23], 0, v[202:203]
	s_mov_b32 m0, s24
	v_lshl_add_u64 v[216:217], v[216:217], 0, s[2:3]
	global_load_lds_dwordx4 v[220:221], off
	v_lshl_add_u64 v[220:221], s[22:23], 0, v[196:197]
	s_add_i32 m0, s24, 0x2000
	s_nop 0
	global_load_lds_dwordx4 v[220:221], off
	s_mov_b32 m0, s42
	s_nop 0
	global_load_lds_dwordx4 v[216:217], off
	v_lshl_add_u64 v[216:217], v[218:219], 0, s[2:3]
	s_mov_b32 m0, s43
	s_nop 0
	global_load_lds_dwordx4 v[216:217], off
	s_waitcnt vmcnt(8)
	s_waitcnt lgkmcnt(0)
	s_barrier
	s_waitcnt lgkmcnt(0)
	v_mfma_f32_16x16x32_bf16 v[62:65], v[130:133], v[162:165], v[62:65]
	v_mfma_f32_16x16x32_bf16 v[58:61], v[138:141], v[162:165], v[58:61]
	v_mfma_f32_16x16x32_bf16 v[46:49], v[130:133], v[170:173], v[46:49]
	v_mfma_f32_16x16x32_bf16 v[42:45], v[138:141], v[170:173], v[42:45]
	v_mfma_f32_16x16x32_bf16 v[30:33], v[130:133], v[178:181], v[30:33]
	v_mfma_f32_16x16x32_bf16 v[26:29], v[138:141], v[178:181], v[26:29]
	v_mfma_f32_16x16x32_bf16 v[14:17], v[130:133], v[186:189], v[14:17]
	v_mfma_f32_16x16x32_bf16 v[10:13], v[138:141], v[186:189], v[10:13]
	v_mfma_f32_16x16x32_bf16 v[62:65], v[134:137], v[166:169], v[62:65]
	v_mfma_f32_16x16x32_bf16 v[58:61], v[142:145], v[166:169], v[58:61]
	v_mfma_f32_16x16x32_bf16 v[46:49], v[134:137], v[174:177], v[46:49]
	v_mfma_f32_16x16x32_bf16 v[42:45], v[142:145], v[174:177], v[42:45]
	v_mfma_f32_16x16x32_bf16 v[30:33], v[134:137], v[182:185], v[30:33]
	v_mfma_f32_16x16x32_bf16 v[26:29], v[142:145], v[182:185], v[26:29]
	v_mfma_f32_16x16x32_bf16 v[14:17], v[134:137], v[190:193], v[14:17]
	v_mfma_f32_16x16x32_bf16 v[10:13], v[142:145], v[190:193], v[10:13]
	v_mfma_f32_16x16x32_bf16 v[54:57], v[146:149], v[162:165], v[54:57]
	v_mfma_f32_16x16x32_bf16 v[50:53], v[154:157], v[162:165], v[50:53]
	v_mfma_f32_16x16x32_bf16 v[38:41], v[146:149], v[170:173], v[38:41]
	v_mfma_f32_16x16x32_bf16 v[34:37], v[154:157], v[170:173], v[34:37]
	v_mfma_f32_16x16x32_bf16 v[22:25], v[146:149], v[178:181], v[22:25]
	v_mfma_f32_16x16x32_bf16 v[18:21], v[154:157], v[178:181], v[18:21]
	v_mfma_f32_16x16x32_bf16 v[6:9], v[146:149], v[186:189], v[6:9]
	v_mfma_f32_16x16x32_bf16 v[2:5], v[154:157], v[186:189], v[2:5]
	v_mfma_f32_16x16x32_bf16 v[54:57], v[150:153], v[166:169], v[54:57]
	v_mfma_f32_16x16x32_bf16 v[50:53], v[158:161], v[166:169], v[50:53]
	v_mfma_f32_16x16x32_bf16 v[38:41], v[150:153], v[174:177], v[38:41]
	v_mfma_f32_16x16x32_bf16 v[34:37], v[158:161], v[174:177], v[34:37]
	v_mfma_f32_16x16x32_bf16 v[22:25], v[150:153], v[182:185], v[22:25]
	v_mfma_f32_16x16x32_bf16 v[18:21], v[158:161], v[182:185], v[18:21]
	v_mfma_f32_16x16x32_bf16 v[6:9], v[150:153], v[190:193], v[6:9]
	v_mfma_f32_16x16x32_bf16 v[2:5], v[158:161], v[190:193], v[2:5]
	s_barrier
	s_add_i32 s53, s53, 2
	s_add_u32 s18, s18, 0x100
	s_addc_u32 s19, s19, 0
	s_cmp_gt_u32 s53, 7
	s_cbranch_scc1 .LBB0_636

.LBB0_647:
	s_add_u32 s22, s16, s18
	s_addc_u32 s23, s17, s19
	s_add_u32 s22, s22, 0x100
	s_addc_u32 s23, s23, 0
	s_add_u32 s28, s51, s18
	s_addc_u32 s29, s52, s19
	s_waitcnt lgkmcnt(0)
	s_cmpk_eq_i32 s18, 0x400
	s_cselect_b32 s25, s11, s23
	s_cselect_b32 s24, s10, s22
	s_cselect_b32 s23, s15, s29
	s_cselect_b32 s22, s14, s28
	s_barrier
	s_waitcnt lgkmcnt(0)
	v_mfma_f32_16x16x32_bf16 v[126:129], v[146:149], v[186:189], v[126:129]
	v_mfma_f32_16x16x32_bf16 v[122:125], v[154:157], v[186:189], v[122:125]
	v_mfma_f32_16x16x32_bf16 v[110:113], v[146:149], v[178:181], v[110:113]
	v_mfma_f32_16x16x32_bf16 v[106:109], v[154:157], v[178:181], v[106:109]
	v_mfma_f32_16x16x32_bf16 v[94:97], v[146:149], v[170:173], v[94:97]
	v_mfma_f32_16x16x32_bf16 v[90:93], v[154:157], v[170:173], v[90:93]
	v_mfma_f32_16x16x32_bf16 v[78:81], v[146:149], v[162:165], v[78:81]
	v_mfma_f32_16x16x32_bf16 v[74:77], v[154:157], v[162:165], v[74:77]
	v_mfma_f32_16x16x32_bf16 v[126:129], v[150:153], v[190:193], v[126:129]
	v_mfma_f32_16x16x32_bf16 v[122:125], v[158:161], v[190:193], v[122:125]
	v_mfma_f32_16x16x32_bf16 v[110:113], v[150:153], v[182:185], v[110:113]
	v_mfma_f32_16x16x32_bf16 v[106:109], v[158:161], v[182:185], v[106:109]
	v_mfma_f32_16x16x32_bf16 v[94:97], v[150:153], v[174:177], v[94:97]
	v_mfma_f32_16x16x32_bf16 v[90:93], v[158:161], v[174:177], v[90:93]
	v_mfma_f32_16x16x32_bf16 v[78:81], v[150:153], v[166:169], v[78:81]
	v_mfma_f32_16x16x32_bf16 v[74:77], v[158:161], v[166:169], v[74:77]
	v_mfma_f32_16x16x32_bf16 v[118:121], v[130:133], v[186:189], v[118:121]
	v_mfma_f32_16x16x32_bf16 v[114:117], v[138:141], v[186:189], v[114:117]
	v_mfma_f32_16x16x32_bf16 v[102:105], v[130:133], v[178:181], v[102:105]
	v_mfma_f32_16x16x32_bf16 v[98:101], v[138:141], v[178:181], v[98:101]
	v_mfma_f32_16x16x32_bf16 v[86:89], v[130:133], v[170:173], v[86:89]
	v_mfma_f32_16x16x32_bf16 v[82:85], v[138:141], v[170:173], v[82:85]
	v_mfma_f32_16x16x32_bf16 v[70:73], v[130:133], v[162:165], v[70:73]
	v_mfma_f32_16x16x32_bf16 v[66:69], v[138:141], v[162:165], v[66:69]
	v_mfma_f32_16x16x32_bf16 v[118:121], v[134:137], v[190:193], v[118:121]
	v_mfma_f32_16x16x32_bf16 v[114:117], v[142:145], v[190:193], v[114:117]
	v_mfma_f32_16x16x32_bf16 v[102:105], v[134:137], v[182:185], v[102:105]
	v_mfma_f32_16x16x32_bf16 v[98:101], v[142:145], v[182:185], v[98:101]
	v_mfma_f32_16x16x32_bf16 v[86:89], v[134:137], v[174:177], v[86:89]
	v_mfma_f32_16x16x32_bf16 v[82:85], v[142:145], v[174:177], v[82:85]
	v_mfma_f32_16x16x32_bf16 v[70:73], v[134:137], v[166:169], v[70:73]
	v_mfma_f32_16x16x32_bf16 v[66:69], v[142:145], v[166:169], v[66:69]
	s_barrier
	s_mov_b32 m0, s35
	v_lshl_add_u64 v[222:223], s[22:23], 0, v[202:203]
	s_add_u32 s28, s22, 0x28000
	ds_read_b128 v[186:189], v228 offset:16384
	ds_read_b128 v[190:193], v228 offset:17408
	ds_read_b128 v[178:181], v228 offset:18432
	ds_read_b128 v[182:185], v228 offset:19456
	ds_read_b128 v[170:173], v228 offset:20480
	ds_read_b128 v[174:177], v228 offset:21504
	ds_read_b128 v[162:165], v228 offset:22528
	ds_read_b128 v[166:169], v228 offset:23552
	global_load_lds_dwordx4 v[222:223], off
	v_lshl_add_u64 v[220:221], s[22:23], 0, v[196:197]
	s_mov_b32 m0, s36
	s_addc_u32 s29, s23, 0
	global_load_lds_dwordx4 v[220:221], off
	v_lshl_add_u64 v[216:217], s[28:29], 0, v[202:203]
	s_mov_b32 m0, s37
	v_lshl_add_u64 v[218:219], s[24:25], 0, v[200:201]
	global_load_lds_dwordx4 v[216:217], off
	v_lshl_add_u64 v[216:217], s[28:29], 0, v[196:197]
	s_mov_b32 m0, s38
	s_mov_b64 s[28:29], -1
	global_load_lds_dwordx4 v[216:217], off
	v_lshl_add_u64 v[216:217], s[24:25], 0, v[204:205]
	s_mov_b32 m0, s34
	s_and_b64 vcc, exec, s[26:27]
	global_load_lds_dwordx4 v[216:217], off
	s_mov_b32 m0, s39
	s_nop 0
	global_load_lds_dwordx4 v[218:219], off
	s_cbranch_vccz .LBB0_649
	s_waitcnt vmcnt(8)
	s_mov_b64 s[28:29], 0

.LBB0_772:
	s_waitcnt lgkmcnt(0)
	s_barrier
	s_waitcnt lgkmcnt(0)
	v_mfma_f32_16x16x32_bf16 v[62:65], v[146:149], v[186:189], v[62:65]
	v_mfma_f32_16x16x32_bf16 v[58:61], v[154:157], v[186:189], v[58:61]
	v_mfma_f32_16x16x32_bf16 v[46:49], v[146:149], v[178:181], v[46:49]
	v_mfma_f32_16x16x32_bf16 v[42:45], v[154:157], v[178:181], v[42:45]
	v_mfma_f32_16x16x32_bf16 v[30:33], v[146:149], v[170:173], v[30:33]
	v_mfma_f32_16x16x32_bf16 v[26:29], v[154:157], v[170:173], v[26:29]
	v_mfma_f32_16x16x32_bf16 v[14:17], v[146:149], v[162:165], v[14:17]
	v_mfma_f32_16x16x32_bf16 v[10:13], v[154:157], v[162:165], v[10:13]
	v_mfma_f32_16x16x32_bf16 v[62:65], v[150:153], v[190:193], v[62:65]
	v_mfma_f32_16x16x32_bf16 v[58:61], v[158:161], v[190:193], v[58:61]
	v_mfma_f32_16x16x32_bf16 v[46:49], v[150:153], v[182:185], v[46:49]
	v_mfma_f32_16x16x32_bf16 v[42:45], v[158:161], v[182:185], v[42:45]
	v_mfma_f32_16x16x32_bf16 v[30:33], v[150:153], v[174:177], v[30:33]
	v_mfma_f32_16x16x32_bf16 v[26:29], v[158:161], v[174:177], v[26:29]
	v_mfma_f32_16x16x32_bf16 v[14:17], v[150:153], v[166:169], v[14:17]
	v_mfma_f32_16x16x32_bf16 v[10:13], v[158:161], v[166:169], v[10:13]
	v_mfma_f32_16x16x32_bf16 v[54:57], v[66:69], v[186:189], v[54:57]
	v_mfma_f32_16x16x32_bf16 v[50:53], v[82:85], v[186:189], v[50:53]
	v_mfma_f32_16x16x32_bf16 v[38:41], v[66:69], v[178:181], v[38:41]
	v_mfma_f32_16x16x32_bf16 v[34:37], v[82:85], v[178:181], v[34:37]
	v_mfma_f32_16x16x32_bf16 v[22:25], v[66:69], v[170:173], v[22:25]
	v_mfma_f32_16x16x32_bf16 v[18:21], v[82:85], v[170:173], v[18:21]
	v_mfma_f32_16x16x32_bf16 v[6:9], v[66:69], v[162:165], v[6:9]
	v_mfma_f32_16x16x32_bf16 v[2:5], v[82:85], v[162:165], v[2:5]
	v_mfma_f32_16x16x32_bf16 v[54:57], v[74:77], v[190:193], v[54:57]
	v_mfma_f32_16x16x32_bf16 v[50:53], v[86:89], v[190:193], v[50:53]
	v_mfma_f32_16x16x32_bf16 v[38:41], v[74:77], v[182:185], v[38:41]
	v_mfma_f32_16x16x32_bf16 v[34:37], v[86:89], v[182:185], v[34:37]
	v_mfma_f32_16x16x32_bf16 v[22:25], v[74:77], v[174:177], v[22:25]
	v_mfma_f32_16x16x32_bf16 v[18:21], v[86:89], v[174:177], v[18:21]
	v_mfma_f32_16x16x32_bf16 v[6:9], v[74:77], v[166:169], v[6:9]
	v_mfma_f32_16x16x32_bf16 v[2:5], v[86:89], v[166:169], v[2:5]
	s_barrier
	s_add_i32 s40, 0, 0x18000
	s_add_i32 s41, 0, 0x1c000
	v_add_u32_e32 v86, s40, v199
	v_add_u32_e32 v158, s41, v199
	ds_read_b128 v[66:69], v86
	ds_read_b128 v[74:77], v86 offset:1024
	ds_read_b128 v[82:85], v86 offset:2048
	ds_read_b128 v[86:89], v86 offset:3072
	ds_read_b128 v[146:149], v158
	ds_read_b128 v[150:153], v158 offset:1024
	ds_read_b128 v[154:157], v158 offset:2048
	ds_read_b128 v[158:161], v158 offset:3072
	s_add_u32 s38, s38, 0x40000
	s_addc_u32 s39, s39, 0
	s_mov_b32 m0, s51
	v_lshl_add_u64 v[228:229], s[38:39], 0, v[194:195]
	ds_read_b128 v[162:165], v227 offset:32768
	ds_read_b128 v[166:169], v227 offset:33792
	ds_read_b128 v[170:173], v227 offset:34816
	ds_read_b128 v[174:177], v227 offset:35840
	ds_read_b128 v[178:181], v227 offset:36864
	ds_read_b128 v[182:185], v227 offset:37888
	ds_read_b128 v[186:189], v227 offset:38912
	ds_read_b128 v[190:193], v227 offset:39936
	global_load_lds_dwordx4 v[228:229], off
	v_lshl_add_u64 v[228:229], s[38:39], 0, v[200:201]
	s_mov_b32 m0, s52
	s_nop 0
	global_load_lds_dwordx4 v[228:229], off
	s_waitcnt vmcnt(8)
	s_waitcnt lgkmcnt(0)
	s_barrier
	s_waitcnt lgkmcnt(0)
	v_mfma_f32_16x16x32_bf16 v[142:145], v[66:69], v[162:165], v[142:145]
	v_mfma_f32_16x16x32_bf16 v[138:141], v[82:85], v[162:165], v[138:141]
	v_mfma_f32_16x16x32_bf16 v[126:129], v[66:69], v[170:173], v[126:129]
	v_mfma_f32_16x16x32_bf16 v[122:125], v[82:85], v[170:173], v[122:125]
	v_mfma_f32_16x16x32_bf16 v[110:113], v[66:69], v[178:181], v[110:113]
	v_mfma_f32_16x16x32_bf16 v[106:109], v[82:85], v[178:181], v[106:109]
	v_mfma_f32_16x16x32_bf16 v[94:97], v[66:69], v[186:189], v[94:97]
	v_mfma_f32_16x16x32_bf16 v[90:93], v[82:85], v[186:189], v[90:93]
	v_mfma_f32_16x16x32_bf16 v[142:145], v[74:77], v[166:169], v[142:145]
	v_mfma_f32_16x16x32_bf16 v[138:141], v[86:89], v[166:169], v[138:141]
	v_mfma_f32_16x16x32_bf16 v[126:129], v[74:77], v[174:177], v[126:129]
	v_mfma_f32_16x16x32_bf16 v[122:125], v[86:89], v[174:177], v[122:125]
	v_mfma_f32_16x16x32_bf16 v[110:113], v[74:77], v[182:185], v[110:113]
	v_mfma_f32_16x16x32_bf16 v[106:109], v[86:89], v[182:185], v[106:109]
	v_mfma_f32_16x16x32_bf16 v[94:97], v[74:77], v[190:193], v[94:97]
	v_mfma_f32_16x16x32_bf16 v[90:93], v[86:89], v[190:193], v[90:93]
	v_mfma_f32_16x16x32_bf16 v[134:137], v[146:149], v[162:165], v[134:137]
	v_mfma_f32_16x16x32_bf16 v[130:133], v[154:157], v[162:165], v[130:133]
	v_mfma_f32_16x16x32_bf16 v[118:121], v[146:149], v[170:173], v[118:121]
	v_mfma_f32_16x16x32_bf16 v[114:117], v[154:157], v[170:173], v[114:117]
	v_mfma_f32_16x16x32_bf16 v[102:105], v[146:149], v[178:181], v[102:105]
	v_mfma_f32_16x16x32_bf16 v[98:101], v[154:157], v[178:181], v[98:101]
	v_mfma_f32_16x16x32_bf16 v[78:81], v[146:149], v[186:189], v[78:81]
	v_mfma_f32_16x16x32_bf16 v[70:73], v[154:157], v[186:189], v[70:73]
	v_mfma_f32_16x16x32_bf16 v[134:137], v[150:153], v[166:169], v[134:137]
	v_mfma_f32_16x16x32_bf16 v[130:133], v[158:161], v[166:169], v[130:133]
	v_mfma_f32_16x16x32_bf16 v[118:121], v[150:153], v[174:177], v[118:121]
	v_mfma_f32_16x16x32_bf16 v[114:117], v[158:161], v[174:177], v[114:117]
	v_mfma_f32_16x16x32_bf16 v[102:105], v[150:153], v[182:185], v[102:105]
	v_mfma_f32_16x16x32_bf16 v[98:101], v[158:161], v[182:185], v[98:101]
	v_mfma_f32_16x16x32_bf16 v[78:81], v[150:153], v[190:193], v[78:81]
	v_mfma_f32_16x16x32_bf16 v[70:73], v[158:161], v[190:193], v[70:73]
	s_barrier
	s_add_i32 s38, s40, s45
	v_lshl_add_u64 v[222:223], v[222:223], 0, s[12:13]
	s_mov_b32 m0, s38
	ds_read_b128 v[162:165], v227 offset:49152
	ds_read_b128 v[166:169], v227 offset:50176
	ds_read_b128 v[170:173], v227 offset:51200
	ds_read_b128 v[174:177], v227 offset:52224
	ds_read_b128 v[178:181], v227 offset:53248
	ds_read_b128 v[182:185], v227 offset:54272
	ds_read_b128 v[186:189], v227 offset:55296
	ds_read_b128 v[190:193], v227 offset:56320
	global_load_lds_dwordx4 v[222:223], off
	s_add_i32 m0, s38, 0x2000
	s_add_u32 s36, s36, 0x40080
	v_lshl_add_u64 v[220:221], v[220:221], 0, s[12:13]
	s_addc_u32 s37, s37, 0
	s_add_i32 s38, s41, s45
	global_load_lds_dwordx4 v[220:221], off
	v_lshl_add_u64 v[220:221], s[36:37], 0, v[196:197]
	s_mov_b32 m0, s38
	v_lshl_add_u64 v[216:217], v[216:217], 0, s[12:13]
	global_load_lds_dwordx4 v[220:221], off
	v_lshl_add_u64 v[220:221], s[36:37], 0, v[202:203]
	s_add_i32 m0, s38, 0x2000
	s_nop 0
	global_load_lds_dwordx4 v[220:221], off
	s_mov_b32 m0, s53
	s_nop 0
	global_load_lds_dwordx4 v[216:217], off
	v_lshl_add_u64 v[216:217], v[218:219], 0, s[12:13]
	s_mov_b32 m0, s54
	s_nop 0
	global_load_lds_dwordx4 v[216:217], off
	s_waitcnt vmcnt(8)
	s_waitcnt lgkmcnt(0)
	s_barrier
	s_waitcnt lgkmcnt(0)
	v_mfma_f32_16x16x32_bf16 v[62:65], v[66:69], v[162:165], v[62:65]
	v_mfma_f32_16x16x32_bf16 v[58:61], v[82:85], v[162:165], v[58:61]
	v_mfma_f32_16x16x32_bf16 v[46:49], v[66:69], v[170:173], v[46:49]
	v_mfma_f32_16x16x32_bf16 v[42:45], v[82:85], v[170:173], v[42:45]
	v_mfma_f32_16x16x32_bf16 v[30:33], v[66:69], v[178:181], v[30:33]
	v_mfma_f32_16x16x32_bf16 v[26:29], v[82:85], v[178:181], v[26:29]
	v_mfma_f32_16x16x32_bf16 v[14:17], v[66:69], v[186:189], v[14:17]
	v_mfma_f32_16x16x32_bf16 v[10:13], v[82:85], v[186:189], v[10:13]
	v_mfma_f32_16x16x32_bf16 v[62:65], v[74:77], v[166:169], v[62:65]
	v_mfma_f32_16x16x32_bf16 v[58:61], v[86:89], v[166:169], v[58:61]
	v_mfma_f32_16x16x32_bf16 v[46:49], v[74:77], v[174:177], v[46:49]
	v_mfma_f32_16x16x32_bf16 v[42:45], v[86:89], v[174:177], v[42:45]
	v_mfma_f32_16x16x32_bf16 v[30:33], v[74:77], v[182:185], v[30:33]
	v_mfma_f32_16x16x32_bf16 v[26:29], v[86:89], v[182:185], v[26:29]
	v_mfma_f32_16x16x32_bf16 v[14:17], v[74:77], v[190:193], v[14:17]
	v_mfma_f32_16x16x32_bf16 v[10:13], v[86:89], v[190:193], v[10:13]
	v_mfma_f32_16x16x32_bf16 v[54:57], v[146:149], v[162:165], v[54:57]
	v_mfma_f32_16x16x32_bf16 v[50:53], v[154:157], v[162:165], v[50:53]
	v_mfma_f32_16x16x32_bf16 v[38:41], v[146:149], v[170:173], v[38:41]
	v_mfma_f32_16x16x32_bf16 v[34:37], v[154:157], v[170:173], v[34:37]
	v_mfma_f32_16x16x32_bf16 v[22:25], v[146:149], v[178:181], v[22:25]
	v_mfma_f32_16x16x32_bf16 v[18:21], v[154:157], v[178:181], v[18:21]
	v_mfma_f32_16x16x32_bf16 v[6:9], v[146:149], v[186:189], v[6:9]
	v_mfma_f32_16x16x32_bf16 v[2:5], v[154:157], v[186:189], v[2:5]
	v_mfma_f32_16x16x32_bf16 v[54:57], v[150:153], v[166:169], v[54:57]
	v_mfma_f32_16x16x32_bf16 v[50:53], v[158:161], v[166:169], v[50:53]
	v_mfma_f32_16x16x32_bf16 v[38:41], v[150:153], v[174:177], v[38:41]
	v_mfma_f32_16x16x32_bf16 v[34:37], v[158:161], v[174:177], v[34:37]
	v_mfma_f32_16x16x32_bf16 v[22:25], v[150:153], v[182:185], v[22:25]
	v_mfma_f32_16x16x32_bf16 v[18:21], v[158:161], v[182:185], v[18:21]
	v_mfma_f32_16x16x32_bf16 v[6:9], v[150:153], v[190:193], v[6:9]
	v_mfma_f32_16x16x32_bf16 v[2:5], v[158:161], v[190:193], v[2:5]
	s_barrier
	s_add_i32 s62, s62, 2
	s_add_u32 s30, s30, 0x100
	s_addc_u32 s31, s31, 0
	s_cmp_gt_u32 s62, 13
	s_cbranch_scc1 .LBB0_781

.LBB0_777:
	s_add_u32 s36, s28, s30
	s_addc_u32 s37, s29, s31
	s_add_u32 s36, s36, 0x100
	s_addc_u32 s37, s37, 0
	s_add_u32 s42, s60, s30
	s_addc_u32 s43, s61, s31
	s_waitcnt lgkmcnt(0)
	s_cmpk_eq_i32 s30, 0x700
	s_cselect_b32 s39, s21, s37
	s_cselect_b32 s38, s58, s36
	s_cselect_b32 s37, s19, s43
	s_cselect_b32 s36, s59, s42
	s_barrier
	s_waitcnt lgkmcnt(0)
	v_mfma_f32_16x16x32_bf16 v[142:145], v[146:149], v[186:189], v[142:145]
	v_mfma_f32_16x16x32_bf16 v[138:141], v[154:157], v[186:189], v[138:141]
	v_mfma_f32_16x16x32_bf16 v[126:129], v[146:149], v[178:181], v[126:129]
	v_mfma_f32_16x16x32_bf16 v[122:125], v[154:157], v[178:181], v[122:125]
	v_mfma_f32_16x16x32_bf16 v[110:113], v[146:149], v[170:173], v[110:113]
	v_mfma_f32_16x16x32_bf16 v[106:109], v[154:157], v[170:173], v[106:109]
	v_mfma_f32_16x16x32_bf16 v[94:97], v[146:149], v[162:165], v[94:97]
	v_mfma_f32_16x16x32_bf16 v[90:93], v[154:157], v[162:165], v[90:93]
	v_mfma_f32_16x16x32_bf16 v[142:145], v[150:153], v[190:193], v[142:145]
	v_mfma_f32_16x16x32_bf16 v[138:141], v[158:161], v[190:193], v[138:141]
	v_mfma_f32_16x16x32_bf16 v[126:129], v[150:153], v[182:185], v[126:129]
	v_mfma_f32_16x16x32_bf16 v[122:125], v[158:161], v[182:185], v[122:125]
	v_mfma_f32_16x16x32_bf16 v[110:113], v[150:153], v[174:177], v[110:113]
	v_mfma_f32_16x16x32_bf16 v[106:109], v[158:161], v[174:177], v[106:109]
	v_mfma_f32_16x16x32_bf16 v[94:97], v[150:153], v[166:169], v[94:97]
	v_mfma_f32_16x16x32_bf16 v[90:93], v[158:161], v[166:169], v[90:93]
	v_mfma_f32_16x16x32_bf16 v[134:137], v[66:69], v[186:189], v[134:137]
	v_mfma_f32_16x16x32_bf16 v[130:133], v[82:85], v[186:189], v[130:133]
	v_mfma_f32_16x16x32_bf16 v[118:121], v[66:69], v[178:181], v[118:121]
	v_mfma_f32_16x16x32_bf16 v[114:117], v[82:85], v[178:181], v[114:117]
	v_mfma_f32_16x16x32_bf16 v[102:105], v[66:69], v[170:173], v[102:105]
	v_mfma_f32_16x16x32_bf16 v[98:101], v[82:85], v[170:173], v[98:101]
	v_mfma_f32_16x16x32_bf16 v[78:81], v[66:69], v[162:165], v[78:81]
	v_mfma_f32_16x16x32_bf16 v[70:73], v[82:85], v[162:165], v[70:73]
	v_mfma_f32_16x16x32_bf16 v[134:137], v[74:77], v[190:193], v[134:137]
	v_mfma_f32_16x16x32_bf16 v[130:133], v[86:89], v[190:193], v[130:133]
	v_mfma_f32_16x16x32_bf16 v[118:121], v[74:77], v[182:185], v[118:121]
	v_mfma_f32_16x16x32_bf16 v[114:117], v[86:89], v[182:185], v[114:117]
	v_mfma_f32_16x16x32_bf16 v[102:105], v[74:77], v[174:177], v[102:105]
	v_mfma_f32_16x16x32_bf16 v[98:101], v[86:89], v[174:177], v[98:101]
	v_mfma_f32_16x16x32_bf16 v[78:81], v[74:77], v[166:169], v[78:81]
	v_mfma_f32_16x16x32_bf16 v[70:73], v[86:89], v[166:169], v[70:73]
	s_barrier
	s_mov_b32 m0, s46
	v_lshl_add_u64 v[222:223], s[36:37], 0, v[196:197]
	s_add_u32 s42, s36, 0x40000
	ds_read_b128 v[186:189], v227 offset:16384
	ds_read_b128 v[190:193], v227 offset:17408
	ds_read_b128 v[178:181], v227 offset:18432
	ds_read_b128 v[182:185], v227 offset:19456
	ds_read_b128 v[170:173], v227 offset:20480
	ds_read_b128 v[174:177], v227 offset:21504
	ds_read_b128 v[162:165], v227 offset:22528
	ds_read_b128 v[166:169], v227 offset:23552
	global_load_lds_dwordx4 v[222:223], off
	v_lshl_add_u64 v[220:221], s[36:37], 0, v[202:203]
	s_mov_b32 m0, s47
	s_addc_u32 s43, s37, 0
	global_load_lds_dwordx4 v[220:221], off
	v_lshl_add_u64 v[216:217], s[42:43], 0, v[196:197]
	s_mov_b32 m0, s48
	v_lshl_add_u64 v[218:219], s[38:39], 0, v[200:201]
	global_load_lds_dwordx4 v[216:217], off
	v_lshl_add_u64 v[216:217], s[42:43], 0, v[202:203]
	s_mov_b32 m0, s49
	s_mov_b64 s[42:43], -1
	global_load_lds_dwordx4 v[216:217], off
	v_lshl_add_u64 v[216:217], s[38:39], 0, v[194:195]
	s_mov_b32 m0, s27
	s_and_b64 vcc, exec, s[40:41]
	global_load_lds_dwordx4 v[216:217], off
	s_mov_b32 m0, s50
	s_nop 0
	global_load_lds_dwordx4 v[218:219], off
	s_cbranch_vccz .LBB0_779
	s_waitcnt vmcnt(8)
	s_mov_b64 s[42:43], 0

.LBB0_841:
	s_waitcnt lgkmcnt(0)
	s_barrier
	s_waitcnt lgkmcnt(0)
	v_mfma_f32_16x16x32_bf16 v[66:69], v[150:153], v[190:193], v[66:69]
	v_mfma_f32_16x16x32_bf16 v[62:65], v[158:161], v[190:193], v[62:65]
	v_mfma_f32_16x16x32_bf16 v[50:53], v[150:153], v[182:185], v[50:53]
	v_mfma_f32_16x16x32_bf16 v[46:49], v[158:161], v[182:185], v[46:49]
	v_mfma_f32_16x16x32_bf16 v[34:37], v[150:153], v[174:177], v[34:37]
	v_mfma_f32_16x16x32_bf16 v[30:33], v[158:161], v[174:177], v[30:33]
	v_mfma_f32_16x16x32_bf16 v[18:21], v[150:153], v[166:169], v[18:21]
	v_mfma_f32_16x16x32_bf16 v[14:17], v[158:161], v[166:169], v[14:17]
	v_mfma_f32_16x16x32_bf16 v[66:69], v[154:157], v[194:197], v[66:69]
	v_mfma_f32_16x16x32_bf16 v[62:65], v[162:165], v[194:197], v[62:65]
	v_mfma_f32_16x16x32_bf16 v[50:53], v[154:157], v[186:189], v[50:53]
	v_mfma_f32_16x16x32_bf16 v[46:49], v[162:165], v[186:189], v[46:49]
	v_mfma_f32_16x16x32_bf16 v[34:37], v[154:157], v[178:181], v[34:37]
	v_mfma_f32_16x16x32_bf16 v[30:33], v[162:165], v[178:181], v[30:33]
	v_mfma_f32_16x16x32_bf16 v[18:21], v[154:157], v[170:173], v[18:21]
	v_mfma_f32_16x16x32_bf16 v[14:17], v[162:165], v[170:173], v[14:17]
	v_mfma_f32_16x16x32_bf16 v[58:61], v[134:137], v[190:193], v[58:61]
	v_mfma_f32_16x16x32_bf16 v[54:57], v[142:145], v[190:193], v[54:57]
	v_mfma_f32_16x16x32_bf16 v[42:45], v[134:137], v[182:185], v[42:45]
	v_mfma_f32_16x16x32_bf16 v[38:41], v[142:145], v[182:185], v[38:41]
	v_mfma_f32_16x16x32_bf16 v[26:29], v[134:137], v[174:177], v[26:29]
	v_mfma_f32_16x16x32_bf16 v[22:25], v[142:145], v[174:177], v[22:25]
	v_mfma_f32_16x16x32_bf16 v[10:13], v[134:137], v[166:169], v[10:13]
	v_mfma_f32_16x16x32_bf16 v[6:9], v[142:145], v[166:169], v[6:9]
	v_mfma_f32_16x16x32_bf16 v[58:61], v[138:141], v[194:197], v[58:61]
	v_mfma_f32_16x16x32_bf16 v[54:57], v[146:149], v[194:197], v[54:57]
	v_mfma_f32_16x16x32_bf16 v[42:45], v[138:141], v[186:189], v[42:45]
	v_mfma_f32_16x16x32_bf16 v[38:41], v[146:149], v[186:189], v[38:41]
	v_mfma_f32_16x16x32_bf16 v[26:29], v[138:141], v[178:181], v[26:29]
	v_mfma_f32_16x16x32_bf16 v[22:25], v[146:149], v[178:181], v[22:25]
	v_mfma_f32_16x16x32_bf16 v[10:13], v[138:141], v[170:173], v[10:13]
	v_mfma_f32_16x16x32_bf16 v[6:9], v[146:149], v[170:173], v[6:9]
	s_barrier
	s_add_i32 s50, 0, 0x18000
	v_add_u32_e32 v3, s50, v199
	s_add_i32 s51, 0, 0x1c000
	ds_read_b128 v[134:137], v3
	ds_read_b128 v[138:141], v3 offset:1024
	ds_read_b128 v[142:145], v3 offset:2048
	ds_read_b128 v[146:149], v3 offset:3072
	v_add_u32_e32 v3, s51, v199
	ds_read_b128 v[150:153], v3
	ds_read_b128 v[154:157], v3 offset:1024
	ds_read_b128 v[158:161], v3 offset:2048
	ds_read_b128 v[162:165], v3 offset:3072
	s_add_u32 s48, s48, 0x80000
	s_addc_u32 s49, s49, 0
	s_mov_b32 m0, s65
	v_lshl_add_u64 v[232:233], s[48:49], 0, v[200:201]
	ds_read_b128 v[166:169], v231 offset:32768
	ds_read_b128 v[170:173], v231 offset:33792
	ds_read_b128 v[174:177], v231 offset:34816
	ds_read_b128 v[178:181], v231 offset:35840
	ds_read_b128 v[182:185], v231 offset:36864
	ds_read_b128 v[186:189], v231 offset:37888
	ds_read_b128 v[190:193], v231 offset:38912
	ds_read_b128 v[194:197], v231 offset:39936
	global_load_lds_dwordx4 v[232:233], off
	v_lshl_add_u64 v[232:233], s[48:49], 0, v[204:205]
	s_mov_b32 m0, s66
	s_nop 0
	global_load_lds_dwordx4 v[232:233], off
	s_waitcnt vmcnt(8)
	s_waitcnt lgkmcnt(0)
	s_barrier
	s_waitcnt lgkmcnt(0)
	v_mfma_f32_16x16x32_bf16 v[130:133], v[134:137], v[166:169], v[130:133]
	v_mfma_f32_16x16x32_bf16 v[126:129], v[142:145], v[166:169], v[126:129]
	v_mfma_f32_16x16x32_bf16 v[122:125], v[134:137], v[174:177], v[122:125]
	v_mfma_f32_16x16x32_bf16 v[114:117], v[142:145], v[174:177], v[114:117]
	v_mfma_f32_16x16x32_bf16 v[98:101], v[134:137], v[182:185], v[98:101]
	v_mfma_f32_16x16x32_bf16 v[94:97], v[142:145], v[182:185], v[94:97]
	v_mfma_f32_16x16x32_bf16 v[82:85], v[134:137], v[190:193], v[82:85]
	v_mfma_f32_16x16x32_bf16 v[78:81], v[142:145], v[190:193], v[78:81]
	v_mfma_f32_16x16x32_bf16 v[130:133], v[138:141], v[170:173], v[130:133]
	v_mfma_f32_16x16x32_bf16 v[126:129], v[146:149], v[170:173], v[126:129]
	v_mfma_f32_16x16x32_bf16 v[122:125], v[138:141], v[178:181], v[122:125]
	v_mfma_f32_16x16x32_bf16 v[114:117], v[146:149], v[178:181], v[114:117]
	v_mfma_f32_16x16x32_bf16 v[98:101], v[138:141], v[186:189], v[98:101]
	v_mfma_f32_16x16x32_bf16 v[94:97], v[146:149], v[186:189], v[94:97]
	v_mfma_f32_16x16x32_bf16 v[82:85], v[138:141], v[194:197], v[82:85]
	v_mfma_f32_16x16x32_bf16 v[78:81], v[146:149], v[194:197], v[78:81]
	v_mfma_f32_16x16x32_bf16 v[118:121], v[150:153], v[166:169], v[118:121]
	v_mfma_f32_16x16x32_bf16 v[110:113], v[158:161], v[166:169], v[110:113]
	v_mfma_f32_16x16x32_bf16 v[106:109], v[150:153], v[174:177], v[106:109]
	v_mfma_f32_16x16x32_bf16 v[102:105], v[158:161], v[174:177], v[102:105]
	v_mfma_f32_16x16x32_bf16 v[90:93], v[150:153], v[182:185], v[90:93]
	v_mfma_f32_16x16x32_bf16 v[86:89], v[158:161], v[182:185], v[86:89]
	v_mfma_f32_16x16x32_bf16 v[74:77], v[150:153], v[190:193], v[74:77]
	v_mfma_f32_16x16x32_bf16 v[70:73], v[158:161], v[190:193], v[70:73]
	v_mfma_f32_16x16x32_bf16 v[118:121], v[154:157], v[170:173], v[118:121]
	v_mfma_f32_16x16x32_bf16 v[110:113], v[162:165], v[170:173], v[110:113]
	v_mfma_f32_16x16x32_bf16 v[106:109], v[154:157], v[178:181], v[106:109]
	v_mfma_f32_16x16x32_bf16 v[102:105], v[162:165], v[178:181], v[102:105]
	v_mfma_f32_16x16x32_bf16 v[90:93], v[154:157], v[186:189], v[90:93]
	v_mfma_f32_16x16x32_bf16 v[86:89], v[162:165], v[186:189], v[86:89]
	v_mfma_f32_16x16x32_bf16 v[74:77], v[154:157], v[194:197], v[74:77]
	v_mfma_f32_16x16x32_bf16 v[70:73], v[162:165], v[194:197], v[70:73]
	s_barrier
	s_add_i32 s48, s50, s58
	v_lshl_add_u64 v[228:229], v[228:229], 0, s[14:15]
	s_mov_b32 m0, s48
	ds_read_b128 v[166:169], v231 offset:49152
	ds_read_b128 v[170:173], v231 offset:50176
	ds_read_b128 v[174:177], v231 offset:51200
	ds_read_b128 v[178:181], v231 offset:52224
	ds_read_b128 v[182:185], v231 offset:53248
	ds_read_b128 v[186:189], v231 offset:54272
	ds_read_b128 v[190:193], v231 offset:55296
	ds_read_b128 v[194:197], v231 offset:56320
	global_load_lds_dwordx4 v[228:229], off
	s_add_i32 m0, s48, 0x2000
	s_add_u32 s46, s46, 0x80080
	v_lshl_add_u64 v[226:227], v[226:227], 0, s[14:15]
	s_addc_u32 s47, s47, 0
	s_add_i32 s48, s51, s58
	global_load_lds_dwordx4 v[226:227], off
	v_lshl_add_u64 v[226:227], s[46:47], 0, v[202:203]
	s_mov_b32 m0, s48
	v_lshl_add_u64 v[4:5], v[4:5], 0, s[14:15]
	global_load_lds_dwordx4 v[226:227], off
	v_lshl_add_u64 v[226:227], s[46:47], 0, v[206:207]
	s_add_i32 m0, s48, 0x2000
	s_nop 0
	global_load_lds_dwordx4 v[226:227], off
	s_mov_b32 m0, s67
	s_nop 0
	global_load_lds_dwordx4 v[4:5], off
	v_lshl_add_u64 v[4:5], v[224:225], 0, s[14:15]
	s_mov_b32 m0, s68
	s_nop 0
	global_load_lds_dwordx4 v[4:5], off
	s_waitcnt vmcnt(8)
	s_waitcnt lgkmcnt(0)
	s_barrier
	s_waitcnt lgkmcnt(0)
	v_mfma_f32_16x16x32_bf16 v[66:69], v[134:137], v[166:169], v[66:69]
	v_mfma_f32_16x16x32_bf16 v[62:65], v[142:145], v[166:169], v[62:65]
	v_mfma_f32_16x16x32_bf16 v[50:53], v[134:137], v[174:177], v[50:53]
	v_mfma_f32_16x16x32_bf16 v[46:49], v[142:145], v[174:177], v[46:49]
	v_mfma_f32_16x16x32_bf16 v[34:37], v[134:137], v[182:185], v[34:37]
	v_mfma_f32_16x16x32_bf16 v[30:33], v[142:145], v[182:185], v[30:33]
	v_mfma_f32_16x16x32_bf16 v[18:21], v[134:137], v[190:193], v[18:21]
	v_mfma_f32_16x16x32_bf16 v[14:17], v[142:145], v[190:193], v[14:17]
	v_mfma_f32_16x16x32_bf16 v[66:69], v[138:141], v[170:173], v[66:69]
	v_mfma_f32_16x16x32_bf16 v[62:65], v[146:149], v[170:173], v[62:65]
	v_mfma_f32_16x16x32_bf16 v[50:53], v[138:141], v[178:181], v[50:53]
	v_mfma_f32_16x16x32_bf16 v[46:49], v[146:149], v[178:181], v[46:49]
	v_mfma_f32_16x16x32_bf16 v[34:37], v[138:141], v[186:189], v[34:37]
	v_mfma_f32_16x16x32_bf16 v[30:33], v[146:149], v[186:189], v[30:33]
	v_mfma_f32_16x16x32_bf16 v[18:21], v[138:141], v[194:197], v[18:21]
	v_mfma_f32_16x16x32_bf16 v[14:17], v[146:149], v[194:197], v[14:17]
	v_mfma_f32_16x16x32_bf16 v[58:61], v[150:153], v[166:169], v[58:61]
	v_mfma_f32_16x16x32_bf16 v[54:57], v[158:161], v[166:169], v[54:57]
	v_mfma_f32_16x16x32_bf16 v[42:45], v[150:153], v[174:177], v[42:45]
	v_mfma_f32_16x16x32_bf16 v[38:41], v[158:161], v[174:177], v[38:41]
	v_mfma_f32_16x16x32_bf16 v[26:29], v[150:153], v[182:185], v[26:29]
	v_mfma_f32_16x16x32_bf16 v[22:25], v[158:161], v[182:185], v[22:25]
	v_mfma_f32_16x16x32_bf16 v[10:13], v[150:153], v[190:193], v[10:13]
	v_mfma_f32_16x16x32_bf16 v[4:7], v[158:161], v[190:193], v[6:9]
	v_mfma_f32_16x16x32_bf16 v[58:61], v[154:157], v[170:173], v[58:61]
	v_mfma_f32_16x16x32_bf16 v[54:57], v[162:165], v[170:173], v[54:57]
	v_mfma_f32_16x16x32_bf16 v[42:45], v[154:157], v[178:181], v[42:45]
	v_mfma_f32_16x16x32_bf16 v[38:41], v[162:165], v[178:181], v[38:41]
	v_mfma_f32_16x16x32_bf16 v[26:29], v[154:157], v[186:189], v[26:29]
	v_mfma_f32_16x16x32_bf16 v[22:25], v[162:165], v[186:189], v[22:25]
	v_mfma_f32_16x16x32_bf16 v[10:13], v[154:157], v[194:197], v[10:13]
	v_mfma_f32_16x16x32_bf16 v[6:9], v[162:165], v[194:197], v[4:7]
	s_barrier
	s_add_i32 s79, s79, 2
	s_add_u32 s42, s42, 0x100
	s_addc_u32 s43, s43, 0
	s_cmp_gt_u32 s79, 29
	s_cbranch_scc1 .LBB0_852

.LBB0_848:
	s_add_u32 s46, s40, s42
	s_addc_u32 s47, s41, s43
	s_add_u32 s46, s46, 0x100
	s_addc_u32 s47, s47, 0
	s_add_u32 s52, s77, s42
	s_addc_u32 s53, s78, s43
	s_waitcnt lgkmcnt(0)
	s_cmpk_eq_i32 s42, 0xf00
	s_cselect_b32 s49, s35, s47
	s_cselect_b32 s48, s75, s46
	s_cselect_b32 s47, s31, s53
	s_cselect_b32 s46, s76, s52
	s_barrier
	s_waitcnt lgkmcnt(0)
	v_mfma_f32_16x16x32_bf16 v[130:133], v[150:153], v[190:193], v[130:133]
	v_mfma_f32_16x16x32_bf16 v[126:129], v[158:161], v[190:193], v[126:129]
	v_mfma_f32_16x16x32_bf16 v[122:125], v[150:153], v[182:185], v[122:125]
	v_mfma_f32_16x16x32_bf16 v[114:117], v[158:161], v[182:185], v[114:117]
	v_mfma_f32_16x16x32_bf16 v[98:101], v[150:153], v[174:177], v[98:101]
	v_mfma_f32_16x16x32_bf16 v[94:97], v[158:161], v[174:177], v[94:97]
	v_mfma_f32_16x16x32_bf16 v[82:85], v[150:153], v[166:169], v[82:85]
	v_mfma_f32_16x16x32_bf16 v[78:81], v[158:161], v[166:169], v[78:81]
	v_mfma_f32_16x16x32_bf16 v[130:133], v[154:157], v[194:197], v[130:133]
	v_mfma_f32_16x16x32_bf16 v[126:129], v[162:165], v[194:197], v[126:129]
	v_mfma_f32_16x16x32_bf16 v[122:125], v[154:157], v[186:189], v[122:125]
	v_mfma_f32_16x16x32_bf16 v[114:117], v[162:165], v[186:189], v[114:117]
	v_mfma_f32_16x16x32_bf16 v[98:101], v[154:157], v[178:181], v[98:101]
	v_mfma_f32_16x16x32_bf16 v[94:97], v[162:165], v[178:181], v[94:97]
	v_mfma_f32_16x16x32_bf16 v[82:85], v[154:157], v[170:173], v[82:85]
	v_mfma_f32_16x16x32_bf16 v[78:81], v[162:165], v[170:173], v[78:81]
	v_mfma_f32_16x16x32_bf16 v[118:121], v[134:137], v[190:193], v[118:121]
	v_mfma_f32_16x16x32_bf16 v[110:113], v[142:145], v[190:193], v[110:113]
	v_mfma_f32_16x16x32_bf16 v[106:109], v[134:137], v[182:185], v[106:109]
	v_mfma_f32_16x16x32_bf16 v[102:105], v[142:145], v[182:185], v[102:105]
	v_mfma_f32_16x16x32_bf16 v[90:93], v[134:137], v[174:177], v[90:93]
	v_mfma_f32_16x16x32_bf16 v[86:89], v[142:145], v[174:177], v[86:89]
	v_mfma_f32_16x16x32_bf16 v[74:77], v[134:137], v[166:169], v[74:77]
	v_mfma_f32_16x16x32_bf16 v[70:73], v[142:145], v[166:169], v[70:73]
	v_mfma_f32_16x16x32_bf16 v[118:121], v[138:141], v[194:197], v[118:121]
	v_mfma_f32_16x16x32_bf16 v[110:113], v[146:149], v[194:197], v[110:113]
	v_mfma_f32_16x16x32_bf16 v[106:109], v[138:141], v[186:189], v[106:109]
	v_mfma_f32_16x16x32_bf16 v[102:105], v[146:149], v[186:189], v[102:105]
	v_mfma_f32_16x16x32_bf16 v[90:93], v[138:141], v[178:181], v[90:93]
	v_mfma_f32_16x16x32_bf16 v[86:89], v[146:149], v[178:181], v[86:89]
	v_mfma_f32_16x16x32_bf16 v[74:77], v[138:141], v[170:173], v[74:77]
	v_mfma_f32_16x16x32_bf16 v[70:73], v[146:149], v[170:173], v[70:73]
	s_barrier
	s_mov_b32 m0, s60
	v_lshl_add_u64 v[228:229], s[46:47], 0, v[202:203]
	s_add_u32 s52, s46, 0x80000
	ds_read_b128 v[190:193], v231 offset:16384
	ds_read_b128 v[194:197], v231 offset:17408
	ds_read_b128 v[182:185], v231 offset:18432
	ds_read_b128 v[186:189], v231 offset:19456
	ds_read_b128 v[174:177], v231 offset:20480
	ds_read_b128 v[178:181], v231 offset:21504
	ds_read_b128 v[166:169], v231 offset:22528
	ds_read_b128 v[170:173], v231 offset:23552
	global_load_lds_dwordx4 v[228:229], off
	v_lshl_add_u64 v[226:227], s[46:47], 0, v[206:207]
	s_mov_b32 m0, s61
	s_addc_u32 s53, s47, 0
	global_load_lds_dwordx4 v[226:227], off
	v_lshl_add_u64 v[4:5], s[52:53], 0, v[202:203]
	s_mov_b32 m0, s62
	v_lshl_add_u64 v[224:225], s[48:49], 0, v[204:205]
	global_load_lds_dwordx4 v[4:5], off
	v_lshl_add_u64 v[4:5], s[52:53], 0, v[206:207]
	s_mov_b32 m0, s63
	s_mov_b64 s[52:53], -1
	global_load_lds_dwordx4 v[4:5], off
	v_lshl_add_u64 v[4:5], s[48:49], 0, v[200:201]
	s_mov_b32 m0, s59
	s_and_b64 vcc, exec, s[50:51]
	global_load_lds_dwordx4 v[4:5], off
	s_mov_b32 m0, s64
	s_nop 0
	global_load_lds_dwordx4 v[224:225], off
	s_cbranch_vccz .LBB0_850
	s_waitcnt vmcnt(8)
	s_mov_b64 s[52:53], 0

.LBB0_914:
	s_waitcnt lgkmcnt(0)
	s_barrier
	s_waitcnt lgkmcnt(0)
	v_mfma_f32_16x16x32_bf16 v[62:65], v[146:149], v[186:189], v[62:65]
	v_mfma_f32_16x16x32_bf16 v[58:61], v[154:157], v[186:189], v[58:61]
	v_mfma_f32_16x16x32_bf16 v[46:49], v[146:149], v[178:181], v[46:49]
	v_mfma_f32_16x16x32_bf16 v[42:45], v[154:157], v[178:181], v[42:45]
	v_mfma_f32_16x16x32_bf16 v[30:33], v[146:149], v[170:173], v[30:33]
	v_mfma_f32_16x16x32_bf16 v[26:29], v[154:157], v[170:173], v[26:29]
	v_mfma_f32_16x16x32_bf16 v[14:17], v[146:149], v[162:165], v[14:17]
	v_mfma_f32_16x16x32_bf16 v[10:13], v[154:157], v[162:165], v[10:13]
	v_mfma_f32_16x16x32_bf16 v[62:65], v[150:153], v[190:193], v[62:65]
	v_mfma_f32_16x16x32_bf16 v[58:61], v[158:161], v[190:193], v[58:61]
	v_mfma_f32_16x16x32_bf16 v[46:49], v[150:153], v[182:185], v[46:49]
	v_mfma_f32_16x16x32_bf16 v[42:45], v[158:161], v[182:185], v[42:45]
	v_mfma_f32_16x16x32_bf16 v[30:33], v[150:153], v[174:177], v[30:33]
	v_mfma_f32_16x16x32_bf16 v[26:29], v[158:161], v[174:177], v[26:29]
	v_mfma_f32_16x16x32_bf16 v[14:17], v[150:153], v[166:169], v[14:17]
	v_mfma_f32_16x16x32_bf16 v[10:13], v[158:161], v[166:169], v[10:13]
	v_mfma_f32_16x16x32_bf16 v[54:57], v[130:133], v[186:189], v[54:57]
	v_mfma_f32_16x16x32_bf16 v[50:53], v[138:141], v[186:189], v[50:53]
	v_mfma_f32_16x16x32_bf16 v[38:41], v[130:133], v[178:181], v[38:41]
	v_mfma_f32_16x16x32_bf16 v[34:37], v[138:141], v[178:181], v[34:37]
	v_mfma_f32_16x16x32_bf16 v[22:25], v[130:133], v[170:173], v[22:25]
	v_mfma_f32_16x16x32_bf16 v[18:21], v[138:141], v[170:173], v[18:21]
	v_mfma_f32_16x16x32_bf16 v[6:9], v[130:133], v[162:165], v[6:9]
	v_mfma_f32_16x16x32_bf16 v[2:5], v[138:141], v[162:165], v[2:5]
	v_mfma_f32_16x16x32_bf16 v[54:57], v[134:137], v[190:193], v[54:57]
	v_mfma_f32_16x16x32_bf16 v[50:53], v[142:145], v[190:193], v[50:53]
	v_mfma_f32_16x16x32_bf16 v[38:41], v[134:137], v[182:185], v[38:41]
	v_mfma_f32_16x16x32_bf16 v[34:37], v[142:145], v[182:185], v[34:37]
	v_mfma_f32_16x16x32_bf16 v[22:25], v[134:137], v[174:177], v[22:25]
	v_mfma_f32_16x16x32_bf16 v[18:21], v[142:145], v[174:177], v[18:21]
	v_mfma_f32_16x16x32_bf16 v[6:9], v[134:137], v[166:169], v[6:9]
	v_mfma_f32_16x16x32_bf16 v[2:5], v[142:145], v[166:169], v[2:5]
	s_barrier
	s_add_i32 s42, 0, 0x18000
	s_add_i32 s43, 0, 0x1c000
	v_add_u32_e32 v142, s42, v199
	v_add_u32_e32 v158, s43, v199
	ds_read_b128 v[130:133], v142
	ds_read_b128 v[134:137], v142 offset:1024
	ds_read_b128 v[138:141], v142 offset:2048
	ds_read_b128 v[142:145], v142 offset:3072
	ds_read_b128 v[146:149], v158
	ds_read_b128 v[150:153], v158 offset:1024
	ds_read_b128 v[154:157], v158 offset:2048
	ds_read_b128 v[158:161], v158 offset:3072
	s_add_u32 s40, s40, 0x80000
	s_addc_u32 s41, s41, 0
	s_mov_b32 m0, s56
	v_lshl_add_u64 v[230:231], s[40:41], 0, v[194:195]
	ds_read_b128 v[162:165], v227 offset:32768
	ds_read_b128 v[166:169], v227 offset:33792
	ds_read_b128 v[170:173], v227 offset:34816
	ds_read_b128 v[174:177], v227 offset:35840
	ds_read_b128 v[178:181], v227 offset:36864
	ds_read_b128 v[182:185], v227 offset:37888
	ds_read_b128 v[186:189], v227 offset:38912
	ds_read_b128 v[190:193], v227 offset:39936
	global_load_lds_dwordx4 v[230:231], off
	v_lshl_add_u64 v[230:231], s[40:41], 0, v[200:201]
	s_mov_b32 m0, s57
	s_nop 0
	global_load_lds_dwordx4 v[230:231], off
	s_waitcnt vmcnt(8)
	s_waitcnt lgkmcnt(0)
	s_barrier
	s_waitcnt lgkmcnt(0)
	v_mfma_f32_16x16x32_bf16 v[126:129], v[130:133], v[162:165], v[126:129]
	v_mfma_f32_16x16x32_bf16 v[122:125], v[138:141], v[162:165], v[122:125]
	v_mfma_f32_16x16x32_bf16 v[110:113], v[130:133], v[170:173], v[110:113]
	v_mfma_f32_16x16x32_bf16 v[106:109], v[138:141], v[170:173], v[106:109]
	v_mfma_f32_16x16x32_bf16 v[94:97], v[130:133], v[178:181], v[94:97]
	v_mfma_f32_16x16x32_bf16 v[90:93], v[138:141], v[178:181], v[90:93]
	v_mfma_f32_16x16x32_bf16 v[78:81], v[130:133], v[186:189], v[78:81]
	v_mfma_f32_16x16x32_bf16 v[74:77], v[138:141], v[186:189], v[74:77]
	v_mfma_f32_16x16x32_bf16 v[126:129], v[134:137], v[166:169], v[126:129]
	v_mfma_f32_16x16x32_bf16 v[122:125], v[142:145], v[166:169], v[122:125]
	v_mfma_f32_16x16x32_bf16 v[110:113], v[134:137], v[174:177], v[110:113]
	v_mfma_f32_16x16x32_bf16 v[106:109], v[142:145], v[174:177], v[106:109]
	v_mfma_f32_16x16x32_bf16 v[94:97], v[134:137], v[182:185], v[94:97]
	v_mfma_f32_16x16x32_bf16 v[90:93], v[142:145], v[182:185], v[90:93]
	v_mfma_f32_16x16x32_bf16 v[78:81], v[134:137], v[190:193], v[78:81]
	v_mfma_f32_16x16x32_bf16 v[74:77], v[142:145], v[190:193], v[74:77]
	v_mfma_f32_16x16x32_bf16 v[118:121], v[146:149], v[162:165], v[118:121]
	v_mfma_f32_16x16x32_bf16 v[114:117], v[154:157], v[162:165], v[114:117]
	v_mfma_f32_16x16x32_bf16 v[102:105], v[146:149], v[170:173], v[102:105]
	v_mfma_f32_16x16x32_bf16 v[98:101], v[154:157], v[170:173], v[98:101]
	v_mfma_f32_16x16x32_bf16 v[86:89], v[146:149], v[178:181], v[86:89]
	v_mfma_f32_16x16x32_bf16 v[82:85], v[154:157], v[178:181], v[82:85]
	v_mfma_f32_16x16x32_bf16 v[70:73], v[146:149], v[186:189], v[70:73]
	v_mfma_f32_16x16x32_bf16 v[66:69], v[154:157], v[186:189], v[66:69]
	v_mfma_f32_16x16x32_bf16 v[118:121], v[150:153], v[166:169], v[118:121]
	v_mfma_f32_16x16x32_bf16 v[114:117], v[158:161], v[166:169], v[114:117]
	v_mfma_f32_16x16x32_bf16 v[102:105], v[150:153], v[174:177], v[102:105]
	v_mfma_f32_16x16x32_bf16 v[98:101], v[158:161], v[174:177], v[98:101]
	v_mfma_f32_16x16x32_bf16 v[86:89], v[150:153], v[182:185], v[86:89]
	v_mfma_f32_16x16x32_bf16 v[82:85], v[158:161], v[182:185], v[82:85]
	v_mfma_f32_16x16x32_bf16 v[70:73], v[150:153], v[190:193], v[70:73]
	v_mfma_f32_16x16x32_bf16 v[66:69], v[158:161], v[190:193], v[66:69]
	s_barrier
	s_add_i32 s40, s42, s49
	v_lshl_add_u64 v[222:223], v[222:223], 0, s[16:17]
	s_mov_b32 m0, s40
	ds_read_b128 v[162:165], v227 offset:49152
	ds_read_b128 v[166:169], v227 offset:50176
	ds_read_b128 v[170:173], v227 offset:51200
	ds_read_b128 v[174:177], v227 offset:52224
	ds_read_b128 v[178:181], v227 offset:53248
	ds_read_b128 v[182:185], v227 offset:54272
	ds_read_b128 v[186:189], v227 offset:55296
	ds_read_b128 v[190:193], v227 offset:56320
	global_load_lds_dwordx4 v[222:223], off
	s_add_i32 m0, s40, 0x2000
	s_add_u32 s38, s38, 0x80080
	v_lshl_add_u64 v[220:221], v[220:221], 0, s[16:17]
	s_addc_u32 s39, s39, 0
	s_add_i32 s40, s43, s49
	global_load_lds_dwordx4 v[220:221], off
	v_lshl_add_u64 v[220:221], s[38:39], 0, v[196:197]
	s_mov_b32 m0, s40
	v_lshl_add_u64 v[216:217], v[216:217], 0, s[16:17]
	global_load_lds_dwordx4 v[220:221], off
	v_lshl_add_u64 v[220:221], s[38:39], 0, v[202:203]
	s_add_i32 m0, s40, 0x2000
	s_nop 0
	global_load_lds_dwordx4 v[220:221], off
	s_mov_b32 m0, s59
	s_nop 0
	global_load_lds_dwordx4 v[216:217], off
	v_lshl_add_u64 v[216:217], v[218:219], 0, s[16:17]
	s_mov_b32 m0, s60
	s_nop 0
	global_load_lds_dwordx4 v[216:217], off
	s_waitcnt vmcnt(8)
	s_waitcnt lgkmcnt(0)
	s_barrier
	s_waitcnt lgkmcnt(0)
	v_mfma_f32_16x16x32_bf16 v[62:65], v[130:133], v[162:165], v[62:65]
	v_mfma_f32_16x16x32_bf16 v[58:61], v[138:141], v[162:165], v[58:61]
	v_mfma_f32_16x16x32_bf16 v[46:49], v[130:133], v[170:173], v[46:49]
	v_mfma_f32_16x16x32_bf16 v[42:45], v[138:141], v[170:173], v[42:45]
	v_mfma_f32_16x16x32_bf16 v[30:33], v[130:133], v[178:181], v[30:33]
	v_mfma_f32_16x16x32_bf16 v[26:29], v[138:141], v[178:181], v[26:29]
	v_mfma_f32_16x16x32_bf16 v[14:17], v[130:133], v[186:189], v[14:17]
	v_mfma_f32_16x16x32_bf16 v[10:13], v[138:141], v[186:189], v[10:13]
	v_mfma_f32_16x16x32_bf16 v[62:65], v[134:137], v[166:169], v[62:65]
	v_mfma_f32_16x16x32_bf16 v[58:61], v[142:145], v[166:169], v[58:61]
	v_mfma_f32_16x16x32_bf16 v[46:49], v[134:137], v[174:177], v[46:49]
	v_mfma_f32_16x16x32_bf16 v[42:45], v[142:145], v[174:177], v[42:45]
	v_mfma_f32_16x16x32_bf16 v[30:33], v[134:137], v[182:185], v[30:33]
	v_mfma_f32_16x16x32_bf16 v[26:29], v[142:145], v[182:185], v[26:29]
	v_mfma_f32_16x16x32_bf16 v[14:17], v[134:137], v[190:193], v[14:17]
	v_mfma_f32_16x16x32_bf16 v[10:13], v[142:145], v[190:193], v[10:13]
	v_mfma_f32_16x16x32_bf16 v[54:57], v[146:149], v[162:165], v[54:57]
	v_mfma_f32_16x16x32_bf16 v[50:53], v[154:157], v[162:165], v[50:53]
	v_mfma_f32_16x16x32_bf16 v[38:41], v[146:149], v[170:173], v[38:41]
	v_mfma_f32_16x16x32_bf16 v[34:37], v[154:157], v[170:173], v[34:37]
	v_mfma_f32_16x16x32_bf16 v[22:25], v[146:149], v[178:181], v[22:25]
	v_mfma_f32_16x16x32_bf16 v[18:21], v[154:157], v[178:181], v[18:21]
	v_mfma_f32_16x16x32_bf16 v[6:9], v[146:149], v[186:189], v[6:9]
	v_mfma_f32_16x16x32_bf16 v[2:5], v[154:157], v[186:189], v[2:5]
	v_mfma_f32_16x16x32_bf16 v[54:57], v[150:153], v[166:169], v[54:57]
	v_mfma_f32_16x16x32_bf16 v[50:53], v[158:161], v[166:169], v[50:53]
	v_mfma_f32_16x16x32_bf16 v[38:41], v[150:153], v[174:177], v[38:41]
	v_mfma_f32_16x16x32_bf16 v[34:37], v[158:161], v[174:177], v[34:37]
	v_mfma_f32_16x16x32_bf16 v[22:25], v[150:153], v[182:185], v[22:25]
	v_mfma_f32_16x16x32_bf16 v[18:21], v[158:161], v[182:185], v[18:21]
	v_mfma_f32_16x16x32_bf16 v[6:9], v[150:153], v[190:193], v[6:9]
	v_mfma_f32_16x16x32_bf16 v[2:5], v[158:161], v[190:193], v[2:5]
	s_barrier
	s_add_i32 s67, s67, 2
	s_add_u32 s34, s34, 0x100
	s_addc_u32 s35, s35, 0
	s_cmp_gt_u32 s67, 29
	s_cbranch_scc1 .LBB0_923

.LBB0_919:
	s_add_u32 s38, s30, s34
	s_addc_u32 s39, s31, s35
	s_add_u32 s38, s38, 0x100
	s_addc_u32 s39, s39, 0
	s_add_u32 s44, s65, s34
	s_addc_u32 s45, s66, s35
	s_waitcnt lgkmcnt(0)
	s_cmpk_eq_i32 s34, 0xf00
	s_cselect_b32 s41, s23, s39
	s_cselect_b32 s40, s29, s38
	s_cselect_b32 s39, s21, s45
	s_cselect_b32 s38, s64, s44
	s_barrier
	s_waitcnt lgkmcnt(0)
	v_mfma_f32_16x16x32_bf16 v[126:129], v[146:149], v[186:189], v[126:129]
	v_mfma_f32_16x16x32_bf16 v[122:125], v[154:157], v[186:189], v[122:125]
	v_mfma_f32_16x16x32_bf16 v[110:113], v[146:149], v[178:181], v[110:113]
	v_mfma_f32_16x16x32_bf16 v[106:109], v[154:157], v[178:181], v[106:109]
	v_mfma_f32_16x16x32_bf16 v[94:97], v[146:149], v[170:173], v[94:97]
	v_mfma_f32_16x16x32_bf16 v[90:93], v[154:157], v[170:173], v[90:93]
	v_mfma_f32_16x16x32_bf16 v[78:81], v[146:149], v[162:165], v[78:81]
	v_mfma_f32_16x16x32_bf16 v[74:77], v[154:157], v[162:165], v[74:77]
	v_mfma_f32_16x16x32_bf16 v[126:129], v[150:153], v[190:193], v[126:129]
	v_mfma_f32_16x16x32_bf16 v[122:125], v[158:161], v[190:193], v[122:125]
	v_mfma_f32_16x16x32_bf16 v[110:113], v[150:153], v[182:185], v[110:113]
	v_mfma_f32_16x16x32_bf16 v[106:109], v[158:161], v[182:185], v[106:109]
	v_mfma_f32_16x16x32_bf16 v[94:97], v[150:153], v[174:177], v[94:97]
	v_mfma_f32_16x16x32_bf16 v[90:93], v[158:161], v[174:177], v[90:93]
	v_mfma_f32_16x16x32_bf16 v[78:81], v[150:153], v[166:169], v[78:81]
	v_mfma_f32_16x16x32_bf16 v[74:77], v[158:161], v[166:169], v[74:77]
	v_mfma_f32_16x16x32_bf16 v[118:121], v[130:133], v[186:189], v[118:121]
	v_mfma_f32_16x16x32_bf16 v[114:117], v[138:141], v[186:189], v[114:117]
	v_mfma_f32_16x16x32_bf16 v[102:105], v[130:133], v[178:181], v[102:105]
	v_mfma_f32_16x16x32_bf16 v[98:101], v[138:141], v[178:181], v[98:101]
	v_mfma_f32_16x16x32_bf16 v[86:89], v[130:133], v[170:173], v[86:89]
	v_mfma_f32_16x16x32_bf16 v[82:85], v[138:141], v[170:173], v[82:85]
	v_mfma_f32_16x16x32_bf16 v[70:73], v[130:133], v[162:165], v[70:73]
	v_mfma_f32_16x16x32_bf16 v[66:69], v[138:141], v[162:165], v[66:69]
	v_mfma_f32_16x16x32_bf16 v[118:121], v[134:137], v[190:193], v[118:121]
	v_mfma_f32_16x16x32_bf16 v[114:117], v[142:145], v[190:193], v[114:117]
	v_mfma_f32_16x16x32_bf16 v[102:105], v[134:137], v[182:185], v[102:105]
	v_mfma_f32_16x16x32_bf16 v[98:101], v[142:145], v[182:185], v[98:101]
	v_mfma_f32_16x16x32_bf16 v[86:89], v[134:137], v[174:177], v[86:89]
	v_mfma_f32_16x16x32_bf16 v[82:85], v[142:145], v[174:177], v[82:85]
	v_mfma_f32_16x16x32_bf16 v[70:73], v[134:137], v[166:169], v[70:73]
	v_mfma_f32_16x16x32_bf16 v[66:69], v[142:145], v[166:169], v[66:69]
	s_barrier
	s_mov_b32 m0, s51
	v_lshl_add_u64 v[222:223], s[38:39], 0, v[196:197]
	s_add_u32 s44, s38, 0x80000
	ds_read_b128 v[186:189], v227 offset:16384
	ds_read_b128 v[190:193], v227 offset:17408
	ds_read_b128 v[178:181], v227 offset:18432
	ds_read_b128 v[182:185], v227 offset:19456
	ds_read_b128 v[170:173], v227 offset:20480
	ds_read_b128 v[174:177], v227 offset:21504
	ds_read_b128 v[162:165], v227 offset:22528
	ds_read_b128 v[166:169], v227 offset:23552
	global_load_lds_dwordx4 v[222:223], off
	v_lshl_add_u64 v[220:221], s[38:39], 0, v[202:203]
	s_mov_b32 m0, s52
	s_addc_u32 s45, s39, 0
	global_load_lds_dwordx4 v[220:221], off
	v_lshl_add_u64 v[216:217], s[44:45], 0, v[196:197]
	s_mov_b32 m0, s53
	v_lshl_add_u64 v[218:219], s[40:41], 0, v[200:201]
	global_load_lds_dwordx4 v[216:217], off
	v_lshl_add_u64 v[216:217], s[44:45], 0, v[202:203]
	s_mov_b32 m0, s54
	s_mov_b64 s[44:45], -1
	global_load_lds_dwordx4 v[216:217], off
	v_lshl_add_u64 v[216:217], s[40:41], 0, v[194:195]
	s_mov_b32 m0, s50
	s_and_b64 vcc, exec, s[42:43]
	global_load_lds_dwordx4 v[216:217], off
	s_mov_b32 m0, s55
	s_nop 0
	global_load_lds_dwordx4 v[218:219], off
	s_cbranch_vccz .LBB0_921
	s_waitcnt vmcnt(8)
	s_mov_b64 s[44:45], 0

.LBB0_1271:
	s_waitcnt lgkmcnt(0)
	v_mov_b32_e32 v203, v201
	v_lshl_add_u64 v[218:219], s[38:39], 0, v[200:201]
	v_lshl_add_u64 v[220:221], s[38:39], 0, v[202:203]
	s_barrier
	s_waitcnt lgkmcnt(0)
	v_mfma_scale_f32_16x16x128_f8f6f4 v[126:129], v[26:33], v[58:65], v[126:129], v225, v225 op_sel_hi:[0,0,0]
	v_mfma_scale_f32_16x16x128_f8f6f4 v[118:121], v[18:25], v[58:65], v[118:121], v225, v225 op_sel_hi:[0,0,0]
	v_mfma_scale_f32_16x16x128_f8f6f4 v[110:113], v[26:33], v[50:57], v[110:113], v225, v225 op_sel_hi:[0,0,0]
	v_mfma_scale_f32_16x16x128_f8f6f4 v[102:105], v[18:25], v[50:57], v[102:105], v225, v225 op_sel_hi:[0,0,0]
	v_mfma_scale_f32_16x16x128_f8f6f4 v[94:97], v[26:33], v[42:49], v[94:97], v225, v225 op_sel_hi:[0,0,0]
	v_mfma_scale_f32_16x16x128_f8f6f4 v[86:89], v[18:25], v[42:49], v[86:89], v225, v225 op_sel_hi:[0,0,0]
	v_mfma_scale_f32_16x16x128_f8f6f4 v[78:81], v[26:33], v[34:41], v[78:81], v225, v225 op_sel_hi:[0,0,0]
	v_mfma_scale_f32_16x16x128_f8f6f4 v[70:73], v[18:25], v[34:41], v[70:73], v225, v225 op_sel_hi:[0,0,0]
	v_mfma_scale_f32_16x16x128_f8f6f4 v[122:125], v[10:17], v[58:65], v[122:125], v225, v225 op_sel_hi:[0,0,0]
	v_mfma_scale_f32_16x16x128_f8f6f4 v[114:117], v[2:9], v[58:65], v[114:117], v225, v225 op_sel_hi:[0,0,0]
	v_mfma_scale_f32_16x16x128_f8f6f4 v[106:109], v[10:17], v[50:57], v[106:109], v225, v225 op_sel_hi:[0,0,0]
	v_mfma_scale_f32_16x16x128_f8f6f4 v[98:101], v[2:9], v[50:57], v[98:101], v225, v225 op_sel_hi:[0,0,0]
	v_mfma_scale_f32_16x16x128_f8f6f4 v[90:93], v[10:17], v[42:49], v[90:93], v225, v225 op_sel_hi:[0,0,0]
	v_mfma_scale_f32_16x16x128_f8f6f4 v[82:85], v[2:9], v[42:49], v[82:85], v225, v225 op_sel_hi:[0,0,0]
	v_mfma_scale_f32_16x16x128_f8f6f4 v[74:77], v[10:17], v[34:41], v[74:77], v225, v225 op_sel_hi:[0,0,0]
	v_mfma_scale_f32_16x16x128_f8f6f4 v[66:69], v[2:9], v[34:41], v[66:69], v225, v225 op_sel_hi:[0,0,0]
	s_barrier
	s_add_i32 s40, 0, 0x18000
	s_add_i32 s41, 0, 0x1c000
	v_add_u32_e32 v14, s40, v223
	v_add_u32_e32 v30, s41, v223
	ds_read_b128 v[2:5], v14
	ds_read_b128 v[6:9], v14 offset:1024
	ds_read_b128 v[10:13], v14 offset:2048
	ds_read_b128 v[14:17], v14 offset:3072
	ds_read_b128 v[18:21], v30
	ds_read_b128 v[22:25], v30 offset:1024
	ds_read_b128 v[26:29], v30 offset:2048
	ds_read_b128 v[30:33], v30 offset:3072
	s_mov_b32 m0, s52
	ds_read_b128 v[34:37], v226 offset:32768
	ds_read_b128 v[38:41], v226 offset:33792
	ds_read_b128 v[42:45], v226 offset:34816
	ds_read_b128 v[46:49], v226 offset:35840
	ds_read_b128 v[50:53], v226 offset:36864
	ds_read_b128 v[54:57], v226 offset:37888
	ds_read_b128 v[58:61], v226 offset:38912
	ds_read_b128 v[62:65], v226 offset:39936
	global_load_lds_dwordx4 v204, s[38:39]
	s_mov_b32 m0, s53
	s_nop 0
	global_load_lds_dwordx4 v206, s[38:39]
	s_waitcnt vmcnt(8)
	s_waitcnt lgkmcnt(0)
	s_barrier
	s_waitcnt lgkmcnt(0)
	v_mfma_scale_f32_16x16x128_f8f6f4 v[190:193], v[2:9], v[34:41], v[190:193], v225, v225 op_sel_hi:[0,0,0]
	v_mfma_scale_f32_16x16x128_f8f6f4 v[186:189], v[10:17], v[34:41], v[186:189], v225, v225 op_sel_hi:[0,0,0]
	v_mfma_scale_f32_16x16x128_f8f6f4 v[174:177], v[2:9], v[42:49], v[174:177], v225, v225 op_sel_hi:[0,0,0]
	v_mfma_scale_f32_16x16x128_f8f6f4 v[166:169], v[10:17], v[42:49], v[166:169], v225, v225 op_sel_hi:[0,0,0]
	v_mfma_scale_f32_16x16x128_f8f6f4 v[158:161], v[2:9], v[50:57], v[158:161], v225, v225 op_sel_hi:[0,0,0]
	v_mfma_scale_f32_16x16x128_f8f6f4 v[150:153], v[10:17], v[50:57], v[150:153], v225, v225 op_sel_hi:[0,0,0]
	v_mfma_scale_f32_16x16x128_f8f6f4 v[142:145], v[2:9], v[58:65], v[142:145], v225, v225 op_sel_hi:[0,0,0]
	v_mfma_scale_f32_16x16x128_f8f6f4 v[134:137], v[10:17], v[58:65], v[134:137], v225, v225 op_sel_hi:[0,0,0]
	v_mfma_scale_f32_16x16x128_f8f6f4 v[182:185], v[18:25], v[34:41], v[182:185], v225, v225 op_sel_hi:[0,0,0]
	v_mfma_scale_f32_16x16x128_f8f6f4 v[178:181], v[26:33], v[34:41], v[178:181], v225, v225 op_sel_hi:[0,0,0]
	v_mfma_scale_f32_16x16x128_f8f6f4 v[170:173], v[18:25], v[42:49], v[170:173], v225, v225 op_sel_hi:[0,0,0]
	v_mfma_scale_f32_16x16x128_f8f6f4 v[162:165], v[26:33], v[42:49], v[162:165], v225, v225 op_sel_hi:[0,0,0]
	v_mfma_scale_f32_16x16x128_f8f6f4 v[154:157], v[18:25], v[50:57], v[154:157], v225, v225 op_sel_hi:[0,0,0]
	v_mfma_scale_f32_16x16x128_f8f6f4 v[146:149], v[26:33], v[50:57], v[146:149], v225, v225 op_sel_hi:[0,0,0]
	v_mfma_scale_f32_16x16x128_f8f6f4 v[138:141], v[18:25], v[58:65], v[138:141], v225, v225 op_sel_hi:[0,0,0]
	v_mfma_scale_f32_16x16x128_f8f6f4 v[130:133], v[26:33], v[58:65], v[130:133], v225, v225 op_sel_hi:[0,0,0]
	s_barrier
	s_add_i32 s38, s40, s44
	v_lshl_add_u64 v[216:217], v[216:217], 0, s[10:11]
	s_mov_b32 m0, s38
	ds_read_b128 v[34:37], v226 offset:49152
	ds_read_b128 v[38:41], v226 offset:50176
	ds_read_b128 v[42:45], v226 offset:51200
	ds_read_b128 v[46:49], v226 offset:52224
	ds_read_b128 v[50:53], v226 offset:53248
	ds_read_b128 v[54:57], v226 offset:54272
	ds_read_b128 v[58:61], v226 offset:55296
	ds_read_b128 v[62:65], v226 offset:56320
	global_load_lds_dwordx4 v[216:217], off
	s_add_i32 m0, s38, 0x2000
	s_add_u32 s36, s36, 0x40080
	v_lshl_add_u64 v[214:215], v[214:215], 0, s[10:11]
	s_addc_u32 s37, s37, 0
	s_add_i32 s38, s41, s44
	global_load_lds_dwordx4 v[214:215], off
	v_lshl_add_u64 v[214:215], s[36:37], 0, v[196:197]
	s_mov_b32 m0, s38
	s_nop 0
	global_load_lds_dwordx4 v[214:215], off
	v_lshl_add_u64 v[214:215], s[36:37], 0, v[194:195]
	s_add_i32 m0, s38, 0x2000
	s_nop 0
	global_load_lds_dwordx4 v[214:215], off
	v_lshl_add_u64 v[214:215], v[218:219], 0, s[10:11]
	s_mov_b32 m0, s54
	s_nop 0
	global_load_lds_dwordx4 v[214:215], off
	v_lshl_add_u64 v[214:215], v[220:221], 0, s[10:11]
	s_mov_b32 m0, s55
	s_nop 0
	global_load_lds_dwordx4 v[214:215], off
	s_waitcnt vmcnt(8)
	s_waitcnt lgkmcnt(0)
	s_barrier
	s_waitcnt lgkmcnt(0)
	v_mfma_scale_f32_16x16x128_f8f6f4 v[126:129], v[2:9], v[34:41], v[126:129], v225, v225 op_sel_hi:[0,0,0]
	v_mfma_scale_f32_16x16x128_f8f6f4 v[118:121], v[10:17], v[34:41], v[118:121], v225, v225 op_sel_hi:[0,0,0]
	v_mfma_scale_f32_16x16x128_f8f6f4 v[110:113], v[2:9], v[42:49], v[110:113], v225, v225 op_sel_hi:[0,0,0]
	v_mfma_scale_f32_16x16x128_f8f6f4 v[102:105], v[10:17], v[42:49], v[102:105], v225, v225 op_sel_hi:[0,0,0]
	v_mfma_scale_f32_16x16x128_f8f6f4 v[94:97], v[2:9], v[50:57], v[94:97], v225, v225 op_sel_hi:[0,0,0]
	v_mfma_scale_f32_16x16x128_f8f6f4 v[86:89], v[10:17], v[50:57], v[86:89], v225, v225 op_sel_hi:[0,0,0]
	v_mfma_scale_f32_16x16x128_f8f6f4 v[78:81], v[2:9], v[58:65], v[78:81], v225, v225 op_sel_hi:[0,0,0]
	v_mfma_scale_f32_16x16x128_f8f6f4 v[70:73], v[10:17], v[58:65], v[70:73], v225, v225 op_sel_hi:[0,0,0]
	v_mfma_scale_f32_16x16x128_f8f6f4 v[122:125], v[18:25], v[34:41], v[122:125], v225, v225 op_sel_hi:[0,0,0]
	v_mfma_scale_f32_16x16x128_f8f6f4 v[114:117], v[26:33], v[34:41], v[114:117], v225, v225 op_sel_hi:[0,0,0]
	v_mfma_scale_f32_16x16x128_f8f6f4 v[106:109], v[18:25], v[42:49], v[106:109], v225, v225 op_sel_hi:[0,0,0]
	v_mfma_scale_f32_16x16x128_f8f6f4 v[98:101], v[26:33], v[42:49], v[98:101], v225, v225 op_sel_hi:[0,0,0]
	v_mfma_scale_f32_16x16x128_f8f6f4 v[90:93], v[18:25], v[50:57], v[90:93], v225, v225 op_sel_hi:[0,0,0]
	v_mfma_scale_f32_16x16x128_f8f6f4 v[82:85], v[26:33], v[50:57], v[82:85], v225, v225 op_sel_hi:[0,0,0]
	v_mfma_scale_f32_16x16x128_f8f6f4 v[74:77], v[18:25], v[58:65], v[74:77], v225, v225 op_sel_hi:[0,0,0]
	v_mfma_scale_f32_16x16x128_f8f6f4 v[66:69], v[26:33], v[58:65], v[66:69], v225, v225 op_sel_hi:[0,0,0]
	s_barrier
	s_add_i32 s68, s68, 2
	s_add_u32 s30, s30, 0x100
	s_addc_u32 s31, s31, 0
	s_cmp_gt_u32 s68, 13
	s_cbranch_scc1 .LBB0_1282

.LBB0_1278:
	s_add_u32 s38, s82, s30
	s_addc_u32 s39, s83, s31
	s_add_u32 s42, s38, 0x74800100
	s_addc_u32 s43, s39, 0
	s_and_b64 s[38:39], s[36:37], exec
	s_cselect_b32 s39, s3, s43
	s_cselect_b32 s38, s2, s42
	s_add_u32 s42, s66, s30
	s_addc_u32 s43, s67, s31
	s_waitcnt lgkmcnt(0)
	s_and_b64 s[36:37], s[36:37], exec
	s_cselect_b32 s37, s25, s43
	s_cselect_b32 s36, s64, s42
	s_barrier
	s_waitcnt lgkmcnt(0)
	v_mfma_scale_f32_16x16x128_f8f6f4 v[190:193], v[26:33], v[58:65], v[190:193], v225, v225 op_sel_hi:[0,0,0]
	v_mfma_scale_f32_16x16x128_f8f6f4 v[186:189], v[18:25], v[58:65], v[186:189], v225, v225 op_sel_hi:[0,0,0]
	v_mfma_scale_f32_16x16x128_f8f6f4 v[174:177], v[26:33], v[50:57], v[174:177], v225, v225 op_sel_hi:[0,0,0]
	v_mfma_scale_f32_16x16x128_f8f6f4 v[166:169], v[18:25], v[50:57], v[166:169], v225, v225 op_sel_hi:[0,0,0]
	v_mfma_scale_f32_16x16x128_f8f6f4 v[158:161], v[26:33], v[42:49], v[158:161], v225, v225 op_sel_hi:[0,0,0]
	v_mfma_scale_f32_16x16x128_f8f6f4 v[150:153], v[18:25], v[42:49], v[150:153], v225, v225 op_sel_hi:[0,0,0]
	v_mfma_scale_f32_16x16x128_f8f6f4 v[142:145], v[26:33], v[34:41], v[142:145], v225, v225 op_sel_hi:[0,0,0]
	v_mfma_scale_f32_16x16x128_f8f6f4 v[134:137], v[18:25], v[34:41], v[134:137], v225, v225 op_sel_hi:[0,0,0]
	v_mfma_scale_f32_16x16x128_f8f6f4 v[182:185], v[10:17], v[58:65], v[182:185], v225, v225 op_sel_hi:[0,0,0]
	v_mfma_scale_f32_16x16x128_f8f6f4 v[178:181], v[2:9], v[58:65], v[178:181], v225, v225 op_sel_hi:[0,0,0]
	v_mfma_scale_f32_16x16x128_f8f6f4 v[170:173], v[10:17], v[50:57], v[170:173], v225, v225 op_sel_hi:[0,0,0]
	v_mfma_scale_f32_16x16x128_f8f6f4 v[162:165], v[2:9], v[50:57], v[162:165], v225, v225 op_sel_hi:[0,0,0]
	v_mfma_scale_f32_16x16x128_f8f6f4 v[154:157], v[10:17], v[42:49], v[154:157], v225, v225 op_sel_hi:[0,0,0]
	v_mfma_scale_f32_16x16x128_f8f6f4 v[146:149], v[2:9], v[42:49], v[146:149], v225, v225 op_sel_hi:[0,0,0]
	v_mfma_scale_f32_16x16x128_f8f6f4 v[138:141], v[10:17], v[34:41], v[138:141], v225, v225 op_sel_hi:[0,0,0]
	v_mfma_scale_f32_16x16x128_f8f6f4 v[130:133], v[2:9], v[34:41], v[130:133], v225, v225 op_sel_hi:[0,0,0]
	s_barrier
	s_mov_b32 m0, s47
	v_lshl_add_u64 v[216:217], s[36:37], 0, v[196:197]
	s_add_u32 s42, s36, 0x40000
	ds_read_b128 v[58:61], v226 offset:16384
	ds_read_b128 v[62:65], v226 offset:17408
	ds_read_b128 v[50:53], v226 offset:18432
	ds_read_b128 v[54:57], v226 offset:19456
	ds_read_b128 v[42:45], v226 offset:20480
	ds_read_b128 v[46:49], v226 offset:21504
	ds_read_b128 v[34:37], v226 offset:22528
	ds_read_b128 v[38:41], v226 offset:23552
	global_load_lds_dwordx4 v[216:217], off
	v_lshl_add_u64 v[214:215], s[36:37], 0, v[194:195]
	s_mov_b32 m0, s48
	s_addc_u32 s43, s37, 0
	global_load_lds_dwordx4 v[214:215], off
	v_lshl_add_u64 v[218:219], s[42:43], 0, v[196:197]
	s_mov_b32 m0, s49
	s_and_b64 vcc, exec, s[40:41]
	global_load_lds_dwordx4 v[218:219], off
	v_lshl_add_u64 v[218:219], s[42:43], 0, v[194:195]
	s_mov_b32 m0, s50
	s_mov_b64 s[42:43], -1
	global_load_lds_dwordx4 v[218:219], off
	s_mov_b32 m0, s29
	s_nop 0
	global_load_lds_dwordx4 v200, s[38:39]
	s_mov_b32 m0, s51
	s_nop 0
	global_load_lds_dwordx4 v202, s[38:39]
	s_cbranch_vccz .LBB0_1280
	s_waitcnt vmcnt(8)
	s_mov_b64 s[42:43], 0

.LBB0_1354:
	s_waitcnt lgkmcnt(0)
	s_barrier
	s_waitcnt lgkmcnt(0)
	v_mfma_scale_f32_16x16x128_f8f6f4 v[126:129], v[26:33], v[58:65], v[126:129], v228, v228 op_sel_hi:[0,0,0]
	v_mfma_scale_f32_16x16x128_f8f6f4 v[122:125], v[18:25], v[58:65], v[122:125], v228, v228 op_sel_hi:[0,0,0]
	v_mfma_scale_f32_16x16x128_f8f6f4 v[114:117], v[26:33], v[50:57], v[114:117], v228, v228 op_sel_hi:[0,0,0]
	v_mfma_scale_f32_16x16x128_f8f6f4 v[106:109], v[18:25], v[50:57], v[106:109], v228, v228 op_sel_hi:[0,0,0]
	v_mfma_scale_f32_16x16x128_f8f6f4 v[98:101], v[26:33], v[42:49], v[98:101], v228, v228 op_sel_hi:[0,0,0]
	v_mfma_scale_f32_16x16x128_f8f6f4 v[90:93], v[18:25], v[42:49], v[90:93], v228, v228 op_sel_hi:[0,0,0]
	v_mfma_scale_f32_16x16x128_f8f6f4 v[82:85], v[26:33], v[34:41], v[82:85], v228, v228 op_sel_hi:[0,0,0]
	v_mfma_scale_f32_16x16x128_f8f6f4 v[74:77], v[18:25], v[34:41], v[74:77], v228, v228 op_sel_hi:[0,0,0]
	v_mfma_scale_f32_16x16x128_f8f6f4 v[118:121], v[10:17], v[58:65], v[118:121], v228, v228 op_sel_hi:[0,0,0]
	v_mfma_scale_f32_16x16x128_f8f6f4 v[110:113], v[2:9], v[58:65], v[110:113], v228, v228 op_sel_hi:[0,0,0]
	v_mfma_scale_f32_16x16x128_f8f6f4 v[102:105], v[10:17], v[50:57], v[102:105], v228, v228 op_sel_hi:[0,0,0]
	v_mfma_scale_f32_16x16x128_f8f6f4 v[94:97], v[2:9], v[50:57], v[94:97], v228, v228 op_sel_hi:[0,0,0]
	v_mfma_scale_f32_16x16x128_f8f6f4 v[86:89], v[10:17], v[42:49], v[86:89], v228, v228 op_sel_hi:[0,0,0]
	v_mfma_scale_f32_16x16x128_f8f6f4 v[78:81], v[2:9], v[42:49], v[78:81], v228, v228 op_sel_hi:[0,0,0]
	v_mfma_scale_f32_16x16x128_f8f6f4 v[70:73], v[10:17], v[34:41], v[70:73], v228, v228 op_sel_hi:[0,0,0]
	v_mfma_scale_f32_16x16x128_f8f6f4 v[66:69], v[2:9], v[34:41], v[66:69], v228, v228 op_sel_hi:[0,0,0]
	s_barrier
	s_add_i32 s50, 0, 0x18000
	s_add_i32 s51, 0, 0x1c000
	v_add_u32_e32 v14, s50, v199
	v_add_u32_e32 v30, s51, v199
	ds_read_b128 v[2:5], v14
	ds_read_b128 v[6:9], v14 offset:1024
	ds_read_b128 v[10:13], v14 offset:2048
	ds_read_b128 v[14:17], v14 offset:3072
	ds_read_b128 v[18:21], v30
	ds_read_b128 v[22:25], v30 offset:1024
	ds_read_b128 v[26:29], v30 offset:2048
	ds_read_b128 v[30:33], v30 offset:3072
	s_add_u32 s48, s48, 0x40000
	s_addc_u32 s49, s49, 0
	s_mov_b32 m0, s63
	v_lshl_add_u64 v[230:231], s[48:49], 0, v[202:203]
	ds_read_b128 v[34:37], v227 offset:32768
	ds_read_b128 v[38:41], v227 offset:33792
	ds_read_b128 v[42:45], v227 offset:34816
	ds_read_b128 v[46:49], v227 offset:35840
	ds_read_b128 v[50:53], v227 offset:36864
	ds_read_b128 v[54:57], v227 offset:37888
	ds_read_b128 v[58:61], v227 offset:38912
	ds_read_b128 v[62:65], v227 offset:39936
	global_load_lds_dwordx4 v[230:231], off
	v_lshl_add_u64 v[230:231], s[48:49], 0, v[196:197]
	s_mov_b32 m0, s64
	s_nop 0
	global_load_lds_dwordx4 v[230:231], off
	s_waitcnt vmcnt(8)
	s_waitcnt lgkmcnt(0)
	s_barrier
	s_waitcnt lgkmcnt(0)
	v_mfma_scale_f32_16x16x128_f8f6f4 v[190:193], v[2:9], v[34:41], v[190:193], v228, v228 op_sel_hi:[0,0,0]
	v_mfma_scale_f32_16x16x128_f8f6f4 v[186:189], v[10:17], v[34:41], v[186:189], v228, v228 op_sel_hi:[0,0,0]
	v_mfma_scale_f32_16x16x128_f8f6f4 v[182:185], v[2:9], v[42:49], v[182:185], v228, v228 op_sel_hi:[0,0,0]
	v_mfma_scale_f32_16x16x128_f8f6f4 v[178:181], v[10:17], v[42:49], v[178:181], v228, v228 op_sel_hi:[0,0,0]
	v_mfma_scale_f32_16x16x128_f8f6f4 v[174:177], v[2:9], v[50:57], v[174:177], v228, v228 op_sel_hi:[0,0,0]
	v_mfma_scale_f32_16x16x128_f8f6f4 v[154:157], v[10:17], v[50:57], v[154:157], v228, v228 op_sel_hi:[0,0,0]
	v_mfma_scale_f32_16x16x128_f8f6f4 v[146:149], v[2:9], v[58:65], v[146:149], v228, v228 op_sel_hi:[0,0,0]
	v_mfma_scale_f32_16x16x128_f8f6f4 v[138:141], v[10:17], v[58:65], v[138:141], v228, v228 op_sel_hi:[0,0,0]
	v_mfma_scale_f32_16x16x128_f8f6f4 v[170:173], v[18:25], v[34:41], v[170:173], v228, v228 op_sel_hi:[0,0,0]
	v_mfma_scale_f32_16x16x128_f8f6f4 v[166:169], v[26:33], v[34:41], v[166:169], v228, v228 op_sel_hi:[0,0,0]
	v_mfma_scale_f32_16x16x128_f8f6f4 v[162:165], v[18:25], v[42:49], v[162:165], v228, v228 op_sel_hi:[0,0,0]
	v_mfma_scale_f32_16x16x128_f8f6f4 v[158:161], v[26:33], v[42:49], v[158:161], v228, v228 op_sel_hi:[0,0,0]
	v_mfma_scale_f32_16x16x128_f8f6f4 v[150:153], v[18:25], v[50:57], v[150:153], v228, v228 op_sel_hi:[0,0,0]
	v_mfma_scale_f32_16x16x128_f8f6f4 v[142:145], v[26:33], v[50:57], v[142:145], v228, v228 op_sel_hi:[0,0,0]
	v_mfma_scale_f32_16x16x128_f8f6f4 v[134:137], v[18:25], v[58:65], v[134:137], v228, v228 op_sel_hi:[0,0,0]
	v_mfma_scale_f32_16x16x128_f8f6f4 v[130:133], v[26:33], v[58:65], v[130:133], v228, v228 op_sel_hi:[0,0,0]
	s_barrier
	s_add_i32 s48, s50, s56
	v_lshl_add_u64 v[222:223], v[222:223], 0, s[12:13]
	s_mov_b32 m0, s48
	ds_read_b128 v[34:37], v227 offset:49152
	ds_read_b128 v[38:41], v227 offset:50176
	ds_read_b128 v[42:45], v227 offset:51200
	ds_read_b128 v[46:49], v227 offset:52224
	ds_read_b128 v[50:53], v227 offset:53248
	ds_read_b128 v[54:57], v227 offset:54272
	ds_read_b128 v[58:61], v227 offset:55296
	ds_read_b128 v[62:65], v227 offset:56320
	global_load_lds_dwordx4 v[222:223], off
	s_add_i32 m0, s48, 0x2000
	s_add_u32 s46, s46, 0x40080
	v_lshl_add_u64 v[220:221], v[220:221], 0, s[12:13]
	s_addc_u32 s47, s47, 0
	s_add_i32 s48, s51, s56
	global_load_lds_dwordx4 v[220:221], off
	v_lshl_add_u64 v[220:221], s[46:47], 0, v[200:201]
	s_mov_b32 m0, s48
	v_lshl_add_u64 v[216:217], v[216:217], 0, s[12:13]
	global_load_lds_dwordx4 v[220:221], off
	v_lshl_add_u64 v[220:221], s[46:47], 0, v[194:195]
	s_add_i32 m0, s48, 0x2000
	s_nop 0
	global_load_lds_dwordx4 v[220:221], off
	s_mov_b32 m0, s65
	s_nop 0
	global_load_lds_dwordx4 v[216:217], off
	v_lshl_add_u64 v[216:217], v[218:219], 0, s[12:13]
	s_mov_b32 m0, s66
	s_nop 0
	global_load_lds_dwordx4 v[216:217], off
	s_waitcnt vmcnt(8)
	s_waitcnt lgkmcnt(0)
	s_barrier
	s_waitcnt lgkmcnt(0)
	v_mfma_scale_f32_16x16x128_f8f6f4 v[126:129], v[2:9], v[34:41], v[126:129], v228, v228 op_sel_hi:[0,0,0]
	v_mfma_scale_f32_16x16x128_f8f6f4 v[122:125], v[10:17], v[34:41], v[122:125], v228, v228 op_sel_hi:[0,0,0]
	v_mfma_scale_f32_16x16x128_f8f6f4 v[114:117], v[2:9], v[42:49], v[114:117], v228, v228 op_sel_hi:[0,0,0]
	v_mfma_scale_f32_16x16x128_f8f6f4 v[106:109], v[10:17], v[42:49], v[106:109], v228, v228 op_sel_hi:[0,0,0]
	v_mfma_scale_f32_16x16x128_f8f6f4 v[98:101], v[2:9], v[50:57], v[98:101], v228, v228 op_sel_hi:[0,0,0]
	v_mfma_scale_f32_16x16x128_f8f6f4 v[90:93], v[10:17], v[50:57], v[90:93], v228, v228 op_sel_hi:[0,0,0]
	v_mfma_scale_f32_16x16x128_f8f6f4 v[82:85], v[2:9], v[58:65], v[82:85], v228, v228 op_sel_hi:[0,0,0]
	v_mfma_scale_f32_16x16x128_f8f6f4 v[74:77], v[10:17], v[58:65], v[74:77], v228, v228 op_sel_hi:[0,0,0]
	v_mfma_scale_f32_16x16x128_f8f6f4 v[118:121], v[18:25], v[34:41], v[118:121], v228, v228 op_sel_hi:[0,0,0]
	v_mfma_scale_f32_16x16x128_f8f6f4 v[110:113], v[26:33], v[34:41], v[110:113], v228, v228 op_sel_hi:[0,0,0]
	v_mfma_scale_f32_16x16x128_f8f6f4 v[102:105], v[18:25], v[42:49], v[102:105], v228, v228 op_sel_hi:[0,0,0]
	v_mfma_scale_f32_16x16x128_f8f6f4 v[94:97], v[26:33], v[42:49], v[94:97], v228, v228 op_sel_hi:[0,0,0]
	v_mfma_scale_f32_16x16x128_f8f6f4 v[86:89], v[18:25], v[50:57], v[86:89], v228, v228 op_sel_hi:[0,0,0]
	v_mfma_scale_f32_16x16x128_f8f6f4 v[78:81], v[26:33], v[50:57], v[78:81], v228, v228 op_sel_hi:[0,0,0]
	v_mfma_scale_f32_16x16x128_f8f6f4 v[70:73], v[18:25], v[58:65], v[70:73], v228, v228 op_sel_hi:[0,0,0]
	v_mfma_scale_f32_16x16x128_f8f6f4 v[66:69], v[26:33], v[58:65], v[66:69], v228, v228 op_sel_hi:[0,0,0]
	s_barrier
	s_add_i32 s77, s77, 2
	s_add_u32 s42, s42, 0x100
	s_addc_u32 s43, s43, 0
	s_cmp_gt_u32 s77, 13
	s_cbranch_scc1 .LBB0_1363

.LBB0_1359:
	s_add_u32 s46, s40, s42
	s_addc_u32 s47, s41, s43
	s_add_u32 s46, s46, 0x100
	s_addc_u32 s47, s47, 0
	s_add_u32 s52, s75, s42
	s_addc_u32 s53, s76, s43
	s_waitcnt lgkmcnt(0)
	s_cmpk_eq_i32 s42, 0x700
	s_cselect_b32 s49, s27, s47
	s_cselect_b32 s48, s73, s46
	s_cselect_b32 s47, s29, s53
	s_cselect_b32 s46, s74, s52
	s_barrier
	s_waitcnt lgkmcnt(0)
	v_mfma_scale_f32_16x16x128_f8f6f4 v[190:193], v[26:33], v[58:65], v[190:193], v228, v228 op_sel_hi:[0,0,0]
	v_mfma_scale_f32_16x16x128_f8f6f4 v[186:189], v[18:25], v[58:65], v[186:189], v228, v228 op_sel_hi:[0,0,0]
	v_mfma_scale_f32_16x16x128_f8f6f4 v[182:185], v[26:33], v[50:57], v[182:185], v228, v228 op_sel_hi:[0,0,0]
	v_mfma_scale_f32_16x16x128_f8f6f4 v[178:181], v[18:25], v[50:57], v[178:181], v228, v228 op_sel_hi:[0,0,0]
	v_mfma_scale_f32_16x16x128_f8f6f4 v[174:177], v[26:33], v[42:49], v[174:177], v228, v228 op_sel_hi:[0,0,0]
	v_mfma_scale_f32_16x16x128_f8f6f4 v[154:157], v[18:25], v[42:49], v[154:157], v228, v228 op_sel_hi:[0,0,0]
	v_mfma_scale_f32_16x16x128_f8f6f4 v[146:149], v[26:33], v[34:41], v[146:149], v228, v228 op_sel_hi:[0,0,0]
	v_mfma_scale_f32_16x16x128_f8f6f4 v[138:141], v[18:25], v[34:41], v[138:141], v228, v228 op_sel_hi:[0,0,0]
	v_mfma_scale_f32_16x16x128_f8f6f4 v[170:173], v[10:17], v[58:65], v[170:173], v228, v228 op_sel_hi:[0,0,0]
	v_mfma_scale_f32_16x16x128_f8f6f4 v[166:169], v[2:9], v[58:65], v[166:169], v228, v228 op_sel_hi:[0,0,0]
	v_mfma_scale_f32_16x16x128_f8f6f4 v[162:165], v[10:17], v[50:57], v[162:165], v228, v228 op_sel_hi:[0,0,0]
	v_mfma_scale_f32_16x16x128_f8f6f4 v[158:161], v[2:9], v[50:57], v[158:161], v228, v228 op_sel_hi:[0,0,0]
	v_mfma_scale_f32_16x16x128_f8f6f4 v[150:153], v[10:17], v[42:49], v[150:153], v228, v228 op_sel_hi:[0,0,0]
	v_mfma_scale_f32_16x16x128_f8f6f4 v[142:145], v[2:9], v[42:49], v[142:145], v228, v228 op_sel_hi:[0,0,0]
	v_mfma_scale_f32_16x16x128_f8f6f4 v[134:137], v[10:17], v[34:41], v[134:137], v228, v228 op_sel_hi:[0,0,0]
	v_mfma_scale_f32_16x16x128_f8f6f4 v[130:133], v[2:9], v[34:41], v[130:133], v228, v228 op_sel_hi:[0,0,0]
	s_barrier
	s_mov_b32 m0, s39
	v_lshl_add_u64 v[222:223], s[46:47], 0, v[200:201]
	s_add_u32 s52, s46, 0x40000
	ds_read_b128 v[58:61], v227 offset:16384
	ds_read_b128 v[62:65], v227 offset:17408
	ds_read_b128 v[50:53], v227 offset:18432
	ds_read_b128 v[54:57], v227 offset:19456
	ds_read_b128 v[42:45], v227 offset:20480
	ds_read_b128 v[46:49], v227 offset:21504
	ds_read_b128 v[34:37], v227 offset:22528
	ds_read_b128 v[38:41], v227 offset:23552
	global_load_lds_dwordx4 v[222:223], off
	v_lshl_add_u64 v[220:221], s[46:47], 0, v[194:195]
	s_mov_b32 m0, s59
	s_addc_u32 s53, s47, 0
	global_load_lds_dwordx4 v[220:221], off
	v_lshl_add_u64 v[216:217], s[52:53], 0, v[200:201]
	s_mov_b32 m0, s60
	v_lshl_add_u64 v[218:219], s[48:49], 0, v[196:197]
	global_load_lds_dwordx4 v[216:217], off
	v_lshl_add_u64 v[216:217], s[52:53], 0, v[194:195]
	s_mov_b32 m0, s61
	s_mov_b64 s[52:53], -1
	global_load_lds_dwordx4 v[216:217], off
	v_lshl_add_u64 v[216:217], s[48:49], 0, v[202:203]
	s_mov_b32 m0, s37
	s_and_b64 vcc, exec, s[50:51]
	global_load_lds_dwordx4 v[216:217], off
	s_mov_b32 m0, s62
	s_nop 0
	global_load_lds_dwordx4 v[218:219], off
	s_cbranch_vccz .LBB0_1361
	s_waitcnt vmcnt(8)
	s_mov_b64 s[52:53], 0

.LBB0_1479:
	ds_read_b128 v[18:21], v190
	ds_read_b128 v[22:25], v190 offset:1024
	ds_read_b128 v[26:29], v190 offset:2048
	ds_read_b128 v[30:33], v190 offset:3072
	ds_read_b128 v[2:5], v191
	ds_read_b128 v[6:9], v191 offset:1024
	ds_read_b128 v[10:13], v191 offset:2048
	ds_read_b128 v[14:17], v191 offset:3072
	s_add_u32 s26, s22, s24
	s_addc_u32 s27, s23, s25
	s_add_u32 s26, s26, 0x38a00100
	s_addc_u32 s27, s27, 0
	s_add_u32 s51, s38, s24
	s_addc_u32 s52, s39, s25
	s_cmpk_eq_i32 s24, 0x700
	s_cselect_b32 s29, s7, s27
	s_cselect_b32 s28, s6, s26
	s_cselect_b32 s27, s3, s52
	s_cselect_b32 s26, s2, s51
	s_mov_b32 m0, s41
	v_lshl_add_u64 v[196:197], v[170:171], 0, s[24:25]
	ds_read_b128 v[174:177], v192
	ds_read_b128 v[178:181], v192 offset:1024
	ds_read_b128 v[200:203], v192 offset:2048
	ds_read_b128 v[204:207], v192 offset:3072
	ds_read_b128 v[208:211], v192 offset:4096
	ds_read_b128 v[212:215], v192 offset:5120
	ds_read_b128 v[216:219], v192 offset:6144
	ds_read_b128 v[220:223], v192 offset:7168
	global_load_lds_dwordx4 v[196:197], off
	v_lshl_add_u64 v[196:197], v[172:173], 0, s[24:25]
	s_mov_b32 m0, s42
	s_nop 0
	global_load_lds_dwordx4 v[196:197], off
	s_waitcnt vmcnt(8)
	s_waitcnt lgkmcnt(0)
	s_barrier
	s_waitcnt lgkmcnt(0)
	v_mfma_scale_f32_16x16x128_f8f6f4 v[158:161], v[18:25], v[174:181], v[158:161], v193, v193 op_sel_hi:[0,0,0]
	v_mfma_scale_f32_16x16x128_f8f6f4 v[154:157], v[26:33], v[174:181], v[154:157], v193, v193 op_sel_hi:[0,0,0]
	v_mfma_scale_f32_16x16x128_f8f6f4 v[142:145], v[18:25], v[200:207], v[142:145], v193, v193 op_sel_hi:[0,0,0]
	v_mfma_scale_f32_16x16x128_f8f6f4 v[138:141], v[26:33], v[200:207], v[138:141], v193, v193 op_sel_hi:[0,0,0]
	v_mfma_scale_f32_16x16x128_f8f6f4 v[126:129], v[18:25], v[208:215], v[126:129], v193, v193 op_sel_hi:[0,0,0]
	v_mfma_scale_f32_16x16x128_f8f6f4 v[122:125], v[26:33], v[208:215], v[122:125], v193, v193 op_sel_hi:[0,0,0]
	v_mfma_scale_f32_16x16x128_f8f6f4 v[110:113], v[18:25], v[216:223], v[110:113], v193, v193 op_sel_hi:[0,0,0]
	v_mfma_scale_f32_16x16x128_f8f6f4 v[106:109], v[26:33], v[216:223], v[106:109], v193, v193 op_sel_hi:[0,0,0]
	v_mfma_scale_f32_16x16x128_f8f6f4 v[150:153], v[2:9], v[174:181], v[150:153], v193, v193 op_sel_hi:[0,0,0]
	v_mfma_scale_f32_16x16x128_f8f6f4 v[146:149], v[10:17], v[174:181], v[146:149], v193, v193 op_sel_hi:[0,0,0]
	v_mfma_scale_f32_16x16x128_f8f6f4 v[134:137], v[2:9], v[200:207], v[134:137], v193, v193 op_sel_hi:[0,0,0]
	v_mfma_scale_f32_16x16x128_f8f6f4 v[130:133], v[10:17], v[200:207], v[130:133], v193, v193 op_sel_hi:[0,0,0]
	v_mfma_scale_f32_16x16x128_f8f6f4 v[118:121], v[2:9], v[208:215], v[118:121], v193, v193 op_sel_hi:[0,0,0]
	v_mfma_scale_f32_16x16x128_f8f6f4 v[114:117], v[10:17], v[208:215], v[114:117], v193, v193 op_sel_hi:[0,0,0]
	v_mfma_scale_f32_16x16x128_f8f6f4 v[102:105], v[2:9], v[216:223], v[102:105], v193, v193 op_sel_hi:[0,0,0]
	v_mfma_scale_f32_16x16x128_f8f6f4 v[98:101], v[10:17], v[216:223], v[98:101], v193, v193 op_sel_hi:[0,0,0]
	s_barrier
	s_mov_b32 m0, s43
	v_lshl_add_u64 v[174:175], s[26:27], 0, v[164:165]
	s_add_u32 s52, s26, 0x40000
	ds_read_b128 v[200:203], v192 offset:16384
	ds_read_b128 v[204:207], v192 offset:17408
	ds_read_b128 v[208:211], v192 offset:18432
	ds_read_b128 v[212:215], v192 offset:19456
	ds_read_b128 v[216:219], v192 offset:20480
	ds_read_b128 v[220:223], v192 offset:21504
	ds_read_b128 v[224:227], v192 offset:22528
	ds_read_b128 v[228:231], v192 offset:23552
	global_load_lds_dwordx4 v[174:175], off
	v_lshl_add_u64 v[176:177], s[26:27], 0, v[168:169]
	s_mov_b32 m0, s44
	s_addc_u32 s53, s27, 0
	global_load_lds_dwordx4 v[176:177], off
	v_lshl_add_u64 v[178:179], s[52:53], 0, v[164:165]
	s_mov_b32 m0, s45
	v_lshl_add_u64 v[180:181], s[28:29], 0, v[166:167]
	global_load_lds_dwordx4 v[178:179], off
	v_lshl_add_u64 v[178:179], s[52:53], 0, v[168:169]
	s_mov_b32 m0, s46
	s_nop 0
	global_load_lds_dwordx4 v[178:179], off
	v_lshl_add_u64 v[178:179], s[28:29], 0, v[162:163]
	s_mov_b32 m0, s1
	s_nop 0
	global_load_lds_dwordx4 v[178:179], off
	s_mov_b32 m0, s31
	s_nop 0
	global_load_lds_dwordx4 v[180:181], off
	s_waitcnt vmcnt(8)
	s_waitcnt lgkmcnt(0)
	s_barrier
	s_waitcnt lgkmcnt(0)
	v_mfma_scale_f32_16x16x128_f8f6f4 v[94:97], v[18:25], v[200:207], v[94:97], v193, v193 op_sel_hi:[0,0,0]
	v_mfma_scale_f32_16x16x128_f8f6f4 v[90:93], v[26:33], v[200:207], v[90:93], v193, v193 op_sel_hi:[0,0,0]
	v_mfma_scale_f32_16x16x128_f8f6f4 v[78:81], v[18:25], v[208:215], v[78:81], v193, v193 op_sel_hi:[0,0,0]
	v_mfma_scale_f32_16x16x128_f8f6f4 v[74:77], v[26:33], v[208:215], v[74:77], v193, v193 op_sel_hi:[0,0,0]
	v_mfma_scale_f32_16x16x128_f8f6f4 v[62:65], v[18:25], v[216:223], v[62:65], v193, v193 op_sel_hi:[0,0,0]
	v_mfma_scale_f32_16x16x128_f8f6f4 v[58:61], v[26:33], v[216:223], v[58:61], v193, v193 op_sel_hi:[0,0,0]
	v_mfma_scale_f32_16x16x128_f8f6f4 v[46:49], v[18:25], v[224:231], v[46:49], v193, v193 op_sel_hi:[0,0,0]
	v_mfma_scale_f32_16x16x128_f8f6f4 v[42:45], v[26:33], v[224:231], v[42:45], v193, v193 op_sel_hi:[0,0,0]
	v_mfma_scale_f32_16x16x128_f8f6f4 v[86:89], v[2:9], v[200:207], v[86:89], v193, v193 op_sel_hi:[0,0,0]
	v_mfma_scale_f32_16x16x128_f8f6f4 v[82:85], v[10:17], v[200:207], v[82:85], v193, v193 op_sel_hi:[0,0,0]
	v_mfma_scale_f32_16x16x128_f8f6f4 v[70:73], v[2:9], v[208:215], v[70:73], v193, v193 op_sel_hi:[0,0,0]
	v_mfma_scale_f32_16x16x128_f8f6f4 v[66:69], v[10:17], v[208:215], v[66:69], v193, v193 op_sel_hi:[0,0,0]
	v_mfma_scale_f32_16x16x128_f8f6f4 v[54:57], v[2:9], v[216:223], v[54:57], v193, v193 op_sel_hi:[0,0,0]
	v_mfma_scale_f32_16x16x128_f8f6f4 v[50:53], v[10:17], v[216:223], v[50:53], v193, v193 op_sel_hi:[0,0,0]
	v_mfma_scale_f32_16x16x128_f8f6f4 v[38:41], v[2:9], v[224:231], v[38:41], v193, v193 op_sel_hi:[0,0,0]
	v_mfma_scale_f32_16x16x128_f8f6f4 v[34:37], v[10:17], v[224:231], v[34:37], v193, v193 op_sel_hi:[0,0,0]
	s_barrier
	ds_read_b128 v[2:5], v194
	ds_read_b128 v[6:9], v194 offset:1024
	ds_read_b128 v[10:13], v194 offset:2048
	ds_read_b128 v[14:17], v194 offset:3072
	ds_read_b128 v[18:21], v195
	ds_read_b128 v[22:25], v195 offset:1024
	ds_read_b128 v[26:29], v195 offset:2048
	ds_read_b128 v[30:33], v195 offset:3072
	s_add_u32 s28, s28, 0x40000
	s_addc_u32 s29, s29, 0
	s_mov_b32 m0, s34
	v_lshl_add_u64 v[196:197], s[28:29], 0, v[162:163]
	ds_read_b128 v[200:203], v192 offset:32768
	ds_read_b128 v[204:207], v192 offset:33792
	ds_read_b128 v[208:211], v192 offset:34816
	ds_read_b128 v[212:215], v192 offset:35840
	ds_read_b128 v[216:219], v192 offset:36864
	ds_read_b128 v[220:223], v192 offset:37888
	ds_read_b128 v[224:227], v192 offset:38912
	ds_read_b128 v[228:231], v192 offset:39936
	global_load_lds_dwordx4 v[196:197], off
	v_lshl_add_u64 v[196:197], s[28:29], 0, v[166:167]
	s_mov_b32 m0, s35
	s_nop 0
	global_load_lds_dwordx4 v[196:197], off
	s_waitcnt vmcnt(8)
	s_waitcnt lgkmcnt(0)
	s_barrier
	s_waitcnt lgkmcnt(0)
	v_mfma_scale_f32_16x16x128_f8f6f4 v[158:161], v[2:9], v[200:207], v[158:161], v193, v193 op_sel_hi:[0,0,0]
	v_mfma_scale_f32_16x16x128_f8f6f4 v[154:157], v[10:17], v[200:207], v[154:157], v193, v193 op_sel_hi:[0,0,0]
	v_mfma_scale_f32_16x16x128_f8f6f4 v[142:145], v[2:9], v[208:215], v[142:145], v193, v193 op_sel_hi:[0,0,0]
	v_mfma_scale_f32_16x16x128_f8f6f4 v[138:141], v[10:17], v[208:215], v[138:141], v193, v193 op_sel_hi:[0,0,0]
	v_mfma_scale_f32_16x16x128_f8f6f4 v[126:129], v[2:9], v[216:223], v[126:129], v193, v193 op_sel_hi:[0,0,0]
	v_mfma_scale_f32_16x16x128_f8f6f4 v[122:125], v[10:17], v[216:223], v[122:125], v193, v193 op_sel_hi:[0,0,0]
	v_mfma_scale_f32_16x16x128_f8f6f4 v[110:113], v[2:9], v[224:231], v[110:113], v193, v193 op_sel_hi:[0,0,0]
	v_mfma_scale_f32_16x16x128_f8f6f4 v[106:109], v[10:17], v[224:231], v[106:109], v193, v193 op_sel_hi:[0,0,0]
	v_mfma_scale_f32_16x16x128_f8f6f4 v[150:153], v[18:25], v[200:207], v[150:153], v193, v193 op_sel_hi:[0,0,0]
	v_mfma_scale_f32_16x16x128_f8f6f4 v[146:149], v[26:33], v[200:207], v[146:149], v193, v193 op_sel_hi:[0,0,0]
	v_mfma_scale_f32_16x16x128_f8f6f4 v[134:137], v[18:25], v[208:215], v[134:137], v193, v193 op_sel_hi:[0,0,0]
	v_mfma_scale_f32_16x16x128_f8f6f4 v[130:133], v[26:33], v[208:215], v[130:133], v193, v193 op_sel_hi:[0,0,0]
	v_mfma_scale_f32_16x16x128_f8f6f4 v[118:121], v[18:25], v[216:223], v[118:121], v193, v193 op_sel_hi:[0,0,0]
	v_mfma_scale_f32_16x16x128_f8f6f4 v[114:117], v[26:33], v[216:223], v[114:117], v193, v193 op_sel_hi:[0,0,0]
	v_mfma_scale_f32_16x16x128_f8f6f4 v[102:105], v[18:25], v[224:231], v[102:105], v193, v193 op_sel_hi:[0,0,0]
	v_mfma_scale_f32_16x16x128_f8f6f4 v[98:101], v[26:33], v[224:231], v[98:101], v193, v193 op_sel_hi:[0,0,0]
	s_barrier
	s_mov_b32 m0, s47
	v_lshl_add_u64 v[174:175], v[174:175], 0, s[20:21]
	s_add_u32 s26, s26, 0x40080
	ds_read_b128 v[200:203], v192 offset:49152
	ds_read_b128 v[204:207], v192 offset:50176
	ds_read_b128 v[208:211], v192 offset:51200
	ds_read_b128 v[212:215], v192 offset:52224
	ds_read_b128 v[216:219], v192 offset:53248
	ds_read_b128 v[220:223], v192 offset:54272
	ds_read_b128 v[224:227], v192 offset:55296
	ds_read_b128 v[228:231], v192 offset:56320
	global_load_lds_dwordx4 v[174:175], off
	v_lshl_add_u64 v[174:175], v[176:177], 0, s[20:21]
	s_mov_b32 m0, s48
	s_addc_u32 s27, s27, 0
	global_load_lds_dwordx4 v[174:175], off
	v_lshl_add_u64 v[174:175], s[26:27], 0, v[164:165]
	s_mov_b32 m0, s49
	s_nop 0
	global_load_lds_dwordx4 v[174:175], off
	v_lshl_add_u64 v[174:175], s[26:27], 0, v[168:169]
	s_mov_b32 m0, s50
	s_nop 0
	global_load_lds_dwordx4 v[174:175], off
	v_lshl_add_u64 v[174:175], v[178:179], 0, s[20:21]
	s_mov_b32 m0, s36
	s_nop 0
	global_load_lds_dwordx4 v[174:175], off
	v_lshl_add_u64 v[174:175], v[180:181], 0, s[20:21]
	s_mov_b32 m0, s37
	s_nop 0
	global_load_lds_dwordx4 v[174:175], off
	s_waitcnt vmcnt(8)
	s_waitcnt lgkmcnt(0)
	s_barrier
	s_waitcnt lgkmcnt(0)
	v_mfma_scale_f32_16x16x128_f8f6f4 v[94:97], v[2:9], v[200:207], v[94:97], v193, v193 op_sel_hi:[0,0,0]
	v_mfma_scale_f32_16x16x128_f8f6f4 v[90:93], v[10:17], v[200:207], v[90:93], v193, v193 op_sel_hi:[0,0,0]
	v_mfma_scale_f32_16x16x128_f8f6f4 v[78:81], v[2:9], v[208:215], v[78:81], v193, v193 op_sel_hi:[0,0,0]
	v_mfma_scale_f32_16x16x128_f8f6f4 v[74:77], v[10:17], v[208:215], v[74:77], v193, v193 op_sel_hi:[0,0,0]
	v_mfma_scale_f32_16x16x128_f8f6f4 v[62:65], v[2:9], v[216:223], v[62:65], v193, v193 op_sel_hi:[0,0,0]
	v_mfma_scale_f32_16x16x128_f8f6f4 v[58:61], v[10:17], v[216:223], v[58:61], v193, v193 op_sel_hi:[0,0,0]
	v_mfma_scale_f32_16x16x128_f8f6f4 v[46:49], v[2:9], v[224:231], v[46:49], v193, v193 op_sel_hi:[0,0,0]
	v_mfma_scale_f32_16x16x128_f8f6f4 v[42:45], v[10:17], v[224:231], v[42:45], v193, v193 op_sel_hi:[0,0,0]
	v_mfma_scale_f32_16x16x128_f8f6f4 v[86:89], v[18:25], v[200:207], v[86:89], v193, v193 op_sel_hi:[0,0,0]
	v_mfma_scale_f32_16x16x128_f8f6f4 v[82:85], v[26:33], v[200:207], v[82:85], v193, v193 op_sel_hi:[0,0,0]
	v_mfma_scale_f32_16x16x128_f8f6f4 v[70:73], v[18:25], v[208:215], v[70:73], v193, v193 op_sel_hi:[0,0,0]
	v_mfma_scale_f32_16x16x128_f8f6f4 v[66:69], v[26:33], v[208:215], v[66:69], v193, v193 op_sel_hi:[0,0,0]
	v_mfma_scale_f32_16x16x128_f8f6f4 v[54:57], v[18:25], v[216:223], v[54:57], v193, v193 op_sel_hi:[0,0,0]
	v_mfma_scale_f32_16x16x128_f8f6f4 v[50:53], v[26:33], v[216:223], v[50:53], v193, v193 op_sel_hi:[0,0,0]
	v_mfma_scale_f32_16x16x128_f8f6f4 v[38:41], v[18:25], v[224:231], v[38:41], v193, v193 op_sel_hi:[0,0,0]
	v_mfma_scale_f32_16x16x128_f8f6f4 v[34:37], v[26:33], v[224:231], v[34:37], v193, v193 op_sel_hi:[0,0,0]
	s_barrier
	s_add_i32 s40, s40, 2
	s_add_u32 s24, s24, 0x100
	s_addc_u32 s25, s25, 0
	s_cmp_gt_u32 s40, 13
	s_cbranch_scc0 .LBB0_1479
	s_nop 15
	s_nop 15
	s_waitcnt vmcnt(0)
	s_cmpk_lt_u32 s30, 0x100
	s_cbranch_scc0 .LBB0_1482
	s_barrier

.LBB0_1530:
	ds_read_b128 v[18:21], v182
	ds_read_b128 v[22:25], v182 offset:1024
	ds_read_b128 v[26:29], v182 offset:2048
	ds_read_b128 v[30:33], v182 offset:3072
	ds_read_b128 v[2:5], v183
	ds_read_b128 v[6:9], v183 offset:1024
	ds_read_b128 v[10:13], v183 offset:2048
	ds_read_b128 v[14:17], v183 offset:3072
	s_add_u32 s26, s22, s24
	s_addc_u32 s27, s23, s25
	s_add_u32 s26, s26, 0x38a00100
	s_addc_u32 s27, s27, 0
	s_add_u32 s51, s38, s24
	s_addc_u32 s52, s39, s25
	s_cmpk_eq_i32 s24, 0x700
	s_cselect_b32 s29, s7, s27
	s_cselect_b32 s28, s6, s26
	s_cselect_b32 s27, s3, s52
	s_cselect_b32 s26, s2, s51
	s_mov_b32 m0, s41
	v_lshl_add_u64 v[216:217], v[170:171], 0, s[24:25]
	ds_read_b128 v[174:177], v184
	ds_read_b128 v[178:181], v184 offset:1024
	ds_read_b128 v[190:193], v184 offset:2048
	ds_read_b128 v[194:197], v184 offset:3072
	ds_read_b128 v[200:203], v184 offset:4096
	ds_read_b128 v[204:207], v184 offset:5120
	ds_read_b128 v[208:211], v184 offset:6144
	ds_read_b128 v[212:215], v184 offset:7168
	global_load_lds_dwordx4 v[216:217], off
	v_lshl_add_u64 v[216:217], v[172:173], 0, s[24:25]
	s_mov_b32 m0, s42
	s_nop 0
	global_load_lds_dwordx4 v[216:217], off
	s_waitcnt vmcnt(8)
	s_waitcnt lgkmcnt(0)
	s_barrier
	s_waitcnt lgkmcnt(0)
	v_mfma_scale_f32_16x16x128_f8f6f4 v[158:161], v[18:25], v[174:181], v[158:161], v185, v185 op_sel_hi:[0,0,0]
	v_mfma_scale_f32_16x16x128_f8f6f4 v[154:157], v[26:33], v[174:181], v[154:157], v185, v185 op_sel_hi:[0,0,0]
	v_mfma_scale_f32_16x16x128_f8f6f4 v[142:145], v[18:25], v[190:197], v[142:145], v185, v185 op_sel_hi:[0,0,0]
	v_mfma_scale_f32_16x16x128_f8f6f4 v[138:141], v[26:33], v[190:197], v[138:141], v185, v185 op_sel_hi:[0,0,0]
	v_mfma_scale_f32_16x16x128_f8f6f4 v[126:129], v[18:25], v[200:207], v[126:129], v185, v185 op_sel_hi:[0,0,0]
	v_mfma_scale_f32_16x16x128_f8f6f4 v[122:125], v[26:33], v[200:207], v[122:125], v185, v185 op_sel_hi:[0,0,0]
	v_mfma_scale_f32_16x16x128_f8f6f4 v[110:113], v[18:25], v[208:215], v[110:113], v185, v185 op_sel_hi:[0,0,0]
	v_mfma_scale_f32_16x16x128_f8f6f4 v[106:109], v[26:33], v[208:215], v[106:109], v185, v185 op_sel_hi:[0,0,0]
	v_mfma_scale_f32_16x16x128_f8f6f4 v[150:153], v[2:9], v[174:181], v[150:153], v185, v185 op_sel_hi:[0,0,0]
	v_mfma_scale_f32_16x16x128_f8f6f4 v[146:149], v[10:17], v[174:181], v[146:149], v185, v185 op_sel_hi:[0,0,0]
	v_mfma_scale_f32_16x16x128_f8f6f4 v[134:137], v[2:9], v[190:197], v[134:137], v185, v185 op_sel_hi:[0,0,0]
	v_mfma_scale_f32_16x16x128_f8f6f4 v[130:133], v[10:17], v[190:197], v[130:133], v185, v185 op_sel_hi:[0,0,0]
	v_mfma_scale_f32_16x16x128_f8f6f4 v[118:121], v[2:9], v[200:207], v[118:121], v185, v185 op_sel_hi:[0,0,0]
	v_mfma_scale_f32_16x16x128_f8f6f4 v[114:117], v[10:17], v[200:207], v[114:117], v185, v185 op_sel_hi:[0,0,0]
	v_mfma_scale_f32_16x16x128_f8f6f4 v[102:105], v[2:9], v[208:215], v[102:105], v185, v185 op_sel_hi:[0,0,0]
	v_mfma_scale_f32_16x16x128_f8f6f4 v[98:101], v[10:17], v[208:215], v[98:101], v185, v185 op_sel_hi:[0,0,0]
	s_barrier
	s_mov_b32 m0, s43
	v_lshl_add_u64 v[174:175], s[26:27], 0, v[164:165]
	s_add_u32 s52, s26, 0x40000
	ds_read_b128 v[190:193], v184 offset:16384
	ds_read_b128 v[194:197], v184 offset:17408
	ds_read_b128 v[200:203], v184 offset:18432
	ds_read_b128 v[204:207], v184 offset:19456
	ds_read_b128 v[208:211], v184 offset:20480
	ds_read_b128 v[212:215], v184 offset:21504
	ds_read_b128 v[216:219], v184 offset:22528
	ds_read_b128 v[220:223], v184 offset:23552
	global_load_lds_dwordx4 v[174:175], off
	v_lshl_add_u64 v[176:177], s[26:27], 0, v[168:169]
	s_mov_b32 m0, s44
	s_addc_u32 s53, s27, 0
	global_load_lds_dwordx4 v[176:177], off
	v_lshl_add_u64 v[178:179], s[52:53], 0, v[164:165]
	s_mov_b32 m0, s45
	v_lshl_add_u64 v[180:181], s[28:29], 0, v[166:167]
	global_load_lds_dwordx4 v[178:179], off
	v_lshl_add_u64 v[178:179], s[52:53], 0, v[168:169]
	s_mov_b32 m0, s46
	s_nop 0
	global_load_lds_dwordx4 v[178:179], off
	v_lshl_add_u64 v[178:179], s[28:29], 0, v[162:163]
	s_mov_b32 m0, s1
	s_nop 0
	global_load_lds_dwordx4 v[178:179], off
	s_mov_b32 m0, s31
	s_nop 0
	global_load_lds_dwordx4 v[180:181], off
	s_waitcnt vmcnt(8)
	s_waitcnt lgkmcnt(0)
	s_barrier
	s_waitcnt lgkmcnt(0)
	v_mfma_scale_f32_16x16x128_f8f6f4 v[94:97], v[18:25], v[190:197], v[94:97], v185, v185 op_sel_hi:[0,0,0]
	v_mfma_scale_f32_16x16x128_f8f6f4 v[90:93], v[26:33], v[190:197], v[90:93], v185, v185 op_sel_hi:[0,0,0]
	v_mfma_scale_f32_16x16x128_f8f6f4 v[78:81], v[18:25], v[200:207], v[78:81], v185, v185 op_sel_hi:[0,0,0]
	v_mfma_scale_f32_16x16x128_f8f6f4 v[74:77], v[26:33], v[200:207], v[74:77], v185, v185 op_sel_hi:[0,0,0]
	v_mfma_scale_f32_16x16x128_f8f6f4 v[62:65], v[18:25], v[208:215], v[62:65], v185, v185 op_sel_hi:[0,0,0]
	v_mfma_scale_f32_16x16x128_f8f6f4 v[58:61], v[26:33], v[208:215], v[58:61], v185, v185 op_sel_hi:[0,0,0]
	v_mfma_scale_f32_16x16x128_f8f6f4 v[46:49], v[18:25], v[216:223], v[46:49], v185, v185 op_sel_hi:[0,0,0]
	v_mfma_scale_f32_16x16x128_f8f6f4 v[42:45], v[26:33], v[216:223], v[42:45], v185, v185 op_sel_hi:[0,0,0]
	v_mfma_scale_f32_16x16x128_f8f6f4 v[86:89], v[2:9], v[190:197], v[86:89], v185, v185 op_sel_hi:[0,0,0]
	v_mfma_scale_f32_16x16x128_f8f6f4 v[82:85], v[10:17], v[190:197], v[82:85], v185, v185 op_sel_hi:[0,0,0]
	v_mfma_scale_f32_16x16x128_f8f6f4 v[70:73], v[2:9], v[200:207], v[70:73], v185, v185 op_sel_hi:[0,0,0]
	v_mfma_scale_f32_16x16x128_f8f6f4 v[66:69], v[10:17], v[200:207], v[66:69], v185, v185 op_sel_hi:[0,0,0]
	v_mfma_scale_f32_16x16x128_f8f6f4 v[54:57], v[2:9], v[208:215], v[54:57], v185, v185 op_sel_hi:[0,0,0]
	v_mfma_scale_f32_16x16x128_f8f6f4 v[50:53], v[10:17], v[208:215], v[50:53], v185, v185 op_sel_hi:[0,0,0]
	v_mfma_scale_f32_16x16x128_f8f6f4 v[38:41], v[2:9], v[216:223], v[38:41], v185, v185 op_sel_hi:[0,0,0]
	v_mfma_scale_f32_16x16x128_f8f6f4 v[34:37], v[10:17], v[216:223], v[34:37], v185, v185 op_sel_hi:[0,0,0]
	s_barrier
	ds_read_b128 v[2:5], v186
	ds_read_b128 v[6:9], v186 offset:1024
	ds_read_b128 v[10:13], v186 offset:2048
	ds_read_b128 v[14:17], v186 offset:3072
	ds_read_b128 v[18:21], v187
	ds_read_b128 v[22:25], v187 offset:1024
	ds_read_b128 v[26:29], v187 offset:2048
	ds_read_b128 v[30:33], v187 offset:3072
	s_add_u32 s28, s28, 0x40000
	s_addc_u32 s29, s29, 0
	s_mov_b32 m0, s34
	v_lshl_add_u64 v[224:225], s[28:29], 0, v[162:163]
	ds_read_b128 v[190:193], v184 offset:32768
	ds_read_b128 v[194:197], v184 offset:33792
	ds_read_b128 v[200:203], v184 offset:34816
	ds_read_b128 v[204:207], v184 offset:35840
	ds_read_b128 v[208:211], v184 offset:36864
	ds_read_b128 v[212:215], v184 offset:37888
	ds_read_b128 v[216:219], v184 offset:38912
	ds_read_b128 v[220:223], v184 offset:39936
	global_load_lds_dwordx4 v[224:225], off
	v_lshl_add_u64 v[224:225], s[28:29], 0, v[166:167]
	s_mov_b32 m0, s35
	s_nop 0
	global_load_lds_dwordx4 v[224:225], off
	s_waitcnt vmcnt(8)
	s_waitcnt lgkmcnt(0)
	s_barrier
	s_waitcnt lgkmcnt(0)
	v_mfma_scale_f32_16x16x128_f8f6f4 v[158:161], v[2:9], v[190:197], v[158:161], v185, v185 op_sel_hi:[0,0,0]
	v_mfma_scale_f32_16x16x128_f8f6f4 v[154:157], v[10:17], v[190:197], v[154:157], v185, v185 op_sel_hi:[0,0,0]
	v_mfma_scale_f32_16x16x128_f8f6f4 v[142:145], v[2:9], v[200:207], v[142:145], v185, v185 op_sel_hi:[0,0,0]
	v_mfma_scale_f32_16x16x128_f8f6f4 v[138:141], v[10:17], v[200:207], v[138:141], v185, v185 op_sel_hi:[0,0,0]
	v_mfma_scale_f32_16x16x128_f8f6f4 v[126:129], v[2:9], v[208:215], v[126:129], v185, v185 op_sel_hi:[0,0,0]
	v_mfma_scale_f32_16x16x128_f8f6f4 v[122:125], v[10:17], v[208:215], v[122:125], v185, v185 op_sel_hi:[0,0,0]
	v_mfma_scale_f32_16x16x128_f8f6f4 v[110:113], v[2:9], v[216:223], v[110:113], v185, v185 op_sel_hi:[0,0,0]
	v_mfma_scale_f32_16x16x128_f8f6f4 v[106:109], v[10:17], v[216:223], v[106:109], v185, v185 op_sel_hi:[0,0,0]
	v_mfma_scale_f32_16x16x128_f8f6f4 v[150:153], v[18:25], v[190:197], v[150:153], v185, v185 op_sel_hi:[0,0,0]
	v_mfma_scale_f32_16x16x128_f8f6f4 v[146:149], v[26:33], v[190:197], v[146:149], v185, v185 op_sel_hi:[0,0,0]
	v_mfma_scale_f32_16x16x128_f8f6f4 v[134:137], v[18:25], v[200:207], v[134:137], v185, v185 op_sel_hi:[0,0,0]
	v_mfma_scale_f32_16x16x128_f8f6f4 v[130:133], v[26:33], v[200:207], v[130:133], v185, v185 op_sel_hi:[0,0,0]
	v_mfma_scale_f32_16x16x128_f8f6f4 v[118:121], v[18:25], v[208:215], v[118:121], v185, v185 op_sel_hi:[0,0,0]
	v_mfma_scale_f32_16x16x128_f8f6f4 v[114:117], v[26:33], v[208:215], v[114:117], v185, v185 op_sel_hi:[0,0,0]
	v_mfma_scale_f32_16x16x128_f8f6f4 v[102:105], v[18:25], v[216:223], v[102:105], v185, v185 op_sel_hi:[0,0,0]
	v_mfma_scale_f32_16x16x128_f8f6f4 v[98:101], v[26:33], v[216:223], v[98:101], v185, v185 op_sel_hi:[0,0,0]
	s_barrier
	s_mov_b32 m0, s47
	v_lshl_add_u64 v[174:175], v[174:175], 0, s[20:21]
	s_add_u32 s26, s26, 0x40080
	ds_read_b128 v[190:193], v184 offset:49152
	ds_read_b128 v[194:197], v184 offset:50176
	ds_read_b128 v[200:203], v184 offset:51200
	ds_read_b128 v[204:207], v184 offset:52224
	ds_read_b128 v[208:211], v184 offset:53248
	ds_read_b128 v[212:215], v184 offset:54272
	ds_read_b128 v[216:219], v184 offset:55296
	ds_read_b128 v[220:223], v184 offset:56320
	global_load_lds_dwordx4 v[174:175], off
	v_lshl_add_u64 v[174:175], v[176:177], 0, s[20:21]
	s_mov_b32 m0, s48
	s_addc_u32 s27, s27, 0
	global_load_lds_dwordx4 v[174:175], off
	v_lshl_add_u64 v[174:175], s[26:27], 0, v[164:165]
	s_mov_b32 m0, s49
	s_nop 0
	global_load_lds_dwordx4 v[174:175], off
	v_lshl_add_u64 v[174:175], s[26:27], 0, v[168:169]
	s_mov_b32 m0, s50
	s_nop 0
	global_load_lds_dwordx4 v[174:175], off
	v_lshl_add_u64 v[174:175], v[178:179], 0, s[20:21]
	s_mov_b32 m0, s36
	s_nop 0
	global_load_lds_dwordx4 v[174:175], off
	v_lshl_add_u64 v[174:175], v[180:181], 0, s[20:21]
	s_mov_b32 m0, s37
	s_nop 0
	global_load_lds_dwordx4 v[174:175], off
	s_waitcnt vmcnt(8)
	s_waitcnt lgkmcnt(0)
	s_barrier
	s_waitcnt lgkmcnt(0)
	v_mfma_scale_f32_16x16x128_f8f6f4 v[94:97], v[2:9], v[190:197], v[94:97], v185, v185 op_sel_hi:[0,0,0]
	v_mfma_scale_f32_16x16x128_f8f6f4 v[90:93], v[10:17], v[190:197], v[90:93], v185, v185 op_sel_hi:[0,0,0]
	v_mfma_scale_f32_16x16x128_f8f6f4 v[78:81], v[2:9], v[200:207], v[78:81], v185, v185 op_sel_hi:[0,0,0]
	v_mfma_scale_f32_16x16x128_f8f6f4 v[74:77], v[10:17], v[200:207], v[74:77], v185, v185 op_sel_hi:[0,0,0]
	v_mfma_scale_f32_16x16x128_f8f6f4 v[62:65], v[2:9], v[208:215], v[62:65], v185, v185 op_sel_hi:[0,0,0]
	v_mfma_scale_f32_16x16x128_f8f6f4 v[58:61], v[10:17], v[208:215], v[58:61], v185, v185 op_sel_hi:[0,0,0]
	v_mfma_scale_f32_16x16x128_f8f6f4 v[46:49], v[2:9], v[216:223], v[46:49], v185, v185 op_sel_hi:[0,0,0]
	v_mfma_scale_f32_16x16x128_f8f6f4 v[42:45], v[10:17], v[216:223], v[42:45], v185, v185 op_sel_hi:[0,0,0]
	v_mfma_scale_f32_16x16x128_f8f6f4 v[86:89], v[18:25], v[190:197], v[86:89], v185, v185 op_sel_hi:[0,0,0]
	v_mfma_scale_f32_16x16x128_f8f6f4 v[82:85], v[26:33], v[190:197], v[82:85], v185, v185 op_sel_hi:[0,0,0]
	v_mfma_scale_f32_16x16x128_f8f6f4 v[70:73], v[18:25], v[200:207], v[70:73], v185, v185 op_sel_hi:[0,0,0]
	v_mfma_scale_f32_16x16x128_f8f6f4 v[66:69], v[26:33], v[200:207], v[66:69], v185, v185 op_sel_hi:[0,0,0]
	v_mfma_scale_f32_16x16x128_f8f6f4 v[54:57], v[18:25], v[208:215], v[54:57], v185, v185 op_sel_hi:[0,0,0]
	v_mfma_scale_f32_16x16x128_f8f6f4 v[50:53], v[26:33], v[208:215], v[50:53], v185, v185 op_sel_hi:[0,0,0]
	v_mfma_scale_f32_16x16x128_f8f6f4 v[38:41], v[18:25], v[216:223], v[38:41], v185, v185 op_sel_hi:[0,0,0]
	v_mfma_scale_f32_16x16x128_f8f6f4 v[34:37], v[26:33], v[216:223], v[34:37], v185, v185 op_sel_hi:[0,0,0]
	s_barrier
	s_add_i32 s40, s40, 2
	s_add_u32 s24, s24, 0x100
	s_addc_u32 s25, s25, 0
	s_cmp_gt_u32 s40, 13
	s_cbranch_scc0 .LBB0_1530
	s_nop 15
	s_nop 15
	s_waitcnt vmcnt(0)
	s_cmpk_lt_u32 s30, 0x100
	s_cbranch_scc0 .LBB0_1533
	s_barrier

.LBB0_1590:
	s_waitcnt lgkmcnt(0)
	s_barrier
	s_waitcnt lgkmcnt(0)
	v_mfma_scale_f32_16x16x128_f8f6f4 v[124:127], v[24:31], v[56:63], v[124:127], v227, v227 op_sel_hi:[0,0,0]
	v_mfma_scale_f32_16x16x128_f8f6f4 v[120:123], v[16:23], v[56:63], v[120:123], v227, v227 op_sel_hi:[0,0,0]
	v_mfma_scale_f32_16x16x128_f8f6f4 v[108:111], v[24:31], v[48:55], v[108:111], v227, v227 op_sel_hi:[0,0,0]
	v_mfma_scale_f32_16x16x128_f8f6f4 v[104:107], v[16:23], v[48:55], v[104:107], v227, v227 op_sel_hi:[0,0,0]
	v_mfma_scale_f32_16x16x128_f8f6f4 v[92:95], v[24:31], v[40:47], v[92:95], v227, v227 op_sel_hi:[0,0,0]
	v_mfma_scale_f32_16x16x128_f8f6f4 v[88:91], v[16:23], v[40:47], v[88:91], v227, v227 op_sel_hi:[0,0,0]
	v_mfma_scale_f32_16x16x128_f8f6f4 v[76:79], v[24:31], v[32:39], v[76:79], v227, v227 op_sel_hi:[0,0,0]
	v_mfma_scale_f32_16x16x128_f8f6f4 v[72:75], v[16:23], v[32:39], v[72:75], v227, v227 op_sel_hi:[0,0,0]
	v_mfma_scale_f32_16x16x128_f8f6f4 v[116:119], v[8:15], v[56:63], v[116:119], v227, v227 op_sel_hi:[0,0,0]
	v_mfma_scale_f32_16x16x128_f8f6f4 v[112:115], v[0:7], v[56:63], v[112:115], v227, v227 op_sel_hi:[0,0,0]
	v_mfma_scale_f32_16x16x128_f8f6f4 v[100:103], v[8:15], v[48:55], v[100:103], v227, v227 op_sel_hi:[0,0,0]
	v_mfma_scale_f32_16x16x128_f8f6f4 v[96:99], v[0:7], v[48:55], v[96:99], v227, v227 op_sel_hi:[0,0,0]
	v_mfma_scale_f32_16x16x128_f8f6f4 v[84:87], v[8:15], v[40:47], v[84:87], v227, v227 op_sel_hi:[0,0,0]
	v_mfma_scale_f32_16x16x128_f8f6f4 v[80:83], v[0:7], v[40:47], v[80:83], v227, v227 op_sel_hi:[0,0,0]
	v_mfma_scale_f32_16x16x128_f8f6f4 v[68:71], v[8:15], v[32:39], v[68:71], v227, v227 op_sel_hi:[0,0,0]
	v_mfma_scale_f32_16x16x128_f8f6f4 v[64:67], v[0:7], v[32:39], v[64:67], v227, v227 op_sel_hi:[0,0,0]
	s_barrier
	s_add_i32 s52, 0, 0x18000
	s_add_i32 s53, 0, 0x1c000
	v_add_u32_e32 v12, s52, v222
	v_add_u32_e32 v28, s53, v222
	ds_read_b128 v[0:3], v12
	ds_read_b128 v[4:7], v12 offset:1024
	ds_read_b128 v[8:11], v12 offset:2048
	ds_read_b128 v[12:15], v12 offset:3072
	ds_read_b128 v[16:19], v28
	ds_read_b128 v[20:23], v28 offset:1024
	ds_read_b128 v[24:27], v28 offset:2048
	ds_read_b128 v[28:31], v28 offset:3072
	s_add_u32 s50, s50, 0x40000
	s_addc_u32 s51, s51, 0
	s_mov_b32 m0, s63
	v_lshl_add_u64 v[228:229], s[50:51], 0, v[192:193]
	ds_read_b128 v[32:35], v226 offset:32768
	ds_read_b128 v[36:39], v226 offset:33792
	ds_read_b128 v[40:43], v226 offset:34816
	ds_read_b128 v[44:47], v226 offset:35840
	ds_read_b128 v[48:51], v226 offset:36864
	ds_read_b128 v[52:55], v226 offset:37888
	ds_read_b128 v[56:59], v226 offset:38912
	ds_read_b128 v[60:63], v226 offset:39936
	global_load_lds_dwordx4 v[228:229], off
	v_lshl_add_u64 v[228:229], s[50:51], 0, v[196:197]
	s_mov_b32 m0, s64
	s_nop 0
	global_load_lds_dwordx4 v[228:229], off
	s_waitcnt vmcnt(8)
	s_waitcnt lgkmcnt(0)
	s_barrier
	s_waitcnt lgkmcnt(0)
	v_mfma_scale_f32_16x16x128_f8f6f4 v[188:191], v[0:7], v[32:39], v[188:191], v227, v227 op_sel_hi:[0,0,0]
	v_mfma_scale_f32_16x16x128_f8f6f4 v[184:187], v[8:15], v[32:39], v[184:187], v227, v227 op_sel_hi:[0,0,0]
	v_mfma_scale_f32_16x16x128_f8f6f4 v[172:175], v[0:7], v[40:47], v[172:175], v227, v227 op_sel_hi:[0,0,0]
	v_mfma_scale_f32_16x16x128_f8f6f4 v[168:171], v[8:15], v[40:47], v[168:171], v227, v227 op_sel_hi:[0,0,0]
	v_mfma_scale_f32_16x16x128_f8f6f4 v[156:159], v[0:7], v[48:55], v[156:159], v227, v227 op_sel_hi:[0,0,0]
	v_mfma_scale_f32_16x16x128_f8f6f4 v[152:155], v[8:15], v[48:55], v[152:155], v227, v227 op_sel_hi:[0,0,0]
	v_mfma_scale_f32_16x16x128_f8f6f4 v[140:143], v[0:7], v[56:63], v[140:143], v227, v227 op_sel_hi:[0,0,0]
	v_mfma_scale_f32_16x16x128_f8f6f4 v[136:139], v[8:15], v[56:63], v[136:139], v227, v227 op_sel_hi:[0,0,0]
	v_mfma_scale_f32_16x16x128_f8f6f4 v[180:183], v[16:23], v[32:39], v[180:183], v227, v227 op_sel_hi:[0,0,0]
	v_mfma_scale_f32_16x16x128_f8f6f4 v[176:179], v[24:31], v[32:39], v[176:179], v227, v227 op_sel_hi:[0,0,0]
	v_mfma_scale_f32_16x16x128_f8f6f4 v[164:167], v[16:23], v[40:47], v[164:167], v227, v227 op_sel_hi:[0,0,0]
	v_mfma_scale_f32_16x16x128_f8f6f4 v[160:163], v[24:31], v[40:47], v[160:163], v227, v227 op_sel_hi:[0,0,0]
	v_mfma_scale_f32_16x16x128_f8f6f4 v[148:151], v[16:23], v[48:55], v[148:151], v227, v227 op_sel_hi:[0,0,0]
	v_mfma_scale_f32_16x16x128_f8f6f4 v[144:147], v[24:31], v[48:55], v[144:147], v227, v227 op_sel_hi:[0,0,0]
	v_mfma_scale_f32_16x16x128_f8f6f4 v[132:135], v[16:23], v[56:63], v[132:135], v227, v227 op_sel_hi:[0,0,0]
	v_mfma_scale_f32_16x16x128_f8f6f4 v[128:131], v[24:31], v[56:63], v[128:131], v227, v227 op_sel_hi:[0,0,0]
	s_barrier
	s_add_i32 s50, s52, s23
	v_lshl_add_u64 v[220:221], v[220:221], 0, s[16:17]
	s_mov_b32 m0, s50
	ds_read_b128 v[32:35], v226 offset:49152
	ds_read_b128 v[36:39], v226 offset:50176
	ds_read_b128 v[40:43], v226 offset:51200
	ds_read_b128 v[44:47], v226 offset:52224
	ds_read_b128 v[48:51], v226 offset:53248
	ds_read_b128 v[52:55], v226 offset:54272
	ds_read_b128 v[56:59], v226 offset:55296
	ds_read_b128 v[60:63], v226 offset:56320
	global_load_lds_dwordx4 v[220:221], off
	s_add_i32 m0, s50, 0x2000
	s_add_u32 s48, s48, 0x40080
	v_lshl_add_u64 v[218:219], v[218:219], 0, s[16:17]
	s_addc_u32 s49, s49, 0
	s_add_i32 s50, s53, s23
	global_load_lds_dwordx4 v[218:219], off
	v_lshl_add_u64 v[218:219], s[48:49], 0, v[194:195]
	s_mov_b32 m0, s50
	v_lshl_add_u64 v[214:215], v[214:215], 0, s[16:17]
	global_load_lds_dwordx4 v[218:219], off
	v_lshl_add_u64 v[218:219], s[48:49], 0, v[200:201]
	s_add_i32 m0, s50, 0x2000
	s_nop 0
	global_load_lds_dwordx4 v[218:219], off
	s_mov_b32 m0, s65
	s_nop 0
	global_load_lds_dwordx4 v[214:215], off
	v_lshl_add_u64 v[214:215], v[216:217], 0, s[16:17]
	s_mov_b32 m0, s66
	s_nop 0
	global_load_lds_dwordx4 v[214:215], off
	s_waitcnt vmcnt(8)
	s_waitcnt lgkmcnt(0)
	s_barrier
	s_waitcnt lgkmcnt(0)
	v_mfma_scale_f32_16x16x128_f8f6f4 v[124:127], v[0:7], v[32:39], v[124:127], v227, v227 op_sel_hi:[0,0,0]
	v_mfma_scale_f32_16x16x128_f8f6f4 v[120:123], v[8:15], v[32:39], v[120:123], v227, v227 op_sel_hi:[0,0,0]
	v_mfma_scale_f32_16x16x128_f8f6f4 v[108:111], v[0:7], v[40:47], v[108:111], v227, v227 op_sel_hi:[0,0,0]
	v_mfma_scale_f32_16x16x128_f8f6f4 v[104:107], v[8:15], v[40:47], v[104:107], v227, v227 op_sel_hi:[0,0,0]
	v_mfma_scale_f32_16x16x128_f8f6f4 v[92:95], v[0:7], v[48:55], v[92:95], v227, v227 op_sel_hi:[0,0,0]
	v_mfma_scale_f32_16x16x128_f8f6f4 v[88:91], v[8:15], v[48:55], v[88:91], v227, v227 op_sel_hi:[0,0,0]
	v_mfma_scale_f32_16x16x128_f8f6f4 v[76:79], v[0:7], v[56:63], v[76:79], v227, v227 op_sel_hi:[0,0,0]
	v_mfma_scale_f32_16x16x128_f8f6f4 v[72:75], v[8:15], v[56:63], v[72:75], v227, v227 op_sel_hi:[0,0,0]
	v_mfma_scale_f32_16x16x128_f8f6f4 v[116:119], v[16:23], v[32:39], v[116:119], v227, v227 op_sel_hi:[0,0,0]
	v_mfma_scale_f32_16x16x128_f8f6f4 v[112:115], v[24:31], v[32:39], v[112:115], v227, v227 op_sel_hi:[0,0,0]
	v_mfma_scale_f32_16x16x128_f8f6f4 v[100:103], v[16:23], v[40:47], v[100:103], v227, v227 op_sel_hi:[0,0,0]
	v_mfma_scale_f32_16x16x128_f8f6f4 v[96:99], v[24:31], v[40:47], v[96:99], v227, v227 op_sel_hi:[0,0,0]
	v_mfma_scale_f32_16x16x128_f8f6f4 v[84:87], v[16:23], v[48:55], v[84:87], v227, v227 op_sel_hi:[0,0,0]
	v_mfma_scale_f32_16x16x128_f8f6f4 v[80:83], v[24:31], v[48:55], v[80:83], v227, v227 op_sel_hi:[0,0,0]
	v_mfma_scale_f32_16x16x128_f8f6f4 v[68:71], v[16:23], v[56:63], v[68:71], v227, v227 op_sel_hi:[0,0,0]
	v_mfma_scale_f32_16x16x128_f8f6f4 v[64:67], v[24:31], v[56:63], v[64:67], v227, v227 op_sel_hi:[0,0,0]
	s_barrier
	s_add_i32 s73, s73, 2
	s_add_u32 s44, s44, 0x100
	s_addc_u32 s45, s45, 0
	s_cmp_gt_u32 s73, 13
	s_cbranch_scc1 .LBB0_1599

.LBB0_1595:
	s_add_u32 s48, s42, s44
	s_addc_u32 s49, s43, s45
	s_add_u32 s48, s48, 0x100
	s_addc_u32 s49, s49, 0
	s_add_u32 s54, s71, s44
	s_addc_u32 s55, s72, s45
	s_waitcnt lgkmcnt(0)
	s_cmpk_eq_i32 s44, 0x700
	s_cselect_b32 s51, s37, s49
	s_cselect_b32 s50, s69, s48
	s_cselect_b32 s49, s35, s55
	s_cselect_b32 s48, s70, s54
	s_barrier
	s_waitcnt lgkmcnt(0)
	v_mfma_scale_f32_16x16x128_f8f6f4 v[188:191], v[24:31], v[56:63], v[188:191], v227, v227 op_sel_hi:[0,0,0]
	v_mfma_scale_f32_16x16x128_f8f6f4 v[184:187], v[16:23], v[56:63], v[184:187], v227, v227 op_sel_hi:[0,0,0]
	v_mfma_scale_f32_16x16x128_f8f6f4 v[172:175], v[24:31], v[48:55], v[172:175], v227, v227 op_sel_hi:[0,0,0]
	v_mfma_scale_f32_16x16x128_f8f6f4 v[168:171], v[16:23], v[48:55], v[168:171], v227, v227 op_sel_hi:[0,0,0]
	v_mfma_scale_f32_16x16x128_f8f6f4 v[156:159], v[24:31], v[40:47], v[156:159], v227, v227 op_sel_hi:[0,0,0]
	v_mfma_scale_f32_16x16x128_f8f6f4 v[152:155], v[16:23], v[40:47], v[152:155], v227, v227 op_sel_hi:[0,0,0]
	v_mfma_scale_f32_16x16x128_f8f6f4 v[140:143], v[24:31], v[32:39], v[140:143], v227, v227 op_sel_hi:[0,0,0]
	v_mfma_scale_f32_16x16x128_f8f6f4 v[136:139], v[16:23], v[32:39], v[136:139], v227, v227 op_sel_hi:[0,0,0]
	v_mfma_scale_f32_16x16x128_f8f6f4 v[180:183], v[8:15], v[56:63], v[180:183], v227, v227 op_sel_hi:[0,0,0]
	v_mfma_scale_f32_16x16x128_f8f6f4 v[176:179], v[0:7], v[56:63], v[176:179], v227, v227 op_sel_hi:[0,0,0]
	v_mfma_scale_f32_16x16x128_f8f6f4 v[164:167], v[8:15], v[48:55], v[164:167], v227, v227 op_sel_hi:[0,0,0]
	v_mfma_scale_f32_16x16x128_f8f6f4 v[160:163], v[0:7], v[48:55], v[160:163], v227, v227 op_sel_hi:[0,0,0]
	v_mfma_scale_f32_16x16x128_f8f6f4 v[148:151], v[8:15], v[40:47], v[148:151], v227, v227 op_sel_hi:[0,0,0]
	v_mfma_scale_f32_16x16x128_f8f6f4 v[144:147], v[0:7], v[40:47], v[144:147], v227, v227 op_sel_hi:[0,0,0]
	v_mfma_scale_f32_16x16x128_f8f6f4 v[132:135], v[8:15], v[32:39], v[132:135], v227, v227 op_sel_hi:[0,0,0]
	v_mfma_scale_f32_16x16x128_f8f6f4 v[128:131], v[0:7], v[32:39], v[128:131], v227, v227 op_sel_hi:[0,0,0]
	s_barrier
	s_mov_b32 m0, s58
	v_lshl_add_u64 v[220:221], s[48:49], 0, v[194:195]
	s_add_u32 s54, s48, 0x40000
	ds_read_b128 v[56:59], v226 offset:16384
	ds_read_b128 v[60:63], v226 offset:17408
	ds_read_b128 v[48:51], v226 offset:18432
	ds_read_b128 v[52:55], v226 offset:19456
	ds_read_b128 v[40:43], v226 offset:20480
	ds_read_b128 v[44:47], v226 offset:21504
	ds_read_b128 v[32:35], v226 offset:22528
	ds_read_b128 v[36:39], v226 offset:23552
	global_load_lds_dwordx4 v[220:221], off
	v_lshl_add_u64 v[218:219], s[48:49], 0, v[200:201]
	s_mov_b32 m0, s59
	s_addc_u32 s55, s49, 0
	global_load_lds_dwordx4 v[218:219], off
	v_lshl_add_u64 v[214:215], s[54:55], 0, v[194:195]
	s_mov_b32 m0, s60
	v_lshl_add_u64 v[216:217], s[50:51], 0, v[196:197]
	global_load_lds_dwordx4 v[214:215], off
	v_lshl_add_u64 v[214:215], s[54:55], 0, v[200:201]
	s_mov_b32 m0, s61
	s_mov_b64 s[54:55], -1
	global_load_lds_dwordx4 v[214:215], off
	v_lshl_add_u64 v[214:215], s[50:51], 0, v[192:193]
	s_mov_b32 m0, s57
	s_and_b64 vcc, exec, s[52:53]
	global_load_lds_dwordx4 v[214:215], off
	s_mov_b32 m0, s62
	s_nop 0
	global_load_lds_dwordx4 v[216:217], off
	s_cbranch_vccz .LBB0_1597
	s_waitcnt vmcnt(8)
	s_mov_b64 s[54:55], 0
